# v10 + B-load issue moved ~one MFMA group later + MoE padding skip with rotated deal
# speedup vs baseline: 1.0302x; 1.0067x over previous
.LBB0_71:
	s_mov_b32 m0, s68
	s_add_i32 s25, s24, 0xffffff80
	ds_read_b64_tr_b16 v[170:171], v166
	ds_read_b64_tr_b16 v[172:173], v167
	ds_read_b64_tr_b16 v[176:177], v167 offset:32
	ds_read_b128 v[178:181], v162
	ds_read_b64_tr_b16 v[174:175], v166 offset:32
	ds_read_b64_tr_b16 v[182:183], v166 offset:64
	ds_read_b64_tr_b16 v[186:187], v166 offset:96
	ds_read_b64_tr_b16 v[184:185], v167 offset:64
	ds_read_b64_tr_b16 v[188:189], v167 offset:96
	ds_read_b128 v[190:193], v162 offset:2048
	ds_read_b128 v[194:197], v162 offset:4096
	buffer_load_dwordx4 v163, s[20:23], s25 offen lds
	s_mov_b32 m0, s67
	v_mfma_f32_16x16x32_bf16 v[44:47], v[244:247], v[252:255], v[44:47]
	v_mfma_f32_16x16x32_bf16 v[40:43], v[248:251], v[252:255], v[40:43]
	v_mfma_f32_16x16x32_bf16 v[36:39], v[198:201], v[252:255], v[36:39]
	v_mfma_f32_16x16x32_bf16 v[32:35], v[202:205], v[252:255], v[32:35]
	s_waitcnt lgkmcnt(7)
	v_mfma_f32_16x16x32_bf16 v[156:159], v[170:173], v[178:181], v[156:159]
	buffer_load_dwordx4 v165, s[20:23], s25 offen lds
	s_mov_b32 m0, s66
	s_nop 0
	buffer_load_dwordx4 v164, s[20:23], s25 offen lds
	s_mov_b32 m0, s65
	s_waitcnt lgkmcnt(6)
	v_mfma_f32_16x16x32_bf16 v[152:155], v[174:177], v[178:181], v[152:155]
	buffer_load_dwordx4 v168, s[20:23], s25 offen lds
	s_add_i32 s25, s9, 0xffd60000
	s_waitcnt lgkmcnt(3)
	v_mfma_f32_16x16x32_bf16 v[148:151], v[182:185], v[178:181], v[148:151]
	s_waitcnt lgkmcnt(2)
	v_mfma_f32_16x16x32_bf16 v[144:147], v[186:189], v[178:181], v[144:147]
	s_waitcnt lgkmcnt(1)
	v_mfma_f32_16x16x32_bf16 v[140:143], v[170:173], v[190:193], v[140:143]
	ds_read_b128 v[178:181], v162 offset:6144
	s_waitcnt vmcnt(11)
	v_cvt_pk_bf16_f32 v15, v14, v15
	v_cvt_pk_bf16_f32 v14, v12, v13
	v_mfma_f32_16x16x32_bf16 v[136:139], v[174:177], v[190:193], v[136:139]
	ds_write_b64 v161, v[14:15] offset:34816
	v_mfma_f32_16x16x32_bf16 v[132:135], v[182:185], v[190:193], v[132:135]
	v_mfma_f32_16x16x32_bf16 v[128:131], v[186:189], v[190:193], v[128:131]
	s_waitcnt lgkmcnt(2)
	v_mfma_f32_16x16x32_bf16 v[124:127], v[170:173], v[194:197], v[124:127]
	ds_read_b128 v[190:193], v162 offset:8192
	v_mfma_f32_16x16x32_bf16 v[120:123], v[174:177], v[194:197], v[120:123]
	v_mfma_f32_16x16x32_bf16 v[116:119], v[182:185], v[194:197], v[116:119]
	v_mfma_f32_16x16x32_bf16 v[112:115], v[186:189], v[194:197], v[112:115]
	s_waitcnt lgkmcnt(2)
	v_mfma_f32_16x16x32_bf16 v[108:111], v[170:173], v[178:181], v[108:111]
	ds_read_b128 v[194:197], v162 offset:10240
	buffer_load_dwordx4 v[12:15], v160, s[12:15], s25 offen
	s_waitcnt vmcnt(11)
	v_cvt_pk_bf16_f32 v3, v2, v3
	v_cvt_pk_bf16_f32 v2, v0, v1
	v_mfma_f32_16x16x32_bf16 v[104:107], v[174:177], v[178:181], v[104:107]
	ds_write_b64 v161, v[2:3] offset:43520
	v_mfma_f32_16x16x32_bf16 v[100:103], v[182:185], v[178:181], v[100:103]
	v_mfma_f32_16x16x32_bf16 v[96:99], v[186:189], v[178:181], v[96:99]
	s_add_i32 s26, s9, 0xffdc0000
	s_waitcnt lgkmcnt(2)
	v_mfma_f32_16x16x32_bf16 v[92:95], v[170:173], v[190:193], v[92:95]
	ds_read_b128 v[178:181], v162 offset:12288
	v_mfma_f32_16x16x32_bf16 v[88:91], v[174:177], v[190:193], v[88:91]
	v_mfma_f32_16x16x32_bf16 v[84:87], v[182:185], v[190:193], v[84:87]
	v_mfma_f32_16x16x32_bf16 v[80:83], v[186:189], v[190:193], v[80:83]
	s_waitcnt lgkmcnt(2)
	v_mfma_f32_16x16x32_bf16 v[76:79], v[170:173], v[194:197], v[76:79]
	ds_read_b128 v[190:193], v162 offset:14336
	buffer_load_dwordx4 v[0:3], v160, s[12:15], s26 offen
	s_waitcnt vmcnt(11)
	v_cvt_pk_bf16_f32 v31, v30, v31
	v_cvt_pk_bf16_f32 v30, v28, v29
	v_mfma_f32_16x16x32_bf16 v[72:75], v[174:177], v[194:197], v[72:75]
	ds_write_b64 v161, v[30:31] offset:52224
	v_mfma_f32_16x16x32_bf16 v[68:71], v[182:185], v[194:197], v[68:71]
	v_mfma_f32_16x16x32_bf16 v[64:67], v[186:189], v[194:197], v[64:67]
	s_add_i32 s27, s9, 0xffe20000
	s_waitcnt lgkmcnt(2)
	v_mfma_f32_16x16x32_bf16 v[60:63], v[170:173], v[178:181], v[60:63]
	ds_read_b128 v[194:197], v162 offset:1024
	v_mfma_f32_16x16x32_bf16 v[56:59], v[174:177], v[178:181], v[56:59]
	v_mfma_f32_16x16x32_bf16 v[52:55], v[182:185], v[178:181], v[52:55]
	v_mfma_f32_16x16x32_bf16 v[48:51], v[186:189], v[178:181], v[48:51]
	s_waitcnt lgkmcnt(2)
	v_mfma_f32_16x16x32_bf16 v[44:47], v[170:173], v[190:193], v[44:47]
	ds_read_b128 v[170:173], v162 offset:3072
	buffer_load_dwordx4 v[28:31], v160, s[12:15], s27 offen
	s_waitcnt vmcnt(11)
	v_cvt_pk_bf16_f32 v27, v26, v27
	v_cvt_pk_bf16_f32 v26, v24, v25
	v_mfma_f32_16x16x32_bf16 v[40:43], v[174:177], v[190:193], v[40:43]
	ds_read_b64_tr_b16 v[244:245], v166 offset:17408
	ds_read_b64_tr_b16 v[248:249], v166 offset:17440
	ds_read_b64_tr_b16 v[198:199], v166 offset:17472
	ds_read_b64_tr_b16 v[202:203], v166 offset:17504
	ds_read_b64_tr_b16 v[246:247], v167 offset:17408
	ds_read_b64_tr_b16 v[250:251], v167 offset:17440
	ds_read_b64_tr_b16 v[200:201], v167 offset:17472
	ds_read_b64_tr_b16 v[204:205], v167 offset:17504
	ds_write_b64 v161, v[26:27] offset:60928
	v_mfma_f32_16x16x32_bf16 v[36:39], v[182:185], v[190:193], v[36:39]
	v_mfma_f32_16x16x32_bf16 v[32:35], v[186:189], v[190:193], v[32:35]
	s_add_i32 s42, s9, 0xffe80000
	s_waitcnt lgkmcnt(4)
	v_mfma_f32_16x16x32_bf16 v[156:159], v[244:247], v[194:197], v[156:159]
	ds_read_b128 v[182:185], v162 offset:5120
	s_waitcnt lgkmcnt(4)
	v_mfma_f32_16x16x32_bf16 v[152:155], v[248:251], v[194:197], v[152:155]
	s_waitcnt lgkmcnt(3)
	v_mfma_f32_16x16x32_bf16 v[148:151], v[198:201], v[194:197], v[148:151]
	s_waitcnt lgkmcnt(2)
	v_mfma_f32_16x16x32_bf16 v[144:147], v[202:205], v[194:197], v[144:147]
	v_mfma_f32_16x16x32_bf16 v[140:143], v[244:247], v[170:173], v[140:143]
	ds_read_b128 v[186:189], v162 offset:7168
	buffer_load_dwordx4 v[24:27], v160, s[12:15], s42 offen
	s_waitcnt vmcnt(11)
	v_cvt_pk_bf16_f32 v23, v22, v23
	v_cvt_pk_bf16_f32 v22, v20, v21
	v_mfma_f32_16x16x32_bf16 v[136:139], v[248:251], v[170:173], v[136:139]
	ds_write_b64 v161, v[22:23] offset:35072
	v_mfma_f32_16x16x32_bf16 v[132:135], v[198:201], v[170:173], v[132:135]
	v_mfma_f32_16x16x32_bf16 v[128:131], v[202:205], v[170:173], v[128:131]
	s_waitcnt lgkmcnt(2)
	v_mfma_f32_16x16x32_bf16 v[124:127], v[244:247], v[182:185], v[124:127]
	ds_read_b128 v[170:173], v162 offset:9216
	v_mfma_f32_16x16x32_bf16 v[120:123], v[248:251], v[182:185], v[120:123]
	v_mfma_f32_16x16x32_bf16 v[116:119], v[198:201], v[182:185], v[116:119]
	v_mfma_f32_16x16x32_bf16 v[112:115], v[202:205], v[182:185], v[112:115]
	s_waitcnt lgkmcnt(2)
	v_mfma_f32_16x16x32_bf16 v[108:111], v[244:247], v[186:189], v[108:111]
	ds_read_b128 v[182:185], v162 offset:11264
	buffer_load_dwordx4 v[20:23], v160, s[16:19], s25 offen
	s_waitcnt vmcnt(11)
	v_cvt_pk_bf16_f32 v7, v6, v7
	v_cvt_pk_bf16_f32 v6, v4, v5
	v_mfma_f32_16x16x32_bf16 v[104:107], v[248:251], v[186:189], v[104:107]
	ds_write_b64 v161, v[6:7] offset:43776
	v_mfma_f32_16x16x32_bf16 v[100:103], v[198:201], v[186:189], v[100:103]
	v_mfma_f32_16x16x32_bf16 v[96:99], v[202:205], v[186:189], v[96:99]
	s_waitcnt lgkmcnt(2)
	v_mfma_f32_16x16x32_bf16 v[92:95], v[244:247], v[170:173], v[92:95]
	ds_read_b128 v[186:189], v162 offset:13312
	v_mfma_f32_16x16x32_bf16 v[88:91], v[248:251], v[170:173], v[88:91]
	v_mfma_f32_16x16x32_bf16 v[84:87], v[198:201], v[170:173], v[84:87]
	v_mfma_f32_16x16x32_bf16 v[80:83], v[202:205], v[170:173], v[80:83]
	s_waitcnt lgkmcnt(2)
	v_mfma_f32_16x16x32_bf16 v[76:79], v[244:247], v[182:185], v[76:79]
	ds_read_b128 v[252:255], v162 offset:15360
	buffer_load_dwordx4 v[4:7], v160, s[16:19], s26 offen
	s_waitcnt vmcnt(11)
	v_cvt_pk_bf16_f32 v11, v10, v11
	v_cvt_pk_bf16_f32 v10, v8, v9
	v_mfma_f32_16x16x32_bf16 v[72:75], v[248:251], v[182:185], v[72:75]
	ds_write_b64 v161, v[10:11] offset:52480
	v_mfma_f32_16x16x32_bf16 v[68:71], v[198:201], v[182:185], v[68:71]
	v_mfma_f32_16x16x32_bf16 v[64:67], v[202:205], v[182:185], v[64:67]
	s_waitcnt lgkmcnt(2)
	v_mfma_f32_16x16x32_bf16 v[60:63], v[244:247], v[186:189], v[60:63]
	v_mfma_f32_16x16x32_bf16 v[56:59], v[248:251], v[186:189], v[56:59]
	v_mfma_f32_16x16x32_bf16 v[52:55], v[198:201], v[186:189], v[52:55]
	v_mfma_f32_16x16x32_bf16 v[48:51], v[202:205], v[186:189], v[48:51]
	s_waitcnt lgkmcnt(1)
	buffer_load_dwordx4 v[8:11], v160, s[16:19], s27 offen
	s_waitcnt vmcnt(11)
	v_cvt_pk_bf16_f32 v19, v18, v19
	v_cvt_pk_bf16_f32 v18, v16, v17
	ds_write_b64 v161, v[18:19] offset:61184
	buffer_load_dwordx4 v[16:19], v160, s[16:19], s42 offen
	s_waitcnt vmcnt(8)
	s_mov_b32 m0, s55
	s_waitcnt lgkmcnt(0)
	s_barrier
	ds_read_b64_tr_b16 v[170:171], v166 offset:34816
	ds_read_b64_tr_b16 v[172:173], v167 offset:34816
	ds_read_b64_tr_b16 v[176:177], v167 offset:34848
	ds_read_b128 v[178:181], v162 offset:32768
	ds_read_b64_tr_b16 v[174:175], v166 offset:34848
	ds_read_b64_tr_b16 v[182:183], v166 offset:34880
	ds_read_b64_tr_b16 v[186:187], v166 offset:34912
	ds_read_b64_tr_b16 v[184:185], v167 offset:34880
	ds_read_b64_tr_b16 v[188:189], v167 offset:34912
	ds_read_b128 v[190:193], v162 offset:34816
	ds_read_b128 v[194:197], v162 offset:36864
	buffer_load_dwordx4 v163, s[20:23], s24 offen lds
	s_mov_b32 m0, s56
	v_mfma_f32_16x16x32_bf16 v[44:47], v[244:247], v[252:255], v[44:47]
	v_mfma_f32_16x16x32_bf16 v[40:43], v[248:251], v[252:255], v[40:43]
	v_mfma_f32_16x16x32_bf16 v[36:39], v[198:201], v[252:255], v[36:39]
	v_mfma_f32_16x16x32_bf16 v[32:35], v[202:205], v[252:255], v[32:35]
	s_waitcnt lgkmcnt(7)
	v_mfma_f32_16x16x32_bf16 v[156:159], v[170:173], v[178:181], v[156:159]
	buffer_load_dwordx4 v165, s[20:23], s24 offen lds
	s_mov_b32 m0, s57
	s_add_i32 s25, s9, 0xffee0000
	buffer_load_dwordx4 v164, s[20:23], s24 offen lds
	s_mov_b32 m0, s59
	s_waitcnt lgkmcnt(6)
	v_mfma_f32_16x16x32_bf16 v[152:155], v[174:177], v[178:181], v[152:155]
	buffer_load_dwordx4 v168, s[20:23], s24 offen lds
	s_waitcnt lgkmcnt(3)
	v_mfma_f32_16x16x32_bf16 v[148:151], v[182:185], v[178:181], v[148:151]
	s_waitcnt lgkmcnt(2)
	v_mfma_f32_16x16x32_bf16 v[144:147], v[186:189], v[178:181], v[144:147]
	s_waitcnt lgkmcnt(1)
	v_mfma_f32_16x16x32_bf16 v[140:143], v[170:173], v[190:193], v[140:143]
	ds_read_b128 v[178:181], v162 offset:38912
	s_waitcnt vmcnt(11)
	v_cvt_pk_bf16_f32 v15, v14, v15
	v_cvt_pk_bf16_f32 v14, v12, v13
	v_mfma_f32_16x16x32_bf16 v[136:139], v[174:177], v[190:193], v[136:139]
	ds_write_b64 v161, v[14:15]
	v_mfma_f32_16x16x32_bf16 v[132:135], v[182:185], v[190:193], v[132:135]
	v_mfma_f32_16x16x32_bf16 v[128:131], v[186:189], v[190:193], v[128:131]
	s_waitcnt lgkmcnt(2)
	v_mfma_f32_16x16x32_bf16 v[124:127], v[170:173], v[194:197], v[124:127]
	ds_read_b128 v[190:193], v162 offset:40960
	v_mfma_f32_16x16x32_bf16 v[120:123], v[174:177], v[194:197], v[120:123]
	v_mfma_f32_16x16x32_bf16 v[116:119], v[182:185], v[194:197], v[116:119]
	v_mfma_f32_16x16x32_bf16 v[112:115], v[186:189], v[194:197], v[112:115]
	s_waitcnt lgkmcnt(2)
	v_mfma_f32_16x16x32_bf16 v[108:111], v[170:173], v[178:181], v[108:111]
	ds_read_b128 v[194:197], v162 offset:43008
	buffer_load_dwordx4 v[12:15], v160, s[12:15], s25 offen
	s_waitcnt vmcnt(11)
	v_cvt_pk_bf16_f32 v3, v2, v3
	v_cvt_pk_bf16_f32 v2, v0, v1
	v_mfma_f32_16x16x32_bf16 v[104:107], v[174:177], v[178:181], v[104:107]
	ds_write_b64 v161, v[2:3] offset:8704
	v_mfma_f32_16x16x32_bf16 v[100:103], v[182:185], v[178:181], v[100:103]
	v_mfma_f32_16x16x32_bf16 v[96:99], v[186:189], v[178:181], v[96:99]
	s_add_i32 s26, s9, 0xfff40000
	s_waitcnt lgkmcnt(2)
; #define G_DMA_A(kt, AO) do { G_DMA1(kt, AO, 0); G_DMA1(kt, AO, 1); G_DMA1(kt, AO, 2); G_DMA1(kt, AO, 3); if (MF == 9) G_DMA5(kt, AO); } while (0)
; #define G_ISSUE_B(kt) do { const unsigned _sb = (unsigned)(kt) * 4u * kstepB; \
;         _Pragma("unroll") for (int _i = 0; _i < 8; ++_i) sb[_i] = bload16(_i < 4 ? rsB0 : rsB1, vob, _sb + (_i & 3) * kstepB); } while (0)
; #define G_WRITE_B(BO) do { \
;         _Pragma("unroll") for (int _i = 0; _i < 8; ++_i) *(LAS u32x2*)(b_wr + (BO) + (_i & 3) * (16 * G_BSTRIDE) + (_i >> 2) * SLAB1) = pack4(__builtin_bit_cast(f32x4, sb[_i])); } while (0)
; #define G_ENDTILE(VM) do { asm volatile("s_waitcnt vmcnt(" #VM ")" ::: "memory"); \
;         asm volatile("s_waitcnt lgkmcnt(0)" ::: "memory"); __builtin_amdgcn_s_barrier(); asm volatile("" ::: "memory"); } while (0)
;     ...
;     __builtin_amdgcn_s_barrier();
;     G_DMA_A(0, G_A0); G_ISSUE_B(0); G_WRITE_B(G_B0);
;     __builtin_amdgcn_sched_barrier(0);
;     G_ISSUE_B(1);
;     __builtin_amdgcn_sched_barrier(0);
;     G_ENDTILE(8);
;     for (int ui = 0;; ++ui) {
; #pragma unroll
;         for (int m = 0; m < MF; ++m)
; #pragma unroll
;             for (int n = 0; n < 4; ++n) acc[m][n] = (f32x4){0.f, 0.f, 0.f, 0.f};
;         for (int t = 0; t < nt - 2; t += 2) {
;             G_TILE(G_A0, G_B0, true, G_B1, G_A1, t + 1, true, t + 2, (void)0);
;             G_ENDTILE(8);
;             G_TILE(G_A1, G_B1, true, G_B0, G_A0, t + 2, true, t + 3, (void)0);
;             G_ENDTILE(8);
;         }
	v_mfma_f32_16x16x32_bf16 v[92:95], v[170:173], v[190:193], v[92:95]
	ds_read_b128 v[178:181], v162 offset:45056
	v_mfma_f32_16x16x32_bf16 v[88:91], v[174:177], v[190:193], v[88:91]
	v_mfma_f32_16x16x32_bf16 v[84:87], v[182:185], v[190:193], v[84:87]
	v_mfma_f32_16x16x32_bf16 v[80:83], v[186:189], v[190:193], v[80:83]
	s_waitcnt lgkmcnt(2)
	v_mfma_f32_16x16x32_bf16 v[76:79], v[170:173], v[194:197], v[76:79]
	ds_read_b128 v[190:193], v162 offset:47104
	buffer_load_dwordx4 v[0:3], v160, s[12:15], s26 offen
	s_waitcnt vmcnt(11)
	v_cvt_pk_bf16_f32 v31, v30, v31
	v_cvt_pk_bf16_f32 v30, v28, v29
	v_mfma_f32_16x16x32_bf16 v[72:75], v[174:177], v[194:197], v[72:75]
	ds_write_b64 v161, v[30:31] offset:17408
	v_mfma_f32_16x16x32_bf16 v[68:71], v[182:185], v[194:197], v[68:71]
	v_mfma_f32_16x16x32_bf16 v[64:67], v[186:189], v[194:197], v[64:67]
	s_add_i32 s27, s9, 0xfffa0000
	s_waitcnt lgkmcnt(2)
	v_mfma_f32_16x16x32_bf16 v[60:63], v[170:173], v[178:181], v[60:63]
	ds_read_b128 v[194:197], v162 offset:33792
	v_mfma_f32_16x16x32_bf16 v[56:59], v[174:177], v[178:181], v[56:59]
	v_mfma_f32_16x16x32_bf16 v[52:55], v[182:185], v[178:181], v[52:55]
	v_mfma_f32_16x16x32_bf16 v[48:51], v[186:189], v[178:181], v[48:51]
	s_waitcnt lgkmcnt(2)
	v_mfma_f32_16x16x32_bf16 v[44:47], v[170:173], v[190:193], v[44:47]
	ds_read_b128 v[170:173], v162 offset:35840
	buffer_load_dwordx4 v[28:31], v160, s[12:15], s27 offen
	s_waitcnt vmcnt(11)
	v_cvt_pk_bf16_f32 v27, v26, v27
	v_cvt_pk_bf16_f32 v26, v24, v25
	v_mfma_f32_16x16x32_bf16 v[40:43], v[174:177], v[190:193], v[40:43]
	ds_read_b64_tr_b16 v[244:245], v166 offset:52224
	ds_read_b64_tr_b16 v[248:249], v166 offset:52256
	ds_read_b64_tr_b16 v[198:199], v166 offset:52288
	ds_read_b64_tr_b16 v[202:203], v166 offset:52320
	ds_read_b64_tr_b16 v[246:247], v167 offset:52224
	ds_read_b64_tr_b16 v[250:251], v167 offset:52256
	ds_read_b64_tr_b16 v[200:201], v167 offset:52288
	ds_read_b64_tr_b16 v[204:205], v167 offset:52320
	ds_write_b64 v161, v[26:27] offset:26112
	v_mfma_f32_16x16x32_bf16 v[36:39], v[182:185], v[190:193], v[36:39]
	v_mfma_f32_16x16x32_bf16 v[32:35], v[186:189], v[190:193], v[32:35]
	s_waitcnt lgkmcnt(4)
	v_mfma_f32_16x16x32_bf16 v[156:159], v[244:247], v[194:197], v[156:159]
	ds_read_b128 v[182:185], v162 offset:37888
	s_waitcnt lgkmcnt(4)
	v_mfma_f32_16x16x32_bf16 v[152:155], v[248:251], v[194:197], v[152:155]
	s_waitcnt lgkmcnt(3)
	v_mfma_f32_16x16x32_bf16 v[148:151], v[198:201], v[194:197], v[148:151]
	s_waitcnt lgkmcnt(2)
	v_mfma_f32_16x16x32_bf16 v[144:147], v[202:205], v[194:197], v[144:147]
	v_mfma_f32_16x16x32_bf16 v[140:143], v[244:247], v[170:173], v[140:143]
	ds_read_b128 v[186:189], v162 offset:39936
	buffer_load_dwordx4 v[24:27], v160, s[12:15], s9 offen
	s_waitcnt vmcnt(11)
	v_cvt_pk_bf16_f32 v23, v22, v23
	v_cvt_pk_bf16_f32 v22, v20, v21
	v_mfma_f32_16x16x32_bf16 v[136:139], v[248:251], v[170:173], v[136:139]
	ds_write_b64 v161, v[22:23] offset:256
	v_mfma_f32_16x16x32_bf16 v[132:135], v[198:201], v[170:173], v[132:135]
	v_mfma_f32_16x16x32_bf16 v[128:131], v[202:205], v[170:173], v[128:131]
	s_waitcnt lgkmcnt(2)
	v_mfma_f32_16x16x32_bf16 v[124:127], v[244:247], v[182:185], v[124:127]
	ds_read_b128 v[170:173], v162 offset:41984
	v_mfma_f32_16x16x32_bf16 v[120:123], v[248:251], v[182:185], v[120:123]
	v_mfma_f32_16x16x32_bf16 v[116:119], v[198:201], v[182:185], v[116:119]
	v_mfma_f32_16x16x32_bf16 v[112:115], v[202:205], v[182:185], v[112:115]
	s_waitcnt lgkmcnt(2)
	v_mfma_f32_16x16x32_bf16 v[108:111], v[244:247], v[186:189], v[108:111]
	ds_read_b128 v[182:185], v162 offset:44032
	buffer_load_dwordx4 v[20:23], v160, s[16:19], s25 offen
	s_waitcnt vmcnt(11)
	v_cvt_pk_bf16_f32 v7, v6, v7
	v_cvt_pk_bf16_f32 v6, v4, v5
	v_mfma_f32_16x16x32_bf16 v[104:107], v[248:251], v[186:189], v[104:107]
	ds_write_b64 v161, v[6:7] offset:8960
	v_mfma_f32_16x16x32_bf16 v[100:103], v[198:201], v[186:189], v[100:103]
	v_mfma_f32_16x16x32_bf16 v[96:99], v[202:205], v[186:189], v[96:99]
	s_waitcnt lgkmcnt(2)
	v_mfma_f32_16x16x32_bf16 v[92:95], v[244:247], v[170:173], v[92:95]
	ds_read_b128 v[186:189], v162 offset:46080
	v_mfma_f32_16x16x32_bf16 v[88:91], v[248:251], v[170:173], v[88:91]
	v_mfma_f32_16x16x32_bf16 v[84:87], v[198:201], v[170:173], v[84:87]
	v_mfma_f32_16x16x32_bf16 v[80:83], v[202:205], v[170:173], v[80:83]
	s_waitcnt lgkmcnt(2)
	v_mfma_f32_16x16x32_bf16 v[76:79], v[244:247], v[182:185], v[76:79]
	ds_read_b128 v[252:255], v162 offset:48128
	buffer_load_dwordx4 v[4:7], v160, s[16:19], s26 offen
	s_waitcnt vmcnt(11)
	v_cvt_pk_bf16_f32 v11, v10, v11
	v_cvt_pk_bf16_f32 v10, v8, v9
	v_mfma_f32_16x16x32_bf16 v[72:75], v[248:251], v[182:185], v[72:75]
	ds_write_b64 v161, v[10:11] offset:17664
	v_mfma_f32_16x16x32_bf16 v[68:71], v[198:201], v[182:185], v[68:71]
	v_mfma_f32_16x16x32_bf16 v[64:67], v[202:205], v[182:185], v[64:67]
	s_waitcnt lgkmcnt(2)
	v_mfma_f32_16x16x32_bf16 v[60:63], v[244:247], v[186:189], v[60:63]
	v_mfma_f32_16x16x32_bf16 v[56:59], v[248:251], v[186:189], v[56:59]
	v_mfma_f32_16x16x32_bf16 v[52:55], v[198:201], v[186:189], v[52:55]
	v_mfma_f32_16x16x32_bf16 v[48:51], v[202:205], v[186:189], v[48:51]
	s_waitcnt lgkmcnt(1)
	buffer_load_dwordx4 v[8:11], v160, s[16:19], s27 offen
	s_waitcnt vmcnt(11)
	v_cvt_pk_bf16_f32 v19, v18, v19
	v_cvt_pk_bf16_f32 v18, v16, v17
	ds_write_b64 v161, v[18:19] offset:26368
	buffer_load_dwordx4 v[16:19], v160, s[16:19], s9 offen
	s_waitcnt vmcnt(8)
	s_waitcnt lgkmcnt(0)
	s_barrier
	s_add_i32 s8, s8, 2
	s_add_i32 s9, s9, 0x300000
	s_addk_i32 s24, 0x100
	s_cmp_ge_i32 s8, s64
	s_cbranch_scc0 .LBB0_71
	v_mfma_f32_16x16x32_bf16 v[44:47], v[244:247], v[252:255], v[44:47]
	v_mfma_f32_16x16x32_bf16 v[40:43], v[248:251], v[252:255], v[40:43]
	v_mfma_f32_16x16x32_bf16 v[36:39], v[198:201], v[252:255], v[36:39]
	v_mfma_f32_16x16x32_bf16 v[32:35], v[202:205], v[252:255], v[32:35]
	s_branch .LBB0_73

.LBB0_378:
	s_mov_b32 m0, s72
	s_add_i32 s25, s24, 0xffffff80
	ds_read_b64_tr_b16 v[170:171], v165
	ds_read_b64_tr_b16 v[172:173], v166
	ds_read_b64_tr_b16 v[176:177], v166 offset:32
	ds_read_b128 v[178:181], v162
	ds_read_b64_tr_b16 v[174:175], v165 offset:32
	ds_read_b64_tr_b16 v[182:183], v165 offset:64
	ds_read_b64_tr_b16 v[186:187], v165 offset:96
	ds_read_b64_tr_b16 v[184:185], v166 offset:64
	ds_read_b64_tr_b16 v[188:189], v166 offset:96
	ds_read_b128 v[190:193], v162 offset:2048
	ds_read_b128 v[198:201], v162 offset:4096
	buffer_load_dwordx4 v163, s[20:23], s25 offen lds
	s_mov_b32 m0, s71
	v_mfma_f32_16x16x32_bf16 v[44:47], v[244:247], v[252:255], v[44:47]
	v_mfma_f32_16x16x32_bf16 v[40:43], v[248:251], v[252:255], v[40:43]
	v_mfma_f32_16x16x32_bf16 v[36:39], v[202:205], v[252:255], v[36:39]
	v_mfma_f32_16x16x32_bf16 v[32:35], v[206:209], v[252:255], v[32:35]
	s_waitcnt lgkmcnt(7)
	v_mfma_f32_16x16x32_bf16 v[156:159], v[170:173], v[178:181], v[156:159]
	buffer_load_dwordx4 v164, s[20:23], s25 offen lds
	s_mov_b32 m0, s70
	s_nop 0
	buffer_load_dwordx4 v167, s[20:23], s25 offen lds
	s_mov_b32 m0, s68
	s_waitcnt lgkmcnt(6)
	v_mfma_f32_16x16x32_bf16 v[152:155], v[174:177], v[178:181], v[152:155]
	buffer_load_dwordx4 v168, s[20:23], s25 offen lds
	s_add_i32 s25, s9, 0xfff20000
	s_waitcnt lgkmcnt(3)
	v_mfma_f32_16x16x32_bf16 v[148:151], v[182:185], v[178:181], v[148:151]
	s_waitcnt lgkmcnt(2)
	v_mfma_f32_16x16x32_bf16 v[144:147], v[186:189], v[178:181], v[144:147]
	s_waitcnt lgkmcnt(1)
	v_mfma_f32_16x16x32_bf16 v[140:143], v[170:173], v[190:193], v[140:143]
	ds_read_b128 v[178:181], v162 offset:6144
	s_waitcnt vmcnt(11)
	v_cvt_pk_bf16_f32 v15, v14, v15
	v_cvt_pk_bf16_f32 v14, v12, v13
	v_mfma_f32_16x16x32_bf16 v[136:139], v[174:177], v[190:193], v[136:139]
	ds_write_b64 v161, v[14:15] offset:34816
	v_mfma_f32_16x16x32_bf16 v[132:135], v[182:185], v[190:193], v[132:135]
	v_mfma_f32_16x16x32_bf16 v[128:131], v[186:189], v[190:193], v[128:131]
	s_waitcnt lgkmcnt(2)
	v_mfma_f32_16x16x32_bf16 v[124:127], v[170:173], v[198:201], v[124:127]
	ds_read_b128 v[190:193], v162 offset:8192
	v_mfma_f32_16x16x32_bf16 v[120:123], v[174:177], v[198:201], v[120:123]
	v_mfma_f32_16x16x32_bf16 v[116:119], v[182:185], v[198:201], v[116:119]
	v_mfma_f32_16x16x32_bf16 v[112:115], v[186:189], v[198:201], v[112:115]
	s_waitcnt lgkmcnt(2)
	v_mfma_f32_16x16x32_bf16 v[108:111], v[170:173], v[178:181], v[108:111]
	ds_read_b128 v[198:201], v162 offset:10240
	buffer_load_dwordx4 v[12:15], v160, s[12:15], s25 offen
	s_waitcnt vmcnt(10)
	v_cvt_pk_bf16_f32 v31, v30, v31
	v_cvt_pk_bf16_f32 v30, v28, v29
	v_mfma_f32_16x16x32_bf16 v[104:107], v[174:177], v[178:181], v[104:107]
	ds_write_b64 v161, v[30:31] offset:43520
	v_mfma_f32_16x16x32_bf16 v[100:103], v[182:185], v[178:181], v[100:103]
	v_mfma_f32_16x16x32_bf16 v[96:99], v[186:189], v[178:181], v[96:99]
	s_add_i32 s26, s9, 0xfff40000
	s_waitcnt lgkmcnt(2)
	v_mfma_f32_16x16x32_bf16 v[92:95], v[170:173], v[190:193], v[92:95]
	ds_read_b128 v[178:181], v162 offset:12288
	v_mfma_f32_16x16x32_bf16 v[88:91], v[174:177], v[190:193], v[88:91]
	v_mfma_f32_16x16x32_bf16 v[84:87], v[182:185], v[190:193], v[84:87]
	v_mfma_f32_16x16x32_bf16 v[80:83], v[186:189], v[190:193], v[80:83]
	s_waitcnt lgkmcnt(2)
	v_mfma_f32_16x16x32_bf16 v[76:79], v[170:173], v[198:201], v[76:79]
	ds_read_b128 v[190:193], v162 offset:14336
	v_cvt_pk_bf16_f32 v7, v6, v7
	v_cvt_pk_bf16_f32 v6, v4, v5
	v_mfma_f32_16x16x32_bf16 v[72:75], v[174:177], v[198:201], v[72:75]
	ds_write_b64 v161, v[6:7] offset:52224
	v_mfma_f32_16x16x32_bf16 v[68:71], v[182:185], v[198:201], v[68:71]
	v_mfma_f32_16x16x32_bf16 v[64:67], v[186:189], v[198:201], v[64:67]
	s_add_i32 s27, s9, 0xfff60000
	buffer_load_dwordx4 v[28:31], v160, s[12:15], s26 offen
	s_waitcnt lgkmcnt(2)
	v_mfma_f32_16x16x32_bf16 v[60:63], v[170:173], v[178:181], v[60:63]
	ds_read_b128 v[198:201], v162 offset:1024
	v_mfma_f32_16x16x32_bf16 v[56:59], v[174:177], v[178:181], v[56:59]
	v_mfma_f32_16x16x32_bf16 v[52:55], v[182:185], v[178:181], v[52:55]
	v_mfma_f32_16x16x32_bf16 v[48:51], v[186:189], v[178:181], v[48:51]
	s_waitcnt lgkmcnt(2)
	v_mfma_f32_16x16x32_bf16 v[44:47], v[170:173], v[190:193], v[44:47]
	ds_read_b128 v[170:173], v162 offset:3072
	buffer_load_dwordx4 v[4:7], v160, s[12:15], s27 offen
	s_waitcnt vmcnt(11)
	v_cvt_pk_bf16_f32 v27, v26, v27
	v_cvt_pk_bf16_f32 v26, v24, v25
	v_mfma_f32_16x16x32_bf16 v[40:43], v[174:177], v[190:193], v[40:43]
	ds_read_b64_tr_b16 v[244:245], v165 offset:17408
	ds_read_b64_tr_b16 v[248:249], v165 offset:17440
	ds_read_b64_tr_b16 v[202:203], v165 offset:17472
	ds_read_b64_tr_b16 v[206:207], v165 offset:17504
	ds_read_b64_tr_b16 v[246:247], v166 offset:17408
	ds_read_b64_tr_b16 v[250:251], v166 offset:17440
	ds_read_b64_tr_b16 v[204:205], v166 offset:17472
	ds_read_b64_tr_b16 v[208:209], v166 offset:17504
	ds_write_b64 v161, v[26:27] offset:60928
	v_mfma_f32_16x16x32_bf16 v[36:39], v[182:185], v[190:193], v[36:39]
	v_mfma_f32_16x16x32_bf16 v[32:35], v[186:189], v[190:193], v[32:35]
	s_add_i32 s45, s9, 0xfff80000
	s_waitcnt lgkmcnt(4)
	v_mfma_f32_16x16x32_bf16 v[156:159], v[244:247], v[198:201], v[156:159]
	ds_read_b128 v[182:185], v162 offset:5120
	s_waitcnt lgkmcnt(4)
	v_mfma_f32_16x16x32_bf16 v[152:155], v[248:251], v[198:201], v[152:155]
	s_waitcnt lgkmcnt(3)
	v_mfma_f32_16x16x32_bf16 v[148:151], v[202:205], v[198:201], v[148:151]
	s_waitcnt lgkmcnt(2)
	v_mfma_f32_16x16x32_bf16 v[144:147], v[206:209], v[198:201], v[144:147]
	v_mfma_f32_16x16x32_bf16 v[140:143], v[244:247], v[170:173], v[140:143]
	ds_read_b128 v[186:189], v162 offset:7168
	buffer_load_dwordx4 v[24:27], v160, s[12:15], s45 offen
	s_waitcnt vmcnt(11)
; #define G_DMA_A(kt, AO) do { G_DMA1(kt, AO, 0); G_DMA1(kt, AO, 1); G_DMA1(kt, AO, 2); G_DMA1(kt, AO, 3); if (MF == 9) G_DMA5(kt, AO); } while (0)
; #define G_ISSUE_B(kt) do { const unsigned _sb = (unsigned)(kt) * 4u * kstepB; \
;         _Pragma("unroll") for (int _i = 0; _i < 8; ++_i) sb[_i] = bload16(_i < 4 ? rsB0 : rsB1, vob, _sb + (_i & 3) * kstepB); } while (0)
; #define G_WRITE_B(BO) do { \
;         _Pragma("unroll") for (int _i = 0; _i < 8; ++_i) *(LAS u32x2*)(b_wr + (BO) + (_i & 3) * (16 * G_BSTRIDE) + (_i >> 2) * SLAB1) = pack4(__builtin_bit_cast(f32x4, sb[_i])); } while (0)
; #define G_ENDTILE(VM) do { asm volatile("s_waitcnt vmcnt(" #VM ")" ::: "memory"); \
;         asm volatile("s_waitcnt lgkmcnt(0)" ::: "memory"); __builtin_amdgcn_s_barrier(); asm volatile("" ::: "memory"); } while (0)
;     ...
;     __builtin_amdgcn_s_barrier();
;     G_DMA_A(0, G_A0); G_ISSUE_B(0); G_WRITE_B(G_B0);
;     __builtin_amdgcn_sched_barrier(0);
;     G_ISSUE_B(1);
;     __builtin_amdgcn_sched_barrier(0);
;     G_ENDTILE(8);
;     for (int ui = 0;; ++ui) {
; #pragma unroll
;         for (int m = 0; m < MF; ++m)
; #pragma unroll
;             for (int n = 0; n < 4; ++n) acc[m][n] = (f32x4){0.f, 0.f, 0.f, 0.f};
;         for (int t = 0; t < nt - 2; t += 2) {
;             G_TILE(G_A0, G_B0, true, G_B1, G_A1, t + 1, true, t + 2, (void)0);
;             G_ENDTILE(8);
;             G_TILE(G_A1, G_B1, true, G_B0, G_A0, t + 2, true, t + 3, (void)0);
;             G_ENDTILE(8);
;         }
	v_cvt_pk_bf16_f32 v23, v22, v23
	v_cvt_pk_bf16_f32 v22, v20, v21
	v_mfma_f32_16x16x32_bf16 v[136:139], v[248:251], v[170:173], v[136:139]
	ds_write_b64 v161, v[22:23] offset:35072
	v_mfma_f32_16x16x32_bf16 v[132:135], v[202:205], v[170:173], v[132:135]
	v_mfma_f32_16x16x32_bf16 v[128:131], v[206:209], v[170:173], v[128:131]
	s_waitcnt lgkmcnt(2)
	v_mfma_f32_16x16x32_bf16 v[124:127], v[244:247], v[182:185], v[124:127]
	ds_read_b128 v[170:173], v162 offset:9216
	v_mfma_f32_16x16x32_bf16 v[120:123], v[248:251], v[182:185], v[120:123]
	v_mfma_f32_16x16x32_bf16 v[116:119], v[202:205], v[182:185], v[116:119]
	v_mfma_f32_16x16x32_bf16 v[112:115], v[206:209], v[182:185], v[112:115]
	s_waitcnt lgkmcnt(2)
	v_mfma_f32_16x16x32_bf16 v[108:111], v[244:247], v[186:189], v[108:111]
	ds_read_b128 v[182:185], v162 offset:11264
	buffer_load_dwordx4 v[20:23], v160, s[16:19], s25 offen
	s_waitcnt vmcnt(10)
	v_cvt_pk_bf16_f32 v11, v10, v11
	v_cvt_pk_bf16_f32 v10, v8, v9
	v_mfma_f32_16x16x32_bf16 v[104:107], v[248:251], v[186:189], v[104:107]
	ds_write_b64 v161, v[10:11] offset:43776
	v_mfma_f32_16x16x32_bf16 v[100:103], v[202:205], v[186:189], v[100:103]
	v_mfma_f32_16x16x32_bf16 v[96:99], v[206:209], v[186:189], v[96:99]
	s_waitcnt lgkmcnt(2)
	v_mfma_f32_16x16x32_bf16 v[92:95], v[244:247], v[170:173], v[92:95]
	ds_read_b128 v[186:189], v162 offset:13312
	v_mfma_f32_16x16x32_bf16 v[88:91], v[248:251], v[170:173], v[88:91]
	v_mfma_f32_16x16x32_bf16 v[84:87], v[202:205], v[170:173], v[84:87]
	v_mfma_f32_16x16x32_bf16 v[80:83], v[206:209], v[170:173], v[80:83]
	s_waitcnt lgkmcnt(2)
	v_mfma_f32_16x16x32_bf16 v[76:79], v[244:247], v[182:185], v[76:79]
	ds_read_b128 v[252:255], v162 offset:15360
	v_cvt_pk_bf16_f32 v3, v2, v3
	v_cvt_pk_bf16_f32 v2, v0, v1
	v_mfma_f32_16x16x32_bf16 v[72:75], v[248:251], v[182:185], v[72:75]
	ds_write_b64 v161, v[2:3] offset:52480
	v_mfma_f32_16x16x32_bf16 v[68:71], v[202:205], v[182:185], v[68:71]
	v_mfma_f32_16x16x32_bf16 v[64:67], v[206:209], v[182:185], v[64:67]
	buffer_load_dwordx4 v[8:11], v160, s[16:19], s26 offen
	s_waitcnt lgkmcnt(2)
	v_mfma_f32_16x16x32_bf16 v[60:63], v[244:247], v[186:189], v[60:63]
	v_mfma_f32_16x16x32_bf16 v[56:59], v[248:251], v[186:189], v[56:59]
	v_mfma_f32_16x16x32_bf16 v[52:55], v[202:205], v[186:189], v[52:55]
	v_mfma_f32_16x16x32_bf16 v[48:51], v[206:209], v[186:189], v[48:51]
	s_waitcnt lgkmcnt(1)
	buffer_load_dwordx4 v[0:3], v160, s[16:19], s27 offen
	s_waitcnt vmcnt(11)
	v_cvt_pk_bf16_f32 v19, v18, v19
	v_cvt_pk_bf16_f32 v18, v16, v17
	ds_write_b64 v161, v[18:19] offset:61184
	buffer_load_dwordx4 v[16:19], v160, s[16:19], s45 offen
	s_waitcnt vmcnt(8)
	s_mov_b32 m0, s59
	s_waitcnt lgkmcnt(0)
	s_barrier
	ds_read_b64_tr_b16 v[170:171], v165 offset:34816
	ds_read_b64_tr_b16 v[172:173], v166 offset:34816
	ds_read_b64_tr_b16 v[176:177], v166 offset:34848
	ds_read_b128 v[178:181], v162 offset:32768
	ds_read_b64_tr_b16 v[174:175], v165 offset:34848
	ds_read_b64_tr_b16 v[182:183], v165 offset:34880
	ds_read_b64_tr_b16 v[186:187], v165 offset:34912
	ds_read_b64_tr_b16 v[184:185], v166 offset:34880
	ds_read_b64_tr_b16 v[188:189], v166 offset:34912
	ds_read_b128 v[190:193], v162 offset:34816
	ds_read_b128 v[198:201], v162 offset:36864
	buffer_load_dwordx4 v163, s[20:23], s24 offen lds
	s_mov_b32 m0, s60
	v_mfma_f32_16x16x32_bf16 v[44:47], v[244:247], v[252:255], v[44:47]
	v_mfma_f32_16x16x32_bf16 v[40:43], v[248:251], v[252:255], v[40:43]
	v_mfma_f32_16x16x32_bf16 v[36:39], v[202:205], v[252:255], v[36:39]
	v_mfma_f32_16x16x32_bf16 v[32:35], v[206:209], v[252:255], v[32:35]
	s_waitcnt lgkmcnt(7)
	v_mfma_f32_16x16x32_bf16 v[156:159], v[170:173], v[178:181], v[156:159]
	buffer_load_dwordx4 v164, s[20:23], s24 offen lds
	s_mov_b32 m0, s61
	s_add_i32 s25, s9, 0xfffa0000
	buffer_load_dwordx4 v167, s[20:23], s24 offen lds
	s_mov_b32 m0, s62
	s_waitcnt lgkmcnt(6)
	v_mfma_f32_16x16x32_bf16 v[152:155], v[174:177], v[178:181], v[152:155]
	buffer_load_dwordx4 v168, s[20:23], s24 offen lds
	s_waitcnt lgkmcnt(3)
	v_mfma_f32_16x16x32_bf16 v[148:151], v[182:185], v[178:181], v[148:151]
	s_waitcnt lgkmcnt(2)
	v_mfma_f32_16x16x32_bf16 v[144:147], v[186:189], v[178:181], v[144:147]
	s_waitcnt lgkmcnt(1)
	v_mfma_f32_16x16x32_bf16 v[140:143], v[170:173], v[190:193], v[140:143]
	ds_read_b128 v[178:181], v162 offset:38912
	s_waitcnt vmcnt(11)
	v_cvt_pk_bf16_f32 v15, v14, v15
	v_cvt_pk_bf16_f32 v14, v12, v13
	v_mfma_f32_16x16x32_bf16 v[136:139], v[174:177], v[190:193], v[136:139]
	ds_write_b64 v161, v[14:15]
	v_mfma_f32_16x16x32_bf16 v[132:135], v[182:185], v[190:193], v[132:135]
	v_mfma_f32_16x16x32_bf16 v[128:131], v[186:189], v[190:193], v[128:131]
	s_waitcnt lgkmcnt(2)
	v_mfma_f32_16x16x32_bf16 v[124:127], v[170:173], v[198:201], v[124:127]
	ds_read_b128 v[190:193], v162 offset:40960
	v_mfma_f32_16x16x32_bf16 v[120:123], v[174:177], v[198:201], v[120:123]
	v_mfma_f32_16x16x32_bf16 v[116:119], v[182:185], v[198:201], v[116:119]
	v_mfma_f32_16x16x32_bf16 v[112:115], v[186:189], v[198:201], v[112:115]
	s_waitcnt lgkmcnt(2)
	v_mfma_f32_16x16x32_bf16 v[108:111], v[170:173], v[178:181], v[108:111]
	ds_read_b128 v[198:201], v162 offset:43008
	buffer_load_dwordx4 v[12:15], v160, s[12:15], s25 offen
	s_waitcnt vmcnt(11)
	v_cvt_pk_bf16_f32 v31, v30, v31
	v_cvt_pk_bf16_f32 v30, v28, v29
	v_mfma_f32_16x16x32_bf16 v[104:107], v[174:177], v[178:181], v[104:107]
	ds_write_b64 v161, v[30:31] offset:8704
	v_mfma_f32_16x16x32_bf16 v[100:103], v[182:185], v[178:181], v[100:103]
	v_mfma_f32_16x16x32_bf16 v[96:99], v[186:189], v[178:181], v[96:99]
	s_add_i32 s26, s9, 0xfffc0000
	s_waitcnt lgkmcnt(2)
; #define G_DMA_A(kt, AO) do { G_DMA1(kt, AO, 0); G_DMA1(kt, AO, 1); G_DMA1(kt, AO, 2); G_DMA1(kt, AO, 3); if (MF == 9) G_DMA5(kt, AO); } while (0)
; #define G_ISSUE_B(kt) do { const unsigned _sb = (unsigned)(kt) * 4u * kstepB; \
;         _Pragma("unroll") for (int _i = 0; _i < 8; ++_i) sb[_i] = bload16(_i < 4 ? rsB0 : rsB1, vob, _sb + (_i & 3) * kstepB); } while (0)
; #define G_WRITE_B(BO) do { \
;         _Pragma("unroll") for (int _i = 0; _i < 8; ++_i) *(LAS u32x2*)(b_wr + (BO) + (_i & 3) * (16 * G_BSTRIDE) + (_i >> 2) * SLAB1) = pack4(__builtin_bit_cast(f32x4, sb[_i])); } while (0)
; #define G_ENDTILE(VM) do { asm volatile("s_waitcnt vmcnt(" #VM ")" ::: "memory"); \
;         asm volatile("s_waitcnt lgkmcnt(0)" ::: "memory"); __builtin_amdgcn_s_barrier(); asm volatile("" ::: "memory"); } while (0)
;     ...
;     __builtin_amdgcn_s_barrier();
;     G_DMA_A(0, G_A0); G_ISSUE_B(0); G_WRITE_B(G_B0);
;     __builtin_amdgcn_sched_barrier(0);
;     G_ISSUE_B(1);
;     __builtin_amdgcn_sched_barrier(0);
;     G_ENDTILE(8);
;     for (int ui = 0;; ++ui) {
; #pragma unroll
;         for (int m = 0; m < MF; ++m)
; #pragma unroll
;             for (int n = 0; n < 4; ++n) acc[m][n] = (f32x4){0.f, 0.f, 0.f, 0.f};
;         for (int t = 0; t < nt - 2; t += 2) {
;             G_TILE(G_A0, G_B0, true, G_B1, G_A1, t + 1, true, t + 2, (void)0);
;             G_ENDTILE(8);
;             G_TILE(G_A1, G_B1, true, G_B0, G_A0, t + 2, true, t + 3, (void)0);
;             G_ENDTILE(8);
;         }
	v_mfma_f32_16x16x32_bf16 v[92:95], v[170:173], v[190:193], v[92:95]
	ds_read_b128 v[178:181], v162 offset:45056
	v_mfma_f32_16x16x32_bf16 v[88:91], v[174:177], v[190:193], v[88:91]
	v_mfma_f32_16x16x32_bf16 v[84:87], v[182:185], v[190:193], v[84:87]
	v_mfma_f32_16x16x32_bf16 v[80:83], v[186:189], v[190:193], v[80:83]
	s_waitcnt lgkmcnt(2)
	v_mfma_f32_16x16x32_bf16 v[76:79], v[170:173], v[198:201], v[76:79]
	ds_read_b128 v[190:193], v162 offset:47104
	buffer_load_dwordx4 v[28:31], v160, s[12:15], s26 offen
	s_waitcnt vmcnt(11)
	v_cvt_pk_bf16_f32 v7, v6, v7
	v_cvt_pk_bf16_f32 v6, v4, v5
	v_mfma_f32_16x16x32_bf16 v[72:75], v[174:177], v[198:201], v[72:75]
	ds_write_b64 v161, v[6:7] offset:17408
	v_mfma_f32_16x16x32_bf16 v[68:71], v[182:185], v[198:201], v[68:71]
	v_mfma_f32_16x16x32_bf16 v[64:67], v[186:189], v[198:201], v[64:67]
	s_add_i32 s27, s9, 0xfffe0000
	s_waitcnt lgkmcnt(2)
	v_mfma_f32_16x16x32_bf16 v[60:63], v[170:173], v[178:181], v[60:63]
	ds_read_b128 v[198:201], v162 offset:33792
	v_mfma_f32_16x16x32_bf16 v[56:59], v[174:177], v[178:181], v[56:59]
	v_mfma_f32_16x16x32_bf16 v[52:55], v[182:185], v[178:181], v[52:55]
	v_mfma_f32_16x16x32_bf16 v[48:51], v[186:189], v[178:181], v[48:51]
	s_waitcnt lgkmcnt(2)
	v_mfma_f32_16x16x32_bf16 v[44:47], v[170:173], v[190:193], v[44:47]
	ds_read_b128 v[170:173], v162 offset:35840
	buffer_load_dwordx4 v[4:7], v160, s[12:15], s27 offen
	s_waitcnt vmcnt(11)
	v_cvt_pk_bf16_f32 v27, v26, v27
	v_cvt_pk_bf16_f32 v26, v24, v25
	v_mfma_f32_16x16x32_bf16 v[40:43], v[174:177], v[190:193], v[40:43]
	ds_read_b64_tr_b16 v[244:245], v165 offset:52224
	ds_read_b64_tr_b16 v[248:249], v165 offset:52256
	ds_read_b64_tr_b16 v[202:203], v165 offset:52288
	ds_read_b64_tr_b16 v[206:207], v165 offset:52320
	ds_read_b64_tr_b16 v[246:247], v166 offset:52224
	ds_read_b64_tr_b16 v[250:251], v166 offset:52256
	ds_read_b64_tr_b16 v[204:205], v166 offset:52288
	ds_read_b64_tr_b16 v[208:209], v166 offset:52320
	ds_write_b64 v161, v[26:27] offset:26112
	v_mfma_f32_16x16x32_bf16 v[36:39], v[182:185], v[190:193], v[36:39]
	v_mfma_f32_16x16x32_bf16 v[32:35], v[186:189], v[190:193], v[32:35]
	s_waitcnt lgkmcnt(4)
	v_mfma_f32_16x16x32_bf16 v[156:159], v[244:247], v[198:201], v[156:159]
	ds_read_b128 v[182:185], v162 offset:37888
	s_waitcnt lgkmcnt(4)
	v_mfma_f32_16x16x32_bf16 v[152:155], v[248:251], v[198:201], v[152:155]
	s_waitcnt lgkmcnt(3)
	v_mfma_f32_16x16x32_bf16 v[148:151], v[202:205], v[198:201], v[148:151]
	s_waitcnt lgkmcnt(2)
	v_mfma_f32_16x16x32_bf16 v[144:147], v[206:209], v[198:201], v[144:147]
	v_mfma_f32_16x16x32_bf16 v[140:143], v[244:247], v[170:173], v[140:143]
	ds_read_b128 v[186:189], v162 offset:39936
	buffer_load_dwordx4 v[24:27], v160, s[12:15], s9 offen
	s_waitcnt vmcnt(11)
	v_cvt_pk_bf16_f32 v23, v22, v23
	v_cvt_pk_bf16_f32 v22, v20, v21
	v_mfma_f32_16x16x32_bf16 v[136:139], v[248:251], v[170:173], v[136:139]
	ds_write_b64 v161, v[22:23] offset:256
	v_mfma_f32_16x16x32_bf16 v[132:135], v[202:205], v[170:173], v[132:135]
	v_mfma_f32_16x16x32_bf16 v[128:131], v[206:209], v[170:173], v[128:131]
	s_waitcnt lgkmcnt(2)
	v_mfma_f32_16x16x32_bf16 v[124:127], v[244:247], v[182:185], v[124:127]
	ds_read_b128 v[170:173], v162 offset:41984
	v_mfma_f32_16x16x32_bf16 v[120:123], v[248:251], v[182:185], v[120:123]
	v_mfma_f32_16x16x32_bf16 v[116:119], v[202:205], v[182:185], v[116:119]
	v_mfma_f32_16x16x32_bf16 v[112:115], v[206:209], v[182:185], v[112:115]
	s_waitcnt lgkmcnt(2)
	v_mfma_f32_16x16x32_bf16 v[108:111], v[244:247], v[186:189], v[108:111]
	ds_read_b128 v[182:185], v162 offset:44032
	buffer_load_dwordx4 v[20:23], v160, s[16:19], s25 offen
	s_waitcnt vmcnt(11)
	v_cvt_pk_bf16_f32 v11, v10, v11
	v_cvt_pk_bf16_f32 v10, v8, v9
	v_mfma_f32_16x16x32_bf16 v[104:107], v[248:251], v[186:189], v[104:107]
	ds_write_b64 v161, v[10:11] offset:8960
	v_mfma_f32_16x16x32_bf16 v[100:103], v[202:205], v[186:189], v[100:103]
	v_mfma_f32_16x16x32_bf16 v[96:99], v[206:209], v[186:189], v[96:99]
	s_waitcnt lgkmcnt(2)
	v_mfma_f32_16x16x32_bf16 v[92:95], v[244:247], v[170:173], v[92:95]
	ds_read_b128 v[186:189], v162 offset:46080
	v_mfma_f32_16x16x32_bf16 v[88:91], v[248:251], v[170:173], v[88:91]
	v_mfma_f32_16x16x32_bf16 v[84:87], v[202:205], v[170:173], v[84:87]
	v_mfma_f32_16x16x32_bf16 v[80:83], v[206:209], v[170:173], v[80:83]
	s_waitcnt lgkmcnt(2)
	v_mfma_f32_16x16x32_bf16 v[76:79], v[244:247], v[182:185], v[76:79]
	ds_read_b128 v[252:255], v162 offset:48128
	buffer_load_dwordx4 v[8:11], v160, s[16:19], s26 offen
	s_waitcnt vmcnt(11)
	v_cvt_pk_bf16_f32 v3, v2, v3
	v_cvt_pk_bf16_f32 v2, v0, v1
	v_mfma_f32_16x16x32_bf16 v[72:75], v[248:251], v[182:185], v[72:75]
	ds_write_b64 v161, v[2:3] offset:17664
	v_mfma_f32_16x16x32_bf16 v[68:71], v[202:205], v[182:185], v[68:71]
	v_mfma_f32_16x16x32_bf16 v[64:67], v[206:209], v[182:185], v[64:67]
	s_waitcnt lgkmcnt(2)
	v_mfma_f32_16x16x32_bf16 v[60:63], v[244:247], v[186:189], v[60:63]
	v_mfma_f32_16x16x32_bf16 v[56:59], v[248:251], v[186:189], v[56:59]
	v_mfma_f32_16x16x32_bf16 v[52:55], v[202:205], v[186:189], v[52:55]
	v_mfma_f32_16x16x32_bf16 v[48:51], v[206:209], v[186:189], v[48:51]
	s_waitcnt lgkmcnt(1)
	buffer_load_dwordx4 v[0:3], v160, s[16:19], s27 offen
	s_waitcnt vmcnt(11)
	v_cvt_pk_bf16_f32 v19, v18, v19
	v_cvt_pk_bf16_f32 v18, v16, v17
	ds_write_b64 v161, v[18:19] offset:26368
	buffer_load_dwordx4 v[16:19], v160, s[16:19], s9 offen
	s_waitcnt vmcnt(8)
	s_waitcnt lgkmcnt(0)
	s_barrier
	s_add_i32 s8, s8, 2
	s_add_i32 s9, s9, 0x100000
	s_addk_i32 s24, 0x100
	s_cmp_ge_i32 s8, s67
	s_cbranch_scc0 .LBB0_378
	v_mfma_f32_16x16x32_bf16 v[44:47], v[244:247], v[252:255], v[44:47]
	v_mfma_f32_16x16x32_bf16 v[40:43], v[248:251], v[252:255], v[40:43]
	v_mfma_f32_16x16x32_bf16 v[36:39], v[202:205], v[252:255], v[36:39]
	v_mfma_f32_16x16x32_bf16 v[32:35], v[206:209], v[252:255], v[32:35]
	s_branch .LBB0_380

; #define G_DMA_A(kt, AO) do { G_DMA1(kt, AO, 0); G_DMA1(kt, AO, 1); G_DMA1(kt, AO, 2); G_DMA1(kt, AO, 3); if (MF == 9) G_DMA5(kt, AO); } while (0)
; #define G_ISSUE_B(kt) do { const unsigned _sb = (unsigned)(kt) * 4u * kstepB; \
;         _Pragma("unroll") for (int _i = 0; _i < 8; ++_i) sb[_i] = bload16(_i < 4 ? rsB0 : rsB1, vob, _sb + (_i & 3) * kstepB); } while (0)
; #define G_WRITE_B(BO) do { \
;         _Pragma("unroll") for (int _i = 0; _i < 8; ++_i) *(LAS u32x2*)(b_wr + (BO) + (_i & 3) * (16 * G_BSTRIDE) + (_i >> 2) * SLAB1) = pack4(__builtin_bit_cast(f32x4, sb[_i])); } while (0)
; #define G_ENDTILE(VM) do { asm volatile("s_waitcnt vmcnt(" #VM ")" ::: "memory"); \
;         asm volatile("s_waitcnt lgkmcnt(0)" ::: "memory"); __builtin_amdgcn_s_barrier(); asm volatile("" ::: "memory"); } while (0)
;     ...
;     __builtin_amdgcn_s_barrier();
;     G_DMA_A(0, G_A0); G_ISSUE_B(0); G_WRITE_B(G_B0);
;     __builtin_amdgcn_sched_barrier(0);
;     G_ISSUE_B(1);
;     __builtin_amdgcn_sched_barrier(0);
;     G_ENDTILE(8);
;     for (int ui = 0;; ++ui) {
; #pragma unroll
;         for (int m = 0; m < MF; ++m)
; #pragma unroll
;             for (int n = 0; n < 4; ++n) acc[m][n] = (f32x4){0.f, 0.f, 0.f, 0.f};
;         for (int t = 0; t < nt - 2; t += 2) {
;             G_TILE(G_A0, G_B0, true, G_B1, G_A1, t + 1, true, t + 2, (void)0);
;             G_ENDTILE(8);
;             G_TILE(G_A1, G_B1, true, G_B0, G_A0, t + 2, true, t + 3, (void)0);
;             G_ENDTILE(8);
;         }
.LBB0_651:
	s_mov_b32 m0, s85
	s_add_i32 s37, s36, 0xffffff80
	ds_read_b64_tr_b16 v[178:179], v188
	ds_read_b64_tr_b16 v[176:177], v187
	ds_read_b64_tr_b16 v[180:181], v187 offset:32
	ds_read_b64_tr_b16 v[198:199], v187 offset:64
	ds_read_b64_tr_b16 v[202:203], v187 offset:96
	ds_read_b128 v[206:209], v186
	ds_read_b64_tr_b16 v[182:183], v188 offset:32
	ds_read_b64_tr_b16 v[200:201], v188 offset:64
	ds_read_b64_tr_b16 v[204:205], v188 offset:96
	ds_read_b128 v[210:213], v186 offset:2048
	ds_read_b128 v[214:217], v186 offset:4096
	buffer_load_dwordx4 v189, s[20:23], s37 offen lds
	s_mov_b32 m0, s7
	v_mfma_f32_16x16x32_bf16 v[44:47], v[244:247], v[238:241], v[44:47]
	v_mfma_f32_16x16x32_bf16 v[40:43], v[218:221], v[238:241], v[40:43]
	v_mfma_f32_16x16x32_bf16 v[36:39], v[248:251], v[238:241], v[36:39]
	v_mfma_f32_16x16x32_bf16 v[32:35], v[252:255], v[238:241], v[32:35]
	s_waitcnt lgkmcnt(5)
	v_mfma_f32_16x16x32_bf16 v[172:175], v[176:179], v[206:209], v[172:175]
	buffer_load_dwordx4 v192, s[20:23], s37 offen lds
	s_mov_b32 m0, s6
	s_nop 0
	buffer_load_dwordx4 v191, s[20:23], s37 offen lds
	s_mov_b32 m0, s47
	s_waitcnt lgkmcnt(4)
	v_mfma_f32_16x16x32_bf16 v[168:171], v[180:183], v[206:209], v[168:171]
	buffer_load_dwordx4 v190, s[20:23], s37 offen lds
	s_mov_b32 m0, s48
	s_nop 0
	buffer_load_dwordx4 v193, s[20:23], s37 offen lds
	s_waitcnt lgkmcnt(3)
	v_mfma_f32_16x16x32_bf16 v[164:167], v[198:201], v[206:209], v[164:167]
	s_add_i32 s37, s17, 0xfff20000
	s_waitcnt lgkmcnt(2)
	v_mfma_f32_16x16x32_bf16 v[160:163], v[202:205], v[206:209], v[160:163]
	s_waitcnt lgkmcnt(1)
	v_mfma_f32_16x16x32_bf16 v[156:159], v[176:179], v[210:213], v[156:159]
	ds_read_b128 v[206:209], v186 offset:6144
	s_waitcnt vmcnt(12)
	v_cvt_pk_bf16_f32 v15, v14, v15
	v_cvt_pk_bf16_f32 v14, v12, v13
	v_mfma_f32_16x16x32_bf16 v[152:155], v[180:183], v[210:213], v[152:155]
	ds_write_b64 v185, v[14:15] offset:34816
	v_mfma_f32_16x16x32_bf16 v[148:151], v[198:201], v[210:213], v[148:151]
	v_mfma_f32_16x16x32_bf16 v[144:147], v[202:205], v[210:213], v[144:147]
	s_waitcnt lgkmcnt(2)
	v_mfma_f32_16x16x32_bf16 v[132:135], v[176:179], v[214:217], v[132:135]
	ds_read_b128 v[210:213], v186 offset:8192
	v_mfma_f32_16x16x32_bf16 v[124:127], v[180:183], v[214:217], v[124:127]
	v_mfma_f32_16x16x32_bf16 v[120:123], v[198:201], v[214:217], v[120:123]
	v_mfma_f32_16x16x32_bf16 v[140:143], v[202:205], v[214:217], v[140:143]
	s_waitcnt lgkmcnt(2)
	v_mfma_f32_16x16x32_bf16 v[136:139], v[176:179], v[206:209], v[136:139]
	ds_read_b128 v[214:217], v186 offset:10240
	buffer_load_dwordx4 v[12:15], v184, s[24:27], s37 offen
	s_waitcnt vmcnt(12)
	v_cvt_pk_bf16_f32 v3, v2, v3
	v_cvt_pk_bf16_f32 v2, v0, v1
	v_mfma_f32_16x16x32_bf16 v[128:131], v[180:183], v[206:209], v[128:131]
	ds_write_b64 v185, v[2:3] offset:43520
	v_mfma_f32_16x16x32_bf16 v[116:119], v[198:201], v[206:209], v[116:119]
	v_mfma_f32_16x16x32_bf16 v[112:115], v[202:205], v[206:209], v[112:115]
	s_add_i32 s38, s17, 0xfff40000
	s_waitcnt lgkmcnt(2)
	v_mfma_f32_16x16x32_bf16 v[100:103], v[176:179], v[210:213], v[100:103]
	ds_read_b128 v[206:209], v186 offset:12288
	v_mfma_f32_16x16x32_bf16 v[92:95], v[180:183], v[210:213], v[92:95]
	v_mfma_f32_16x16x32_bf16 v[88:91], v[198:201], v[210:213], v[88:91]
	v_mfma_f32_16x16x32_bf16 v[108:111], v[202:205], v[210:213], v[108:111]
	s_waitcnt lgkmcnt(2)
	v_mfma_f32_16x16x32_bf16 v[104:107], v[176:179], v[214:217], v[104:107]
	ds_read_b128 v[210:213], v186 offset:14336
	buffer_load_dwordx4 v[0:3], v184, s[24:27], s38 offen
	s_waitcnt vmcnt(12)
	v_cvt_pk_bf16_f32 v31, v30, v31
	v_cvt_pk_bf16_f32 v30, v28, v29
	v_mfma_f32_16x16x32_bf16 v[96:99], v[180:183], v[214:217], v[96:99]
	ds_write_b64 v185, v[30:31] offset:52224
	v_mfma_f32_16x16x32_bf16 v[84:87], v[198:201], v[214:217], v[84:87]
	v_mfma_f32_16x16x32_bf16 v[80:83], v[202:205], v[214:217], v[80:83]
	s_add_i32 s39, s17, 0xfff60000
	s_waitcnt lgkmcnt(2)
	v_mfma_f32_16x16x32_bf16 v[72:75], v[176:179], v[206:209], v[72:75]
	ds_read_b128 v[214:217], v186 offset:16384
	v_mfma_f32_16x16x32_bf16 v[64:67], v[180:183], v[206:209], v[64:67]
	v_mfma_f32_16x16x32_bf16 v[60:63], v[198:201], v[206:209], v[60:63]
	v_mfma_f32_16x16x32_bf16 v[76:79], v[202:205], v[206:209], v[76:79]
	s_waitcnt lgkmcnt(2)
	v_mfma_f32_16x16x32_bf16 v[68:71], v[176:179], v[210:213], v[68:71]
	ds_read_b128 v[206:209], v186 offset:1024
	buffer_load_dwordx4 v[28:31], v184, s[24:27], s39 offen
	s_waitcnt vmcnt(12)
	v_cvt_pk_bf16_f32 v27, v26, v27
	v_cvt_pk_bf16_f32 v26, v24, v25
	v_mfma_f32_16x16x32_bf16 v[56:59], v[180:183], v[210:213], v[56:59]
	ds_write_b64 v185, v[26:27] offset:60928
	v_mfma_f32_16x16x32_bf16 v[52:55], v[198:201], v[210:213], v[52:55]
	v_mfma_f32_16x16x32_bf16 v[48:51], v[202:205], v[210:213], v[48:51]
	s_add_i32 s42, s17, 0xfff80000
	ds_read_b128 v[210:213], v186 offset:3072
	s_waitcnt lgkmcnt(3)
	v_mfma_f32_16x16x32_bf16 v[44:47], v[176:179], v[214:217], v[44:47]
	ds_read_b64_tr_b16 v[246:247], v188 offset:17408
	ds_read_b64_tr_b16 v[220:221], v188 offset:17440
	ds_read_b64_tr_b16 v[244:245], v187 offset:17408
	ds_read_b64_tr_b16 v[218:219], v187 offset:17440
	v_mfma_f32_16x16x32_bf16 v[40:43], v[180:183], v[214:217], v[40:43]
	ds_read_b64_tr_b16 v[248:249], v187 offset:17472
	ds_read_b64_tr_b16 v[250:251], v188 offset:17472
	v_mfma_f32_16x16x32_bf16 v[36:39], v[198:201], v[214:217], v[36:39]
	ds_read_b64_tr_b16 v[252:253], v187 offset:17504
	ds_read_b64_tr_b16 v[254:255], v188 offset:17504
	v_mfma_f32_16x16x32_bf16 v[32:35], v[202:205], v[214:217], v[32:35]
	s_waitcnt lgkmcnt(5)
; #define G_DMA_A(kt, AO) do { G_DMA1(kt, AO, 0); G_DMA1(kt, AO, 1); G_DMA1(kt, AO, 2); G_DMA1(kt, AO, 3); if (MF == 9) G_DMA5(kt, AO); } while (0)
; #define G_ISSUE_B(kt) do { const unsigned _sb = (unsigned)(kt) * 4u * kstepB; \
;         _Pragma("unroll") for (int _i = 0; _i < 8; ++_i) sb[_i] = bload16(_i < 4 ? rsB0 : rsB1, vob, _sb + (_i & 3) * kstepB); } while (0)
; #define G_WRITE_B(BO) do { \
;         _Pragma("unroll") for (int _i = 0; _i < 8; ++_i) *(LAS u32x2*)(b_wr + (BO) + (_i & 3) * (16 * G_BSTRIDE) + (_i >> 2) * SLAB1) = pack4(__builtin_bit_cast(f32x4, sb[_i])); } while (0)
; #define G_ENDTILE(VM) do { asm volatile("s_waitcnt vmcnt(" #VM ")" ::: "memory"); \
;         asm volatile("s_waitcnt lgkmcnt(0)" ::: "memory"); __builtin_amdgcn_s_barrier(); asm volatile("" ::: "memory"); } while (0)
;     ...
;     __builtin_amdgcn_s_barrier();
;     G_DMA_A(0, G_A0); G_ISSUE_B(0); G_WRITE_B(G_B0);
;     __builtin_amdgcn_sched_barrier(0);
;     G_ISSUE_B(1);
;     __builtin_amdgcn_sched_barrier(0);
;     G_ENDTILE(8);
;     for (int ui = 0;; ++ui) {
; #pragma unroll
;         for (int m = 0; m < MF; ++m)
; #pragma unroll
;             for (int n = 0; n < 4; ++n) acc[m][n] = (f32x4){0.f, 0.f, 0.f, 0.f};
;         for (int t = 0; t < nt - 2; t += 2) {
;             G_TILE(G_A0, G_B0, true, G_B1, G_A1, t + 1, true, t + 2, (void)0);
;             G_ENDTILE(8);
;             G_TILE(G_A1, G_B1, true, G_B0, G_A0, t + 2, true, t + 3, (void)0);
;             G_ENDTILE(8);
;         }
	v_mfma_f32_16x16x32_bf16 v[172:175], v[244:247], v[206:209], v[172:175]
	ds_read_b128 v[202:205], v186 offset:5120
	buffer_load_dwordx4 v[24:27], v184, s[24:27], s42 offen
	s_waitcnt vmcnt(12)
	v_cvt_pk_bf16_f32 v23, v22, v23
	v_cvt_pk_bf16_f32 v22, v20, v21
	s_waitcnt lgkmcnt(5)
	v_mfma_f32_16x16x32_bf16 v[168:171], v[218:221], v[206:209], v[168:171]
	ds_write_b64 v185, v[22:23] offset:34880
	s_waitcnt lgkmcnt(4)
	v_mfma_f32_16x16x32_bf16 v[164:167], v[248:251], v[206:209], v[164:167]
	s_waitcnt lgkmcnt(2)
	v_mfma_f32_16x16x32_bf16 v[160:163], v[252:255], v[206:209], v[160:163]
	v_mfma_f32_16x16x32_bf16 v[156:159], v[244:247], v[210:213], v[156:159]
	ds_read_b128 v[206:209], v186 offset:7168
	v_mfma_f32_16x16x32_bf16 v[152:155], v[218:221], v[210:213], v[152:155]
	v_mfma_f32_16x16x32_bf16 v[148:151], v[248:251], v[210:213], v[148:151]
	v_mfma_f32_16x16x32_bf16 v[144:147], v[252:255], v[210:213], v[144:147]
	s_waitcnt lgkmcnt(2)
	v_mfma_f32_16x16x32_bf16 v[132:135], v[244:247], v[202:205], v[132:135]
	ds_read_b128 v[210:213], v186 offset:9216
	buffer_load_dwordx4 v[20:23], v184, s[28:31], s37 offen
	s_waitcnt vmcnt(12)
	v_cvt_pk_bf16_f32 v7, v6, v7
	v_cvt_pk_bf16_f32 v6, v4, v5
	v_mfma_f32_16x16x32_bf16 v[124:127], v[218:221], v[202:205], v[124:127]
	ds_write_b64 v185, v[6:7] offset:43584
	v_mfma_f32_16x16x32_bf16 v[120:123], v[248:251], v[202:205], v[120:123]
	v_mfma_f32_16x16x32_bf16 v[140:143], v[252:255], v[202:205], v[140:143]
	s_waitcnt lgkmcnt(2)
	v_mfma_f32_16x16x32_bf16 v[136:139], v[244:247], v[206:209], v[136:139]
	ds_read_b128 v[202:205], v186 offset:11264
	v_mfma_f32_16x16x32_bf16 v[128:131], v[218:221], v[206:209], v[128:131]
	v_mfma_f32_16x16x32_bf16 v[116:119], v[248:251], v[206:209], v[116:119]
	v_mfma_f32_16x16x32_bf16 v[112:115], v[252:255], v[206:209], v[112:115]
	s_waitcnt lgkmcnt(2)
	v_mfma_f32_16x16x32_bf16 v[100:103], v[244:247], v[210:213], v[100:103]
	ds_read_b128 v[206:209], v186 offset:13312
	buffer_load_dwordx4 v[4:7], v184, s[28:31], s38 offen
	s_waitcnt vmcnt(12)
	v_cvt_pk_bf16_f32 v11, v10, v11
	v_cvt_pk_bf16_f32 v10, v8, v9
	v_mfma_f32_16x16x32_bf16 v[92:95], v[218:221], v[210:213], v[92:95]
	ds_write_b64 v185, v[10:11] offset:52288
	v_mfma_f32_16x16x32_bf16 v[88:91], v[248:251], v[210:213], v[88:91]
	v_mfma_f32_16x16x32_bf16 v[108:111], v[252:255], v[210:213], v[108:111]
	s_waitcnt lgkmcnt(2)
	v_mfma_f32_16x16x32_bf16 v[104:107], v[244:247], v[202:205], v[104:107]
	ds_read_b128 v[210:213], v186 offset:15360
	v_mfma_f32_16x16x32_bf16 v[96:99], v[218:221], v[202:205], v[96:99]
	v_mfma_f32_16x16x32_bf16 v[84:87], v[248:251], v[202:205], v[84:87]
	v_mfma_f32_16x16x32_bf16 v[80:83], v[252:255], v[202:205], v[80:83]
	s_waitcnt lgkmcnt(2)
	v_mfma_f32_16x16x32_bf16 v[72:75], v[244:247], v[206:209], v[72:75]
	ds_read_b128 v[238:241], v186 offset:17408
	buffer_load_dwordx4 v[8:11], v184, s[28:31], s39 offen
	s_waitcnt vmcnt(12)
	v_cvt_pk_bf16_f32 v19, v18, v19
	v_cvt_pk_bf16_f32 v18, v16, v17
	v_mfma_f32_16x16x32_bf16 v[64:67], v[218:221], v[206:209], v[64:67]
	ds_write_b64 v185, v[18:19] offset:60992
	v_mfma_f32_16x16x32_bf16 v[60:63], v[248:251], v[206:209], v[60:63]
	v_mfma_f32_16x16x32_bf16 v[76:79], v[252:255], v[206:209], v[76:79]
	s_waitcnt lgkmcnt(2)
	v_mfma_f32_16x16x32_bf16 v[68:71], v[244:247], v[210:213], v[68:71]
	v_mfma_f32_16x16x32_bf16 v[56:59], v[218:221], v[210:213], v[56:59]
	v_mfma_f32_16x16x32_bf16 v[52:55], v[248:251], v[210:213], v[52:55]
	v_mfma_f32_16x16x32_bf16 v[48:51], v[252:255], v[210:213], v[48:51]
	s_waitcnt lgkmcnt(1)
	buffer_load_dwordx4 v[16:19], v184, s[28:31], s42 offen
	s_waitcnt vmcnt(8)
	s_mov_b32 m0, s46
	s_waitcnt lgkmcnt(0)
	s_barrier
	ds_read_b64_tr_b16 v[178:179], v188 offset:34816
	ds_read_b64_tr_b16 v[176:177], v187 offset:34816
	ds_read_b64_tr_b16 v[180:181], v187 offset:34848
	ds_read_b64_tr_b16 v[198:199], v187 offset:34880
	ds_read_b64_tr_b16 v[202:203], v187 offset:34912
	ds_read_b128 v[206:209], v186 offset:36864
	ds_read_b64_tr_b16 v[182:183], v188 offset:34848
	ds_read_b64_tr_b16 v[200:201], v188 offset:34880
	ds_read_b64_tr_b16 v[204:205], v188 offset:34912
	ds_read_b128 v[210:213], v186 offset:38912
	ds_read_b128 v[214:217], v186 offset:40960
	buffer_load_dwordx4 v189, s[20:23], s36 offen lds
	s_mov_b32 m0, s86
	v_mfma_f32_16x16x32_bf16 v[44:47], v[244:247], v[238:241], v[44:47]
	v_mfma_f32_16x16x32_bf16 v[40:43], v[218:221], v[238:241], v[40:43]
	v_mfma_f32_16x16x32_bf16 v[36:39], v[248:251], v[238:241], v[36:39]
	v_mfma_f32_16x16x32_bf16 v[32:35], v[252:255], v[238:241], v[32:35]
	s_waitcnt lgkmcnt(5)
	v_mfma_f32_16x16x32_bf16 v[172:175], v[176:179], v[206:209], v[172:175]
	buffer_load_dwordx4 v192, s[20:23], s36 offen lds
	s_mov_b32 m0, s89
	s_add_i32 s37, s17, 0xfffa0000
	buffer_load_dwordx4 v191, s[20:23], s36 offen lds
	s_mov_b32 m0, s90
	s_waitcnt lgkmcnt(4)
	v_mfma_f32_16x16x32_bf16 v[168:171], v[180:183], v[206:209], v[168:171]
	buffer_load_dwordx4 v190, s[20:23], s36 offen lds
	s_mov_b32 m0, s91
	s_nop 0
	buffer_load_dwordx4 v193, s[20:23], s36 offen lds
	s_waitcnt lgkmcnt(3)
	v_mfma_f32_16x16x32_bf16 v[164:167], v[198:201], v[206:209], v[164:167]
	s_waitcnt lgkmcnt(2)
	v_mfma_f32_16x16x32_bf16 v[160:163], v[202:205], v[206:209], v[160:163]
	s_waitcnt lgkmcnt(1)
	v_mfma_f32_16x16x32_bf16 v[156:159], v[176:179], v[210:213], v[156:159]
	ds_read_b128 v[206:209], v186 offset:43008
	s_waitcnt vmcnt(12)
	v_cvt_pk_bf16_f32 v15, v14, v15
	v_cvt_pk_bf16_f32 v14, v12, v13
	v_mfma_f32_16x16x32_bf16 v[152:155], v[180:183], v[210:213], v[152:155]
	ds_write_b64 v185, v[14:15]
	v_mfma_f32_16x16x32_bf16 v[148:151], v[198:201], v[210:213], v[148:151]
	v_mfma_f32_16x16x32_bf16 v[144:147], v[202:205], v[210:213], v[144:147]
	s_waitcnt lgkmcnt(2)
; #define G_DMA_A(kt, AO) do { G_DMA1(kt, AO, 0); G_DMA1(kt, AO, 1); G_DMA1(kt, AO, 2); G_DMA1(kt, AO, 3); if (MF == 9) G_DMA5(kt, AO); } while (0)
; #define G_ISSUE_B(kt) do { const unsigned _sb = (unsigned)(kt) * 4u * kstepB; \
;         _Pragma("unroll") for (int _i = 0; _i < 8; ++_i) sb[_i] = bload16(_i < 4 ? rsB0 : rsB1, vob, _sb + (_i & 3) * kstepB); } while (0)
; #define G_WRITE_B(BO) do { \
;         _Pragma("unroll") for (int _i = 0; _i < 8; ++_i) *(LAS u32x2*)(b_wr + (BO) + (_i & 3) * (16 * G_BSTRIDE) + (_i >> 2) * SLAB1) = pack4(__builtin_bit_cast(f32x4, sb[_i])); } while (0)
; #define G_ENDTILE(VM) do { asm volatile("s_waitcnt vmcnt(" #VM ")" ::: "memory"); \
;         asm volatile("s_waitcnt lgkmcnt(0)" ::: "memory"); __builtin_amdgcn_s_barrier(); asm volatile("" ::: "memory"); } while (0)
;     ...
;     __builtin_amdgcn_s_barrier();
;     G_DMA_A(0, G_A0); G_ISSUE_B(0); G_WRITE_B(G_B0);
;     __builtin_amdgcn_sched_barrier(0);
;     G_ISSUE_B(1);
;     __builtin_amdgcn_sched_barrier(0);
;     G_ENDTILE(8);
;     for (int ui = 0;; ++ui) {
; #pragma unroll
;         for (int m = 0; m < MF; ++m)
; #pragma unroll
;             for (int n = 0; n < 4; ++n) acc[m][n] = (f32x4){0.f, 0.f, 0.f, 0.f};
;         for (int t = 0; t < nt - 2; t += 2) {
;             G_TILE(G_A0, G_B0, true, G_B1, G_A1, t + 1, true, t + 2, (void)0);
;             G_ENDTILE(8);
;             G_TILE(G_A1, G_B1, true, G_B0, G_A0, t + 2, true, t + 3, (void)0);
;             G_ENDTILE(8);
;         }
	v_mfma_f32_16x16x32_bf16 v[132:135], v[176:179], v[214:217], v[132:135]
	ds_read_b128 v[210:213], v186 offset:45056
	v_mfma_f32_16x16x32_bf16 v[124:127], v[180:183], v[214:217], v[124:127]
	v_mfma_f32_16x16x32_bf16 v[120:123], v[198:201], v[214:217], v[120:123]
	v_mfma_f32_16x16x32_bf16 v[140:143], v[202:205], v[214:217], v[140:143]
	s_waitcnt lgkmcnt(2)
	v_mfma_f32_16x16x32_bf16 v[136:139], v[176:179], v[206:209], v[136:139]
	ds_read_b128 v[214:217], v186 offset:47104
	buffer_load_dwordx4 v[12:15], v184, s[24:27], s37 offen
	s_waitcnt vmcnt(12)
	v_cvt_pk_bf16_f32 v3, v2, v3
	v_cvt_pk_bf16_f32 v2, v0, v1
	v_mfma_f32_16x16x32_bf16 v[128:131], v[180:183], v[206:209], v[128:131]
	ds_write_b64 v185, v[2:3] offset:8704
	v_mfma_f32_16x16x32_bf16 v[116:119], v[198:201], v[206:209], v[116:119]
	v_mfma_f32_16x16x32_bf16 v[112:115], v[202:205], v[206:209], v[112:115]
	s_add_i32 s38, s17, 0xfffc0000
	s_waitcnt lgkmcnt(2)
	v_mfma_f32_16x16x32_bf16 v[100:103], v[176:179], v[210:213], v[100:103]
	ds_read_b128 v[206:209], v186 offset:49152
	v_mfma_f32_16x16x32_bf16 v[92:95], v[180:183], v[210:213], v[92:95]
	v_mfma_f32_16x16x32_bf16 v[88:91], v[198:201], v[210:213], v[88:91]
	v_mfma_f32_16x16x32_bf16 v[108:111], v[202:205], v[210:213], v[108:111]
	s_waitcnt lgkmcnt(2)
	v_mfma_f32_16x16x32_bf16 v[104:107], v[176:179], v[214:217], v[104:107]
	ds_read_b128 v[210:213], v186 offset:51200
	buffer_load_dwordx4 v[0:3], v184, s[24:27], s38 offen
	s_waitcnt vmcnt(12)
	v_cvt_pk_bf16_f32 v31, v30, v31
	v_cvt_pk_bf16_f32 v30, v28, v29
	v_mfma_f32_16x16x32_bf16 v[96:99], v[180:183], v[214:217], v[96:99]
	ds_write_b64 v185, v[30:31] offset:17408
	v_mfma_f32_16x16x32_bf16 v[84:87], v[198:201], v[214:217], v[84:87]
	v_mfma_f32_16x16x32_bf16 v[80:83], v[202:205], v[214:217], v[80:83]
	s_add_i32 s39, s17, 0xfffe0000
	s_waitcnt lgkmcnt(2)
	v_mfma_f32_16x16x32_bf16 v[72:75], v[176:179], v[206:209], v[72:75]
	ds_read_b128 v[214:217], v186 offset:53248
	v_mfma_f32_16x16x32_bf16 v[64:67], v[180:183], v[206:209], v[64:67]
	v_mfma_f32_16x16x32_bf16 v[60:63], v[198:201], v[206:209], v[60:63]
	v_mfma_f32_16x16x32_bf16 v[76:79], v[202:205], v[206:209], v[76:79]
	s_waitcnt lgkmcnt(2)
	v_mfma_f32_16x16x32_bf16 v[68:71], v[176:179], v[210:213], v[68:71]
	ds_read_b128 v[206:209], v186 offset:37888
	buffer_load_dwordx4 v[28:31], v184, s[24:27], s39 offen
	s_waitcnt vmcnt(12)
	v_cvt_pk_bf16_f32 v27, v26, v27
	v_cvt_pk_bf16_f32 v26, v24, v25
	v_mfma_f32_16x16x32_bf16 v[56:59], v[180:183], v[210:213], v[56:59]
	ds_write_b64 v185, v[26:27] offset:26112
	v_mfma_f32_16x16x32_bf16 v[52:55], v[198:201], v[210:213], v[52:55]
	v_mfma_f32_16x16x32_bf16 v[48:51], v[202:205], v[210:213], v[48:51]
	ds_read_b128 v[210:213], v186 offset:39936
	s_waitcnt lgkmcnt(3)
	v_mfma_f32_16x16x32_bf16 v[44:47], v[176:179], v[214:217], v[44:47]
	ds_read_b64_tr_b16 v[246:247], v188 offset:52224
	ds_read_b64_tr_b16 v[220:221], v188 offset:52256
	ds_read_b64_tr_b16 v[244:245], v187 offset:52224
	ds_read_b64_tr_b16 v[218:219], v187 offset:52256
	v_mfma_f32_16x16x32_bf16 v[40:43], v[180:183], v[214:217], v[40:43]
	ds_read_b64_tr_b16 v[248:249], v187 offset:52288
	ds_read_b64_tr_b16 v[250:251], v188 offset:52288
	v_mfma_f32_16x16x32_bf16 v[36:39], v[198:201], v[214:217], v[36:39]
	ds_read_b64_tr_b16 v[252:253], v187 offset:52320
	ds_read_b64_tr_b16 v[254:255], v188 offset:52320
	v_mfma_f32_16x16x32_bf16 v[32:35], v[202:205], v[214:217], v[32:35]
	s_waitcnt lgkmcnt(5)
	v_mfma_f32_16x16x32_bf16 v[172:175], v[244:247], v[206:209], v[172:175]
	ds_read_b128 v[202:205], v186 offset:41984
	buffer_load_dwordx4 v[24:27], v184, s[24:27], s17 offen
	s_waitcnt vmcnt(12)
	v_cvt_pk_bf16_f32 v23, v22, v23
	v_cvt_pk_bf16_f32 v22, v20, v21
	s_waitcnt lgkmcnt(5)
; #define G_DMA_A(kt, AO) do { G_DMA1(kt, AO, 0); G_DMA1(kt, AO, 1); G_DMA1(kt, AO, 2); G_DMA1(kt, AO, 3); if (MF == 9) G_DMA5(kt, AO); } while (0)
; #define G_ISSUE_B(kt) do { const unsigned _sb = (unsigned)(kt) * 4u * kstepB; \
;         _Pragma("unroll") for (int _i = 0; _i < 8; ++_i) sb[_i] = bload16(_i < 4 ? rsB0 : rsB1, vob, _sb + (_i & 3) * kstepB); } while (0)
; #define G_WRITE_B(BO) do { \
;         _Pragma("unroll") for (int _i = 0; _i < 8; ++_i) *(LAS u32x2*)(b_wr + (BO) + (_i & 3) * (16 * G_BSTRIDE) + (_i >> 2) * SLAB1) = pack4(__builtin_bit_cast(f32x4, sb[_i])); } while (0)
; #define G_ENDTILE(VM) do { asm volatile("s_waitcnt vmcnt(" #VM ")" ::: "memory"); \
;         asm volatile("s_waitcnt lgkmcnt(0)" ::: "memory"); __builtin_amdgcn_s_barrier(); asm volatile("" ::: "memory"); } while (0)
;     ...
;     __builtin_amdgcn_s_barrier();
;     G_DMA_A(0, G_A0); G_ISSUE_B(0); G_WRITE_B(G_B0);
;     __builtin_amdgcn_sched_barrier(0);
;     G_ISSUE_B(1);
;     __builtin_amdgcn_sched_barrier(0);
;     G_ENDTILE(8);
;     for (int ui = 0;; ++ui) {
; #pragma unroll
;         for (int m = 0; m < MF; ++m)
; #pragma unroll
;             for (int n = 0; n < 4; ++n) acc[m][n] = (f32x4){0.f, 0.f, 0.f, 0.f};
;         for (int t = 0; t < nt - 2; t += 2) {
;             G_TILE(G_A0, G_B0, true, G_B1, G_A1, t + 1, true, t + 2, (void)0);
;             G_ENDTILE(8);
;             G_TILE(G_A1, G_B1, true, G_B0, G_A0, t + 2, true, t + 3, (void)0);
;             G_ENDTILE(8);
;         }
	v_mfma_f32_16x16x32_bf16 v[168:171], v[218:221], v[206:209], v[168:171]
	ds_write_b64 v185, v[22:23] offset:64
	s_waitcnt lgkmcnt(4)
	v_mfma_f32_16x16x32_bf16 v[164:167], v[248:251], v[206:209], v[164:167]
	s_waitcnt lgkmcnt(2)
	v_mfma_f32_16x16x32_bf16 v[160:163], v[252:255], v[206:209], v[160:163]
	v_mfma_f32_16x16x32_bf16 v[156:159], v[244:247], v[210:213], v[156:159]
	ds_read_b128 v[206:209], v186 offset:44032
	v_mfma_f32_16x16x32_bf16 v[152:155], v[218:221], v[210:213], v[152:155]
	v_mfma_f32_16x16x32_bf16 v[148:151], v[248:251], v[210:213], v[148:151]
	v_mfma_f32_16x16x32_bf16 v[144:147], v[252:255], v[210:213], v[144:147]
	s_waitcnt lgkmcnt(2)
	v_mfma_f32_16x16x32_bf16 v[132:135], v[244:247], v[202:205], v[132:135]
	ds_read_b128 v[210:213], v186 offset:46080
	buffer_load_dwordx4 v[20:23], v184, s[28:31], s37 offen
	s_waitcnt vmcnt(12)
	v_cvt_pk_bf16_f32 v7, v6, v7
	v_cvt_pk_bf16_f32 v6, v4, v5
	v_mfma_f32_16x16x32_bf16 v[124:127], v[218:221], v[202:205], v[124:127]
	ds_write_b64 v185, v[6:7] offset:8768
	v_mfma_f32_16x16x32_bf16 v[120:123], v[248:251], v[202:205], v[120:123]
	v_mfma_f32_16x16x32_bf16 v[140:143], v[252:255], v[202:205], v[140:143]
	s_waitcnt lgkmcnt(2)
	v_mfma_f32_16x16x32_bf16 v[136:139], v[244:247], v[206:209], v[136:139]
	ds_read_b128 v[202:205], v186 offset:48128
	v_mfma_f32_16x16x32_bf16 v[128:131], v[218:221], v[206:209], v[128:131]
	v_mfma_f32_16x16x32_bf16 v[116:119], v[248:251], v[206:209], v[116:119]
	v_mfma_f32_16x16x32_bf16 v[112:115], v[252:255], v[206:209], v[112:115]
	s_waitcnt lgkmcnt(2)
	v_mfma_f32_16x16x32_bf16 v[100:103], v[244:247], v[210:213], v[100:103]
	ds_read_b128 v[206:209], v186 offset:50176
	buffer_load_dwordx4 v[4:7], v184, s[28:31], s38 offen
	s_waitcnt vmcnt(12)
	v_cvt_pk_bf16_f32 v11, v10, v11
	v_cvt_pk_bf16_f32 v10, v8, v9
	v_mfma_f32_16x16x32_bf16 v[92:95], v[218:221], v[210:213], v[92:95]
	ds_write_b64 v185, v[10:11] offset:17472
	v_mfma_f32_16x16x32_bf16 v[88:91], v[248:251], v[210:213], v[88:91]
	v_mfma_f32_16x16x32_bf16 v[108:111], v[252:255], v[210:213], v[108:111]
	s_waitcnt lgkmcnt(2)
	v_mfma_f32_16x16x32_bf16 v[104:107], v[244:247], v[202:205], v[104:107]
	ds_read_b128 v[210:213], v186 offset:52224
	v_mfma_f32_16x16x32_bf16 v[96:99], v[218:221], v[202:205], v[96:99]
	v_mfma_f32_16x16x32_bf16 v[84:87], v[248:251], v[202:205], v[84:87]
	v_mfma_f32_16x16x32_bf16 v[80:83], v[252:255], v[202:205], v[80:83]
	s_waitcnt lgkmcnt(2)
	v_mfma_f32_16x16x32_bf16 v[72:75], v[244:247], v[206:209], v[72:75]
	ds_read_b128 v[238:241], v186 offset:54272
	buffer_load_dwordx4 v[8:11], v184, s[28:31], s39 offen
	s_waitcnt vmcnt(12)
	v_cvt_pk_bf16_f32 v19, v18, v19
	v_cvt_pk_bf16_f32 v18, v16, v17
	v_mfma_f32_16x16x32_bf16 v[64:67], v[218:221], v[206:209], v[64:67]
	ds_write_b64 v185, v[18:19] offset:26176
	v_mfma_f32_16x16x32_bf16 v[60:63], v[248:251], v[206:209], v[60:63]
	v_mfma_f32_16x16x32_bf16 v[76:79], v[252:255], v[206:209], v[76:79]
	s_waitcnt lgkmcnt(2)
	v_mfma_f32_16x16x32_bf16 v[68:71], v[244:247], v[210:213], v[68:71]
	v_mfma_f32_16x16x32_bf16 v[56:59], v[218:221], v[210:213], v[56:59]
	v_mfma_f32_16x16x32_bf16 v[52:55], v[248:251], v[210:213], v[52:55]
	v_mfma_f32_16x16x32_bf16 v[48:51], v[252:255], v[210:213], v[48:51]
	s_waitcnt lgkmcnt(1)
	buffer_load_dwordx4 v[16:19], v184, s[28:31], s17 offen
	s_waitcnt vmcnt(8)
	s_waitcnt lgkmcnt(0)
	s_barrier
	s_add_i32 s16, s16, 2
	s_add_i32 s17, s17, 0x100000
	s_addk_i32 s36, 0x100
	s_cmp_ge_i32 s16, s97
	s_cbranch_scc0 .LBB0_651
	v_mfma_f32_16x16x32_bf16 v[44:47], v[244:247], v[238:241], v[44:47]
	v_mfma_f32_16x16x32_bf16 v[40:43], v[218:221], v[238:241], v[40:43]
	v_mfma_f32_16x16x32_bf16 v[36:39], v[248:251], v[238:241], v[36:39]
	v_mfma_f32_16x16x32_bf16 v[32:35], v[252:255], v[238:241], v[32:35]
	s_branch .LBB0_653

; #define G_DMA_A(kt, AO) do { G_DMA1(kt, AO, 0); G_DMA1(kt, AO, 1); G_DMA1(kt, AO, 2); G_DMA1(kt, AO, 3); if (MF == 9) G_DMA5(kt, AO); } while (0)
; #define G_ISSUE_B(kt) do { const unsigned _sb = (unsigned)(kt) * 4u * kstepB; \
;         _Pragma("unroll") for (int _i = 0; _i < 8; ++_i) sb[_i] = bload16(_i < 4 ? rsB0 : rsB1, vob, _sb + (_i & 3) * kstepB); } while (0)
; #define G_WRITE_B(BO) do { \
;         _Pragma("unroll") for (int _i = 0; _i < 8; ++_i) *(LAS u32x2*)(b_wr + (BO) + (_i & 3) * (16 * G_BSTRIDE) + (_i >> 2) * SLAB1) = pack4(__builtin_bit_cast(f32x4, sb[_i])); } while (0)
; #define G_ENDTILE(VM) do { asm volatile("s_waitcnt vmcnt(" #VM ")" ::: "memory"); \
;         asm volatile("s_waitcnt lgkmcnt(0)" ::: "memory"); __builtin_amdgcn_s_barrier(); asm volatile("" ::: "memory"); } while (0)
;     ...
;     __builtin_amdgcn_s_barrier();
;     G_DMA_A(0, G_A0); G_ISSUE_B(0); G_WRITE_B(G_B0);
;     __builtin_amdgcn_sched_barrier(0);
;     G_ISSUE_B(1);
;     __builtin_amdgcn_sched_barrier(0);
;     G_ENDTILE(8);
;     for (int ui = 0;; ++ui) {
; #pragma unroll
;         for (int m = 0; m < MF; ++m)
; #pragma unroll
;             for (int n = 0; n < 4; ++n) acc[m][n] = (f32x4){0.f, 0.f, 0.f, 0.f};
;         for (int t = 0; t < nt - 2; t += 2) {
;             G_TILE(G_A0, G_B0, true, G_B1, G_A1, t + 1, true, t + 2, (void)0);
;             G_ENDTILE(8);
;             G_TILE(G_A1, G_B1, true, G_B0, G_A0, t + 2, true, t + 3, (void)0);
;             G_ENDTILE(8);
;         }
.Lchk5_s3:
	ds_read_b128 v[206:209], v186 offset:6144
	v_cvt_pk_bf16_f32 v15, v14, v15
	v_cvt_pk_bf16_f32 v14, v12, v13
	ds_write_b64 v185, v[14:15] offset:34816
	s_waitcnt lgkmcnt(2)
	s_cmp_le_u32 s99, 2
	s_cbranch_scc1 .Lchk5_s4
	v_mfma_f32_16x16x32_bf16 v[132:135], v[176:179], v[214:217], v[132:135]
	v_mfma_f32_16x16x32_bf16 v[124:127], v[180:183], v[214:217], v[124:127]
	v_mfma_f32_16x16x32_bf16 v[120:123], v[198:201], v[214:217], v[120:123]
	v_mfma_f32_16x16x32_bf16 v[140:143], v[202:205], v[214:217], v[140:143]
.Lchk5_s4:
	ds_read_b128 v[210:213], v186 offset:8192
	s_waitcnt lgkmcnt(2)
	s_waitcnt vmcnt(11)
	s_cmp_le_u32 s99, 3
	s_cbranch_scc1 .Lchk5_s5
	v_mfma_f32_16x16x32_bf16 v[136:139], v[176:179], v[206:209], v[136:139]
	v_mfma_f32_16x16x32_bf16 v[128:131], v[180:183], v[206:209], v[128:131]
	v_mfma_f32_16x16x32_bf16 v[116:119], v[198:201], v[206:209], v[116:119]
	v_mfma_f32_16x16x32_bf16 v[112:115], v[202:205], v[206:209], v[112:115]
.Lchk5_s5:
	ds_read_b128 v[214:217], v186 offset:10240
	buffer_load_dwordx4 v[12:15], v184, s[24:27], s37 offen
	v_cvt_pk_bf16_f32 v3, v2, v3
	v_cvt_pk_bf16_f32 v2, v0, v1
	ds_write_b64 v185, v[2:3] offset:43520
	s_add_i32 s38, s17, 0xfff40000
	s_waitcnt lgkmcnt(2)
	s_cmp_le_u32 s99, 4
	s_cbranch_scc1 .Lchk5_s6
	v_mfma_f32_16x16x32_bf16 v[100:103], v[176:179], v[210:213], v[100:103]
	v_mfma_f32_16x16x32_bf16 v[92:95], v[180:183], v[210:213], v[92:95]
	v_mfma_f32_16x16x32_bf16 v[88:91], v[198:201], v[210:213], v[88:91]
	v_mfma_f32_16x16x32_bf16 v[108:111], v[202:205], v[210:213], v[108:111]
.Lchk5_s6:
	ds_read_b128 v[206:209], v186 offset:12288
	s_waitcnt lgkmcnt(2)
	s_waitcnt vmcnt(11)
	s_cmp_le_u32 s99, 5
	s_cbranch_scc1 .Lchk5_s7
	v_mfma_f32_16x16x32_bf16 v[104:107], v[176:179], v[214:217], v[104:107]
	v_mfma_f32_16x16x32_bf16 v[96:99], v[180:183], v[214:217], v[96:99]
	v_mfma_f32_16x16x32_bf16 v[84:87], v[198:201], v[214:217], v[84:87]
	v_mfma_f32_16x16x32_bf16 v[80:83], v[202:205], v[214:217], v[80:83]
.Lchk5_s7:
	ds_read_b128 v[210:213], v186 offset:14336
	buffer_load_dwordx4 v[0:3], v184, s[24:27], s38 offen
	v_cvt_pk_bf16_f32 v31, v30, v31
	v_cvt_pk_bf16_f32 v30, v28, v29
	ds_write_b64 v185, v[30:31] offset:52224
	s_add_i32 s39, s17, 0xfff60000
	s_waitcnt lgkmcnt(2)
	s_cmp_le_u32 s99, 6
	s_cbranch_scc1 .Lchk5_s8
	v_mfma_f32_16x16x32_bf16 v[72:75], v[176:179], v[206:209], v[72:75]
	v_mfma_f32_16x16x32_bf16 v[64:67], v[180:183], v[206:209], v[64:67]
	v_mfma_f32_16x16x32_bf16 v[60:63], v[198:201], v[206:209], v[60:63]
	v_mfma_f32_16x16x32_bf16 v[76:79], v[202:205], v[206:209], v[76:79]
.Lchk5_s8:
	ds_read_b128 v[214:217], v186 offset:16384
	s_waitcnt lgkmcnt(2)
	s_waitcnt vmcnt(11)
	s_cmp_le_u32 s99, 7
	s_cbranch_scc1 .Lchk5_s9
	v_mfma_f32_16x16x32_bf16 v[68:71], v[176:179], v[210:213], v[68:71]
	v_mfma_f32_16x16x32_bf16 v[56:59], v[180:183], v[210:213], v[56:59]
	v_mfma_f32_16x16x32_bf16 v[52:55], v[198:201], v[210:213], v[52:55]
	v_mfma_f32_16x16x32_bf16 v[48:51], v[202:205], v[210:213], v[48:51]
.Lchk5_s9:
	ds_read_b128 v[206:209], v186 offset:1024
	buffer_load_dwordx4 v[28:31], v184, s[24:27], s39 offen
	v_cvt_pk_bf16_f32 v27, v26, v27
	v_cvt_pk_bf16_f32 v26, v24, v25
	ds_write_b64 v185, v[26:27] offset:60928
	s_add_i32 s42, s17, 0xfff80000
	ds_read_b128 v[210:213], v186 offset:3072
	s_waitcnt lgkmcnt(3)
	s_cmp_le_u32 s99, 8
	s_cbranch_scc1 .Lchk5_s10
	v_mfma_f32_16x16x32_bf16 v[44:47], v[176:179], v[214:217], v[44:47]
	v_mfma_f32_16x16x32_bf16 v[40:43], v[180:183], v[214:217], v[40:43]
	v_mfma_f32_16x16x32_bf16 v[36:39], v[198:201], v[214:217], v[36:39]
	v_mfma_f32_16x16x32_bf16 v[32:35], v[202:205], v[214:217], v[32:35]
.Lchk5_s10:
	ds_read_b64_tr_b16 v[246:247], v188 offset:17408
	ds_read_b64_tr_b16 v[220:221], v188 offset:17440
	ds_read_b64_tr_b16 v[244:245], v187 offset:17408
	ds_read_b64_tr_b16 v[218:219], v187 offset:17440
	ds_read_b64_tr_b16 v[248:249], v187 offset:17472
	ds_read_b64_tr_b16 v[250:251], v188 offset:17472
	ds_read_b64_tr_b16 v[252:253], v187 offset:17504
	ds_read_b64_tr_b16 v[254:255], v188 offset:17504
	s_waitcnt lgkmcnt(5)
	s_waitcnt vmcnt(11)
	s_waitcnt lgkmcnt(4)
	s_waitcnt lgkmcnt(2)
	s_waitcnt lgkmcnt(0)
	s_cmp_le_u32 s99, 0
	s_cbranch_scc1 .Lchk5_s11
	v_mfma_f32_16x16x32_bf16 v[172:175], v[244:247], v[206:209], v[172:175]
	v_mfma_f32_16x16x32_bf16 v[168:171], v[218:221], v[206:209], v[168:171]
	v_mfma_f32_16x16x32_bf16 v[164:167], v[248:251], v[206:209], v[164:167]
	v_mfma_f32_16x16x32_bf16 v[160:163], v[252:255], v[206:209], v[160:163]
; #define G_DMA_A(kt, AO) do { G_DMA1(kt, AO, 0); G_DMA1(kt, AO, 1); G_DMA1(kt, AO, 2); G_DMA1(kt, AO, 3); if (MF == 9) G_DMA5(kt, AO); } while (0)
; #define G_ISSUE_B(kt) do { const unsigned _sb = (unsigned)(kt) * 4u * kstepB; \
;         _Pragma("unroll") for (int _i = 0; _i < 8; ++_i) sb[_i] = bload16(_i < 4 ? rsB0 : rsB1, vob, _sb + (_i & 3) * kstepB); } while (0)
; #define G_WRITE_B(BO) do { \
;         _Pragma("unroll") for (int _i = 0; _i < 8; ++_i) *(LAS u32x2*)(b_wr + (BO) + (_i & 3) * (16 * G_BSTRIDE) + (_i >> 2) * SLAB1) = pack4(__builtin_bit_cast(f32x4, sb[_i])); } while (0)
; #define G_ENDTILE(VM) do { asm volatile("s_waitcnt vmcnt(" #VM ")" ::: "memory"); \
;         asm volatile("s_waitcnt lgkmcnt(0)" ::: "memory"); __builtin_amdgcn_s_barrier(); asm volatile("" ::: "memory"); } while (0)
;     ...
;     __builtin_amdgcn_s_barrier();
;     G_DMA_A(0, G_A0); G_ISSUE_B(0); G_WRITE_B(G_B0);
;     __builtin_amdgcn_sched_barrier(0);
;     G_ISSUE_B(1);
;     __builtin_amdgcn_sched_barrier(0);
;     G_ENDTILE(8);
;     for (int ui = 0;; ++ui) {
; #pragma unroll
;         for (int m = 0; m < MF; ++m)
; #pragma unroll
;             for (int n = 0; n < 4; ++n) acc[m][n] = (f32x4){0.f, 0.f, 0.f, 0.f};
;         for (int t = 0; t < nt - 2; t += 2) {
;             G_TILE(G_A0, G_B0, true, G_B1, G_A1, t + 1, true, t + 2, (void)0);
;             G_ENDTILE(8);
;             G_TILE(G_A1, G_B1, true, G_B0, G_A0, t + 2, true, t + 3, (void)0);
;             G_ENDTILE(8);
;         }
.Lchk5_s11:
	ds_read_b128 v[202:205], v186 offset:5120
	buffer_load_dwordx4 v[24:27], v184, s[24:27], s42 offen
	v_cvt_pk_bf16_f32 v23, v22, v23
	v_cvt_pk_bf16_f32 v22, v20, v21
	ds_write_b64 v185, v[22:23] offset:34880
	s_cmp_le_u32 s99, 1
	s_cbranch_scc1 .Lchk5_s12
	v_mfma_f32_16x16x32_bf16 v[156:159], v[244:247], v[210:213], v[156:159]
	v_mfma_f32_16x16x32_bf16 v[152:155], v[218:221], v[210:213], v[152:155]
	v_mfma_f32_16x16x32_bf16 v[148:151], v[248:251], v[210:213], v[148:151]
	v_mfma_f32_16x16x32_bf16 v[144:147], v[252:255], v[210:213], v[144:147]
.Lchk5_s12:
	ds_read_b128 v[206:209], v186 offset:7168
	s_waitcnt lgkmcnt(2)
	s_waitcnt vmcnt(11)
	s_cmp_le_u32 s99, 2
	s_cbranch_scc1 .Lchk5_s13
	v_mfma_f32_16x16x32_bf16 v[132:135], v[244:247], v[202:205], v[132:135]
	v_mfma_f32_16x16x32_bf16 v[124:127], v[218:221], v[202:205], v[124:127]
	v_mfma_f32_16x16x32_bf16 v[120:123], v[248:251], v[202:205], v[120:123]
	v_mfma_f32_16x16x32_bf16 v[140:143], v[252:255], v[202:205], v[140:143]
.Lchk5_s13:
	ds_read_b128 v[210:213], v186 offset:9216
	buffer_load_dwordx4 v[20:23], v184, s[28:31], s37 offen
	v_cvt_pk_bf16_f32 v7, v6, v7
	v_cvt_pk_bf16_f32 v6, v4, v5
	ds_write_b64 v185, v[6:7] offset:43584
	s_waitcnt lgkmcnt(2)
	s_cmp_le_u32 s99, 3
	s_cbranch_scc1 .Lchk5_s14
	v_mfma_f32_16x16x32_bf16 v[136:139], v[244:247], v[206:209], v[136:139]
	v_mfma_f32_16x16x32_bf16 v[128:131], v[218:221], v[206:209], v[128:131]
	v_mfma_f32_16x16x32_bf16 v[116:119], v[248:251], v[206:209], v[116:119]
	v_mfma_f32_16x16x32_bf16 v[112:115], v[252:255], v[206:209], v[112:115]
.Lchk5_s14:
	ds_read_b128 v[202:205], v186 offset:11264
	s_waitcnt lgkmcnt(2)
	s_waitcnt vmcnt(11)
	s_cmp_le_u32 s99, 4
	s_cbranch_scc1 .Lchk5_s15
	v_mfma_f32_16x16x32_bf16 v[100:103], v[244:247], v[210:213], v[100:103]
	v_mfma_f32_16x16x32_bf16 v[92:95], v[218:221], v[210:213], v[92:95]
	v_mfma_f32_16x16x32_bf16 v[88:91], v[248:251], v[210:213], v[88:91]
	v_mfma_f32_16x16x32_bf16 v[108:111], v[252:255], v[210:213], v[108:111]
.Lchk5_s15:
	ds_read_b128 v[206:209], v186 offset:13312
	buffer_load_dwordx4 v[4:7], v184, s[28:31], s38 offen
	v_cvt_pk_bf16_f32 v11, v10, v11
	v_cvt_pk_bf16_f32 v10, v8, v9
	ds_write_b64 v185, v[10:11] offset:52288
	s_waitcnt lgkmcnt(2)
	s_cmp_le_u32 s99, 5
	s_cbranch_scc1 .Lchk5_s16
	v_mfma_f32_16x16x32_bf16 v[104:107], v[244:247], v[202:205], v[104:107]
	v_mfma_f32_16x16x32_bf16 v[96:99], v[218:221], v[202:205], v[96:99]
	v_mfma_f32_16x16x32_bf16 v[84:87], v[248:251], v[202:205], v[84:87]
	v_mfma_f32_16x16x32_bf16 v[80:83], v[252:255], v[202:205], v[80:83]
.Lchk5_s16:
	ds_read_b128 v[210:213], v186 offset:15360
	s_waitcnt lgkmcnt(2)
	s_waitcnt vmcnt(11)
	s_cmp_le_u32 s99, 6
	s_cbranch_scc1 .Lchk5_s17
	v_mfma_f32_16x16x32_bf16 v[72:75], v[244:247], v[206:209], v[72:75]
	v_mfma_f32_16x16x32_bf16 v[64:67], v[218:221], v[206:209], v[64:67]
	v_mfma_f32_16x16x32_bf16 v[60:63], v[248:251], v[206:209], v[60:63]
	v_mfma_f32_16x16x32_bf16 v[76:79], v[252:255], v[206:209], v[76:79]
.Lchk5_s17:
	ds_read_b128 v[238:241], v186 offset:17408
	buffer_load_dwordx4 v[8:11], v184, s[28:31], s39 offen
	v_cvt_pk_bf16_f32 v19, v18, v19
	v_cvt_pk_bf16_f32 v18, v16, v17
	ds_write_b64 v185, v[18:19] offset:60992
	s_waitcnt lgkmcnt(2)
	s_cmp_le_u32 s99, 7
	s_cbranch_scc1 .Lchk5_s18
	v_mfma_f32_16x16x32_bf16 v[68:71], v[244:247], v[210:213], v[68:71]
	v_mfma_f32_16x16x32_bf16 v[56:59], v[218:221], v[210:213], v[56:59]
	v_mfma_f32_16x16x32_bf16 v[52:55], v[248:251], v[210:213], v[52:55]
	v_mfma_f32_16x16x32_bf16 v[48:51], v[252:255], v[210:213], v[48:51]
.Lchk5_s18:
	s_waitcnt lgkmcnt(1)
	buffer_load_dwordx4 v[16:19], v184, s[28:31], s42 offen
	s_waitcnt vmcnt(8)
	s_mov_b32 m0, s46
	s_waitcnt lgkmcnt(0)
	s_barrier
	ds_read_b64_tr_b16 v[178:179], v188 offset:34816
	ds_read_b64_tr_b16 v[176:177], v187 offset:34816
	ds_read_b64_tr_b16 v[180:181], v187 offset:34848
	ds_read_b64_tr_b16 v[198:199], v187 offset:34880
	ds_read_b64_tr_b16 v[202:203], v187 offset:34912
	ds_read_b128 v[206:209], v186 offset:36864
	ds_read_b64_tr_b16 v[182:183], v188 offset:34848
	ds_read_b64_tr_b16 v[200:201], v188 offset:34880
	ds_read_b64_tr_b16 v[204:205], v188 offset:34912
	ds_read_b128 v[210:213], v186 offset:38912
	ds_read_b128 v[214:217], v186 offset:40960
	buffer_load_dwordx4 v189, s[20:23], s36 offen lds
	s_mov_b32 m0, s86
	s_cmp_le_u32 s99, 8
	s_cbranch_scc1 .Lchk5_s19
	v_mfma_f32_16x16x32_bf16 v[44:47], v[244:247], v[238:241], v[44:47]
	v_mfma_f32_16x16x32_bf16 v[40:43], v[218:221], v[238:241], v[40:43]
	v_mfma_f32_16x16x32_bf16 v[36:39], v[248:251], v[238:241], v[36:39]
	v_mfma_f32_16x16x32_bf16 v[32:35], v[252:255], v[238:241], v[32:35]

; #define G_DMA_A(kt, AO) do { G_DMA1(kt, AO, 0); G_DMA1(kt, AO, 1); G_DMA1(kt, AO, 2); G_DMA1(kt, AO, 3); if (MF == 9) G_DMA5(kt, AO); } while (0)
; #define G_ISSUE_B(kt) do { const unsigned _sb = (unsigned)(kt) * 4u * kstepB; \
;         _Pragma("unroll") for (int _i = 0; _i < 8; ++_i) sb[_i] = bload16(_i < 4 ? rsB0 : rsB1, vob, _sb + (_i & 3) * kstepB); } while (0)
; #define G_WRITE_B(BO) do { \
;         _Pragma("unroll") for (int _i = 0; _i < 8; ++_i) *(LAS u32x2*)(b_wr + (BO) + (_i & 3) * (16 * G_BSTRIDE) + (_i >> 2) * SLAB1) = pack4(__builtin_bit_cast(f32x4, sb[_i])); } while (0)
; #define G_ENDTILE(VM) do { asm volatile("s_waitcnt vmcnt(" #VM ")" ::: "memory"); \
;         asm volatile("s_waitcnt lgkmcnt(0)" ::: "memory"); __builtin_amdgcn_s_barrier(); asm volatile("" ::: "memory"); } while (0)
;     ...
;     __builtin_amdgcn_s_barrier();
;     G_DMA_A(0, G_A0); G_ISSUE_B(0); G_WRITE_B(G_B0);
;     __builtin_amdgcn_sched_barrier(0);
;     G_ISSUE_B(1);
;     __builtin_amdgcn_sched_barrier(0);
;     G_ENDTILE(8);
;     for (int ui = 0;; ++ui) {
; #pragma unroll
;         for (int m = 0; m < MF; ++m)
; #pragma unroll
;             for (int n = 0; n < 4; ++n) acc[m][n] = (f32x4){0.f, 0.f, 0.f, 0.f};
;         for (int t = 0; t < nt - 2; t += 2) {
;             G_TILE(G_A0, G_B0, true, G_B1, G_A1, t + 1, true, t + 2, (void)0);
;             G_ENDTILE(8);
;             G_TILE(G_A1, G_B1, true, G_B0, G_A0, t + 2, true, t + 3, (void)0);
;             G_ENDTILE(8);
;         }
.Lchk5_s21:
	ds_read_b128 v[206:209], v186 offset:43008
	v_cvt_pk_bf16_f32 v15, v14, v15
	v_cvt_pk_bf16_f32 v14, v12, v13
	ds_write_b64 v185, v[14:15]
	s_waitcnt lgkmcnt(2)
	s_cmp_le_u32 s99, 2
	s_cbranch_scc1 .Lchk5_s22
	v_mfma_f32_16x16x32_bf16 v[132:135], v[176:179], v[214:217], v[132:135]
	v_mfma_f32_16x16x32_bf16 v[124:127], v[180:183], v[214:217], v[124:127]
	v_mfma_f32_16x16x32_bf16 v[120:123], v[198:201], v[214:217], v[120:123]
	v_mfma_f32_16x16x32_bf16 v[140:143], v[202:205], v[214:217], v[140:143]
.Lchk5_s22:
	ds_read_b128 v[210:213], v186 offset:45056
	s_waitcnt lgkmcnt(2)
	s_waitcnt vmcnt(11)
	s_cmp_le_u32 s99, 3
	s_cbranch_scc1 .Lchk5_s23
	v_mfma_f32_16x16x32_bf16 v[136:139], v[176:179], v[206:209], v[136:139]
	v_mfma_f32_16x16x32_bf16 v[128:131], v[180:183], v[206:209], v[128:131]
	v_mfma_f32_16x16x32_bf16 v[116:119], v[198:201], v[206:209], v[116:119]
	v_mfma_f32_16x16x32_bf16 v[112:115], v[202:205], v[206:209], v[112:115]
.Lchk5_s23:
	ds_read_b128 v[214:217], v186 offset:47104
	buffer_load_dwordx4 v[12:15], v184, s[24:27], s37 offen
	v_cvt_pk_bf16_f32 v3, v2, v3
	v_cvt_pk_bf16_f32 v2, v0, v1
	ds_write_b64 v185, v[2:3] offset:8704
	s_add_i32 s38, s17, 0xfffc0000
	s_waitcnt lgkmcnt(2)
	s_cmp_le_u32 s99, 4
	s_cbranch_scc1 .Lchk5_s24
	v_mfma_f32_16x16x32_bf16 v[100:103], v[176:179], v[210:213], v[100:103]
	v_mfma_f32_16x16x32_bf16 v[92:95], v[180:183], v[210:213], v[92:95]
	v_mfma_f32_16x16x32_bf16 v[88:91], v[198:201], v[210:213], v[88:91]
	v_mfma_f32_16x16x32_bf16 v[108:111], v[202:205], v[210:213], v[108:111]
.Lchk5_s24:
	ds_read_b128 v[206:209], v186 offset:49152
	s_waitcnt lgkmcnt(2)
	s_waitcnt vmcnt(11)
	s_cmp_le_u32 s99, 5
	s_cbranch_scc1 .Lchk5_s25
	v_mfma_f32_16x16x32_bf16 v[104:107], v[176:179], v[214:217], v[104:107]
	v_mfma_f32_16x16x32_bf16 v[96:99], v[180:183], v[214:217], v[96:99]
	v_mfma_f32_16x16x32_bf16 v[84:87], v[198:201], v[214:217], v[84:87]
	v_mfma_f32_16x16x32_bf16 v[80:83], v[202:205], v[214:217], v[80:83]
.Lchk5_s25:
	ds_read_b128 v[210:213], v186 offset:51200
	buffer_load_dwordx4 v[0:3], v184, s[24:27], s38 offen
	v_cvt_pk_bf16_f32 v31, v30, v31
	v_cvt_pk_bf16_f32 v30, v28, v29
	ds_write_b64 v185, v[30:31] offset:17408
	s_add_i32 s39, s17, 0xfffe0000
	s_waitcnt lgkmcnt(2)
	s_cmp_le_u32 s99, 6
	s_cbranch_scc1 .Lchk5_s26
	v_mfma_f32_16x16x32_bf16 v[72:75], v[176:179], v[206:209], v[72:75]
	v_mfma_f32_16x16x32_bf16 v[64:67], v[180:183], v[206:209], v[64:67]
	v_mfma_f32_16x16x32_bf16 v[60:63], v[198:201], v[206:209], v[60:63]
	v_mfma_f32_16x16x32_bf16 v[76:79], v[202:205], v[206:209], v[76:79]
.Lchk5_s26:
	ds_read_b128 v[214:217], v186 offset:53248
	s_waitcnt lgkmcnt(2)
	s_waitcnt vmcnt(11)
	s_cmp_le_u32 s99, 7
	s_cbranch_scc1 .Lchk5_s27
	v_mfma_f32_16x16x32_bf16 v[68:71], v[176:179], v[210:213], v[68:71]
	v_mfma_f32_16x16x32_bf16 v[56:59], v[180:183], v[210:213], v[56:59]
	v_mfma_f32_16x16x32_bf16 v[52:55], v[198:201], v[210:213], v[52:55]
	v_mfma_f32_16x16x32_bf16 v[48:51], v[202:205], v[210:213], v[48:51]
.Lchk5_s27:
	ds_read_b128 v[206:209], v186 offset:37888
	buffer_load_dwordx4 v[28:31], v184, s[24:27], s39 offen
	v_cvt_pk_bf16_f32 v27, v26, v27
	v_cvt_pk_bf16_f32 v26, v24, v25
	ds_write_b64 v185, v[26:27] offset:26112
	ds_read_b128 v[210:213], v186 offset:39936
	s_waitcnt lgkmcnt(3)
	s_cmp_le_u32 s99, 8
	s_cbranch_scc1 .Lchk5_s28
	v_mfma_f32_16x16x32_bf16 v[44:47], v[176:179], v[214:217], v[44:47]
	v_mfma_f32_16x16x32_bf16 v[40:43], v[180:183], v[214:217], v[40:43]
	v_mfma_f32_16x16x32_bf16 v[36:39], v[198:201], v[214:217], v[36:39]
	v_mfma_f32_16x16x32_bf16 v[32:35], v[202:205], v[214:217], v[32:35]
.Lchk5_s28:
	ds_read_b64_tr_b16 v[246:247], v188 offset:52224
	ds_read_b64_tr_b16 v[220:221], v188 offset:52256
	ds_read_b64_tr_b16 v[244:245], v187 offset:52224
	ds_read_b64_tr_b16 v[218:219], v187 offset:52256
	ds_read_b64_tr_b16 v[248:249], v187 offset:52288
	ds_read_b64_tr_b16 v[250:251], v188 offset:52288
	ds_read_b64_tr_b16 v[252:253], v187 offset:52320
	ds_read_b64_tr_b16 v[254:255], v188 offset:52320
	s_waitcnt lgkmcnt(5)
	s_waitcnt vmcnt(11)
	s_waitcnt lgkmcnt(4)
	s_waitcnt lgkmcnt(2)
	s_waitcnt lgkmcnt(0)
	s_cmp_le_u32 s99, 0
	s_cbranch_scc1 .Lchk5_s29
	v_mfma_f32_16x16x32_bf16 v[172:175], v[244:247], v[206:209], v[172:175]
	v_mfma_f32_16x16x32_bf16 v[168:171], v[218:221], v[206:209], v[168:171]
	v_mfma_f32_16x16x32_bf16 v[164:167], v[248:251], v[206:209], v[164:167]
	v_mfma_f32_16x16x32_bf16 v[160:163], v[252:255], v[206:209], v[160:163]
; #define G_DMA_A(kt, AO) do { G_DMA1(kt, AO, 0); G_DMA1(kt, AO, 1); G_DMA1(kt, AO, 2); G_DMA1(kt, AO, 3); if (MF == 9) G_DMA5(kt, AO); } while (0)
; #define G_ISSUE_B(kt) do { const unsigned _sb = (unsigned)(kt) * 4u * kstepB; \
;         _Pragma("unroll") for (int _i = 0; _i < 8; ++_i) sb[_i] = bload16(_i < 4 ? rsB0 : rsB1, vob, _sb + (_i & 3) * kstepB); } while (0)
; #define G_WRITE_B(BO) do { \
;         _Pragma("unroll") for (int _i = 0; _i < 8; ++_i) *(LAS u32x2*)(b_wr + (BO) + (_i & 3) * (16 * G_BSTRIDE) + (_i >> 2) * SLAB1) = pack4(__builtin_bit_cast(f32x4, sb[_i])); } while (0)
; #define G_ENDTILE(VM) do { asm volatile("s_waitcnt vmcnt(" #VM ")" ::: "memory"); \
;         asm volatile("s_waitcnt lgkmcnt(0)" ::: "memory"); __builtin_amdgcn_s_barrier(); asm volatile("" ::: "memory"); } while (0)
;     ...
;     __builtin_amdgcn_s_barrier();
;     G_DMA_A(0, G_A0); G_ISSUE_B(0); G_WRITE_B(G_B0);
;     __builtin_amdgcn_sched_barrier(0);
;     G_ISSUE_B(1);
;     __builtin_amdgcn_sched_barrier(0);
;     G_ENDTILE(8);
;     for (int ui = 0;; ++ui) {
; #pragma unroll
;         for (int m = 0; m < MF; ++m)
; #pragma unroll
;             for (int n = 0; n < 4; ++n) acc[m][n] = (f32x4){0.f, 0.f, 0.f, 0.f};
;         for (int t = 0; t < nt - 2; t += 2) {
;             G_TILE(G_A0, G_B0, true, G_B1, G_A1, t + 1, true, t + 2, (void)0);
;             G_ENDTILE(8);
;             G_TILE(G_A1, G_B1, true, G_B0, G_A0, t + 2, true, t + 3, (void)0);
;             G_ENDTILE(8);
;         }
.Lchk5_s29:
	ds_read_b128 v[202:205], v186 offset:41984
	buffer_load_dwordx4 v[24:27], v184, s[24:27], s17 offen
	v_cvt_pk_bf16_f32 v23, v22, v23
	v_cvt_pk_bf16_f32 v22, v20, v21
	ds_write_b64 v185, v[22:23] offset:64
	s_cmp_le_u32 s99, 1
	s_cbranch_scc1 .Lchk5_s30
	v_mfma_f32_16x16x32_bf16 v[156:159], v[244:247], v[210:213], v[156:159]
	v_mfma_f32_16x16x32_bf16 v[152:155], v[218:221], v[210:213], v[152:155]
	v_mfma_f32_16x16x32_bf16 v[148:151], v[248:251], v[210:213], v[148:151]
	v_mfma_f32_16x16x32_bf16 v[144:147], v[252:255], v[210:213], v[144:147]
.Lchk5_s30:
	ds_read_b128 v[206:209], v186 offset:44032
	s_waitcnt lgkmcnt(2)
	s_waitcnt vmcnt(11)
	s_cmp_le_u32 s99, 2
	s_cbranch_scc1 .Lchk5_s31
	v_mfma_f32_16x16x32_bf16 v[132:135], v[244:247], v[202:205], v[132:135]
	v_mfma_f32_16x16x32_bf16 v[124:127], v[218:221], v[202:205], v[124:127]
	v_mfma_f32_16x16x32_bf16 v[120:123], v[248:251], v[202:205], v[120:123]
	v_mfma_f32_16x16x32_bf16 v[140:143], v[252:255], v[202:205], v[140:143]
.Lchk5_s31:
	ds_read_b128 v[210:213], v186 offset:46080
	buffer_load_dwordx4 v[20:23], v184, s[28:31], s37 offen
	v_cvt_pk_bf16_f32 v7, v6, v7
	v_cvt_pk_bf16_f32 v6, v4, v5
	ds_write_b64 v185, v[6:7] offset:8768
	s_waitcnt lgkmcnt(2)
	s_cmp_le_u32 s99, 3
	s_cbranch_scc1 .Lchk5_s32
	v_mfma_f32_16x16x32_bf16 v[136:139], v[244:247], v[206:209], v[136:139]
	v_mfma_f32_16x16x32_bf16 v[128:131], v[218:221], v[206:209], v[128:131]
	v_mfma_f32_16x16x32_bf16 v[116:119], v[248:251], v[206:209], v[116:119]
	v_mfma_f32_16x16x32_bf16 v[112:115], v[252:255], v[206:209], v[112:115]
.Lchk5_s32:
	ds_read_b128 v[202:205], v186 offset:48128
	s_waitcnt lgkmcnt(2)
	s_waitcnt vmcnt(11)
	s_cmp_le_u32 s99, 4
	s_cbranch_scc1 .Lchk5_s33
	v_mfma_f32_16x16x32_bf16 v[100:103], v[244:247], v[210:213], v[100:103]
	v_mfma_f32_16x16x32_bf16 v[92:95], v[218:221], v[210:213], v[92:95]
	v_mfma_f32_16x16x32_bf16 v[88:91], v[248:251], v[210:213], v[88:91]
	v_mfma_f32_16x16x32_bf16 v[108:111], v[252:255], v[210:213], v[108:111]
.Lchk5_s33:
	ds_read_b128 v[206:209], v186 offset:50176
	buffer_load_dwordx4 v[4:7], v184, s[28:31], s38 offen
	v_cvt_pk_bf16_f32 v11, v10, v11
	v_cvt_pk_bf16_f32 v10, v8, v9
	ds_write_b64 v185, v[10:11] offset:17472
	s_waitcnt lgkmcnt(2)
	s_cmp_le_u32 s99, 5
	s_cbranch_scc1 .Lchk5_s34
	v_mfma_f32_16x16x32_bf16 v[104:107], v[244:247], v[202:205], v[104:107]
	v_mfma_f32_16x16x32_bf16 v[96:99], v[218:221], v[202:205], v[96:99]
	v_mfma_f32_16x16x32_bf16 v[84:87], v[248:251], v[202:205], v[84:87]
	v_mfma_f32_16x16x32_bf16 v[80:83], v[252:255], v[202:205], v[80:83]
.Lchk5_s34:
	ds_read_b128 v[210:213], v186 offset:52224
	s_waitcnt lgkmcnt(2)
	s_waitcnt vmcnt(11)
	s_cmp_le_u32 s99, 6
	s_cbranch_scc1 .Lchk5_s35
	v_mfma_f32_16x16x32_bf16 v[72:75], v[244:247], v[206:209], v[72:75]
	v_mfma_f32_16x16x32_bf16 v[64:67], v[218:221], v[206:209], v[64:67]
	v_mfma_f32_16x16x32_bf16 v[60:63], v[248:251], v[206:209], v[60:63]
	v_mfma_f32_16x16x32_bf16 v[76:79], v[252:255], v[206:209], v[76:79]
.Lchk5_s35:
	ds_read_b128 v[238:241], v186 offset:54272
	buffer_load_dwordx4 v[8:11], v184, s[28:31], s39 offen
	v_cvt_pk_bf16_f32 v19, v18, v19
	v_cvt_pk_bf16_f32 v18, v16, v17
	ds_write_b64 v185, v[18:19] offset:26176
	s_waitcnt lgkmcnt(2)
	s_cmp_le_u32 s99, 7
	s_cbranch_scc1 .Lchk5_s36
	v_mfma_f32_16x16x32_bf16 v[68:71], v[244:247], v[210:213], v[68:71]
	v_mfma_f32_16x16x32_bf16 v[56:59], v[218:221], v[210:213], v[56:59]
	v_mfma_f32_16x16x32_bf16 v[52:55], v[248:251], v[210:213], v[52:55]
	v_mfma_f32_16x16x32_bf16 v[48:51], v[252:255], v[210:213], v[48:51]
.Lchk5_s36:
	s_waitcnt lgkmcnt(1)
	buffer_load_dwordx4 v[16:19], v184, s[28:31], s17 offen
	s_waitcnt vmcnt(8)
	s_waitcnt lgkmcnt(0)
	s_barrier
	s_add_i32 s16, s16, 2
	s_add_i32 s17, s17, 0x100000
	s_addk_i32 s36, 0x100
	s_cmp_ge_i32 s16, s97
	s_cbranch_scc0 .Lchk5_loop
	s_cmp_le_u32 s99, 8
	s_cbranch_scc1 .Lchk5_s37
	v_mfma_f32_16x16x32_bf16 v[44:47], v[244:247], v[238:241], v[44:47]
	v_mfma_f32_16x16x32_bf16 v[40:43], v[218:221], v[238:241], v[40:43]
	v_mfma_f32_16x16x32_bf16 v[36:39], v[248:251], v[238:241], v[36:39]
	v_mfma_f32_16x16x32_bf16 v[32:35], v[252:255], v[238:241], v[32:35]

; #define G_DMA_A(kt, AO) do { G_DMA1(kt, AO, 0); G_DMA1(kt, AO, 1); G_DMA1(kt, AO, 2); G_DMA1(kt, AO, 3); if (MF == 9) G_DMA5(kt, AO); } while (0)
; #define G_ISSUE_B(kt) do { const unsigned _sb = (unsigned)(kt) * 4u * kstepB; \
;         _Pragma("unroll") for (int _i = 0; _i < 8; ++_i) sb[_i] = bload16(_i < 4 ? rsB0 : rsB1, vob, _sb + (_i & 3) * kstepB); } while (0)
; #define G_WRITE_B(BO) do { \
;         _Pragma("unroll") for (int _i = 0; _i < 8; ++_i) *(LAS u32x2*)(b_wr + (BO) + (_i & 3) * (16 * G_BSTRIDE) + (_i >> 2) * SLAB1) = pack4(__builtin_bit_cast(f32x4, sb[_i])); } while (0)
; #define G_ENDTILE(VM) do { asm volatile("s_waitcnt vmcnt(" #VM ")" ::: "memory"); \
;         asm volatile("s_waitcnt lgkmcnt(0)" ::: "memory"); __builtin_amdgcn_s_barrier(); asm volatile("" ::: "memory"); } while (0)
;     ...
;     __builtin_amdgcn_s_barrier();
;     G_DMA_A(0, G_A0); G_ISSUE_B(0); G_WRITE_B(G_B0);
;     __builtin_amdgcn_sched_barrier(0);
;     G_ISSUE_B(1);
;     __builtin_amdgcn_sched_barrier(0);
;     G_ENDTILE(8);
;     for (int ui = 0;; ++ui) {
; #pragma unroll
;         for (int m = 0; m < MF; ++m)
; #pragma unroll
;             for (int n = 0; n < 4; ++n) acc[m][n] = (f32x4){0.f, 0.f, 0.f, 0.f};
;         for (int t = 0; t < nt - 2; t += 2) {
;             G_TILE(G_A0, G_B0, true, G_B1, G_A1, t + 1, true, t + 2, (void)0);
;             G_ENDTILE(8);
;             G_TILE(G_A1, G_B1, true, G_B0, G_A0, t + 2, true, t + 3, (void)0);
;             G_ENDTILE(8);
;         }
.LBB0_863:
	s_mov_b32 m0, s85
	s_add_i32 s38, s36, 0xffffff80
	ds_read_b64_tr_b16 v[178:179], v206
	ds_read_b64_tr_b16 v[176:177], v205
	ds_read_b64_tr_b16 v[180:181], v205 offset:32
	ds_read_b64_tr_b16 v[184:185], v205 offset:64
	ds_read_b64_tr_b16 v[188:189], v205 offset:96
	ds_read_b128 v[192:195], v199
	ds_read_b64_tr_b16 v[182:183], v206 offset:32
	ds_read_b64_tr_b16 v[186:187], v206 offset:64
	ds_read_b64_tr_b16 v[190:191], v206 offset:96
	ds_read_b128 v[208:211], v199 offset:2048
	ds_read_b128 v[212:215], v199 offset:4096
	buffer_load_dwordx4 v200, s[20:23], s38 offen lds
	s_mov_b32 m0, s86
	v_mfma_f32_16x16x32_bf16 v[44:47], v[244:247], v[252:255], v[44:47]
	v_mfma_f32_16x16x32_bf16 v[40:43], v[248:251], v[252:255], v[40:43]
	v_mfma_f32_16x16x32_bf16 v[36:39], v[216:219], v[252:255], v[36:39]
	v_mfma_f32_16x16x32_bf16 v[32:35], v[220:223], v[252:255], v[32:35]
	s_waitcnt lgkmcnt(0)
	v_mfma_f32_16x16x32_bf16 v[172:175], v[176:179], v[192:195], v[172:175]
	buffer_load_dwordx4 v201, s[20:23], s38 offen lds
	s_mov_b32 m0, s87
	s_nop 0
	buffer_load_dwordx4 v202, s[20:23], s38 offen lds
	s_mov_b32 m0, s88
	v_mfma_f32_16x16x32_bf16 v[168:171], v[180:183], v[192:195], v[168:171]
	buffer_load_dwordx4 v203, s[20:23], s38 offen lds
	s_mov_b32 m0, s89
	s_nop 0
	buffer_load_dwordx4 v204, s[20:23], s38 offen lds
	v_mfma_f32_16x16x32_bf16 v[164:167], v[184:187], v[192:195], v[164:167]
	s_add_i32 s38, s9, 0xfff20000
	v_mfma_f32_16x16x32_bf16 v[160:163], v[188:191], v[192:195], v[160:163]
	v_mfma_f32_16x16x32_bf16 v[156:159], v[176:179], v[208:211], v[156:159]
	ds_read_b128 v[192:195], v199 offset:6144
	s_waitcnt vmcnt(12)
	v_cvt_pk_bf16_f32 v23, v22, v23
	v_cvt_pk_bf16_f32 v22, v20, v21
	v_mfma_f32_16x16x32_bf16 v[152:155], v[180:183], v[208:211], v[152:155]
	ds_write_b64 v198, v[22:23] offset:34816
	v_mfma_f32_16x16x32_bf16 v[148:151], v[184:187], v[208:211], v[148:151]
	v_mfma_f32_16x16x32_bf16 v[144:147], v[188:191], v[208:211], v[144:147]
	v_mfma_f32_16x16x32_bf16 v[132:135], v[176:179], v[212:215], v[132:135]
	ds_read_b128 v[208:211], v199 offset:8192
	v_mfma_f32_16x16x32_bf16 v[124:127], v[180:183], v[212:215], v[124:127]
	v_mfma_f32_16x16x32_bf16 v[120:123], v[184:187], v[212:215], v[120:123]
	v_mfma_f32_16x16x32_bf16 v[140:143], v[188:191], v[212:215], v[140:143]
	s_waitcnt lgkmcnt(2)
	v_mfma_f32_16x16x32_bf16 v[136:139], v[176:179], v[192:195], v[136:139]
	ds_read_b128 v[212:215], v199 offset:10240
	buffer_load_dwordx4 v[20:23], v197, s[24:27], s38 offen
	s_waitcnt vmcnt(11)
	v_cvt_pk_bf16_f32 v31, v30, v31
	v_cvt_pk_bf16_f32 v30, v28, v29
	v_mfma_f32_16x16x32_bf16 v[128:131], v[180:183], v[192:195], v[128:131]
	ds_write_b64 v198, v[30:31] offset:43520
	v_mfma_f32_16x16x32_bf16 v[116:119], v[184:187], v[192:195], v[116:119]
	v_mfma_f32_16x16x32_bf16 v[112:115], v[188:191], v[192:195], v[112:115]
	s_add_i32 s39, s9, 0xfff40000
	s_waitcnt lgkmcnt(2)
	v_mfma_f32_16x16x32_bf16 v[100:103], v[176:179], v[208:211], v[100:103]
	ds_read_b128 v[192:195], v199 offset:12288
	v_mfma_f32_16x16x32_bf16 v[92:95], v[180:183], v[208:211], v[92:95]
	v_mfma_f32_16x16x32_bf16 v[88:91], v[184:187], v[208:211], v[88:91]
	v_mfma_f32_16x16x32_bf16 v[108:111], v[188:191], v[208:211], v[108:111]
	s_waitcnt lgkmcnt(2)
	v_mfma_f32_16x16x32_bf16 v[104:107], v[176:179], v[212:215], v[104:107]
	ds_read_b128 v[208:211], v199 offset:14336
	v_cvt_pk_bf16_f32 v19, v18, v19
	v_cvt_pk_bf16_f32 v18, v16, v17
	v_mfma_f32_16x16x32_bf16 v[96:99], v[180:183], v[212:215], v[96:99]
	ds_write_b64 v198, v[18:19] offset:52224
	v_mfma_f32_16x16x32_bf16 v[84:87], v[184:187], v[212:215], v[84:87]
	v_mfma_f32_16x16x32_bf16 v[80:83], v[188:191], v[212:215], v[80:83]
	s_add_i32 s43, s9, 0xfff60000
	buffer_load_dwordx4 v[28:31], v197, s[24:27], s39 offen
	s_waitcnt lgkmcnt(2)
	v_mfma_f32_16x16x32_bf16 v[72:75], v[176:179], v[192:195], v[72:75]
	ds_read_b128 v[212:215], v199 offset:16384
	v_mfma_f32_16x16x32_bf16 v[64:67], v[180:183], v[192:195], v[64:67]
	v_mfma_f32_16x16x32_bf16 v[60:63], v[184:187], v[192:195], v[60:63]
	v_mfma_f32_16x16x32_bf16 v[76:79], v[188:191], v[192:195], v[76:79]
	s_waitcnt lgkmcnt(2)
	v_mfma_f32_16x16x32_bf16 v[68:71], v[176:179], v[208:211], v[68:71]
	ds_read_b128 v[192:195], v199 offset:1024
	buffer_load_dwordx4 v[16:19], v197, s[24:27], s43 offen
	s_waitcnt vmcnt(12)
	v_cvt_pk_bf16_f32 v27, v26, v27
	v_cvt_pk_bf16_f32 v26, v24, v25
	v_mfma_f32_16x16x32_bf16 v[56:59], v[180:183], v[208:211], v[56:59]
	ds_write_b64 v198, v[26:27] offset:60928
	v_mfma_f32_16x16x32_bf16 v[52:55], v[184:187], v[208:211], v[52:55]
	v_mfma_f32_16x16x32_bf16 v[48:51], v[188:191], v[208:211], v[48:51]
	s_add_i32 s45, s9, 0xfff80000
	ds_read_b128 v[208:211], v199 offset:3072
	s_waitcnt lgkmcnt(3)
	v_mfma_f32_16x16x32_bf16 v[44:47], v[176:179], v[212:215], v[44:47]
	ds_read_b64_tr_b16 v[246:247], v206 offset:17408
	ds_read_b64_tr_b16 v[218:219], v206 offset:17440
	ds_read_b64_tr_b16 v[244:245], v205 offset:17408
	ds_read_b64_tr_b16 v[216:217], v205 offset:17440
	v_mfma_f32_16x16x32_bf16 v[40:43], v[180:183], v[212:215], v[40:43]
	ds_read_b64_tr_b16 v[248:249], v205 offset:17472
	ds_read_b64_tr_b16 v[250:251], v206 offset:17472
	v_mfma_f32_16x16x32_bf16 v[36:39], v[184:187], v[212:215], v[36:39]
	ds_read_b64_tr_b16 v[252:253], v205 offset:17504
	ds_read_b64_tr_b16 v[254:255], v206 offset:17504
	v_mfma_f32_16x16x32_bf16 v[32:35], v[188:191], v[212:215], v[32:35]
	s_waitcnt lgkmcnt(5)
	v_mfma_f32_16x16x32_bf16 v[172:175], v[244:247], v[192:195], v[172:175]
	ds_read_b128 v[188:191], v199 offset:5120
	buffer_load_dwordx4 v[24:27], v197, s[24:27], s45 offen
	s_waitcnt vmcnt(12)
; #define G_DMA_A(kt, AO) do { G_DMA1(kt, AO, 0); G_DMA1(kt, AO, 1); G_DMA1(kt, AO, 2); G_DMA1(kt, AO, 3); if (MF == 9) G_DMA5(kt, AO); } while (0)
; #define G_ISSUE_B(kt) do { const unsigned _sb = (unsigned)(kt) * 4u * kstepB; \
;         _Pragma("unroll") for (int _i = 0; _i < 8; ++_i) sb[_i] = bload16(_i < 4 ? rsB0 : rsB1, vob, _sb + (_i & 3) * kstepB); } while (0)
; #define G_WRITE_B(BO) do { \
;         _Pragma("unroll") for (int _i = 0; _i < 8; ++_i) *(LAS u32x2*)(b_wr + (BO) + (_i & 3) * (16 * G_BSTRIDE) + (_i >> 2) * SLAB1) = pack4(__builtin_bit_cast(f32x4, sb[_i])); } while (0)
; #define G_ENDTILE(VM) do { asm volatile("s_waitcnt vmcnt(" #VM ")" ::: "memory"); \
;         asm volatile("s_waitcnt lgkmcnt(0)" ::: "memory"); __builtin_amdgcn_s_barrier(); asm volatile("" ::: "memory"); } while (0)
;     ...
;     __builtin_amdgcn_s_barrier();
;     G_DMA_A(0, G_A0); G_ISSUE_B(0); G_WRITE_B(G_B0);
;     __builtin_amdgcn_sched_barrier(0);
;     G_ISSUE_B(1);
;     __builtin_amdgcn_sched_barrier(0);
;     G_ENDTILE(8);
;     for (int ui = 0;; ++ui) {
; #pragma unroll
;         for (int m = 0; m < MF; ++m)
; #pragma unroll
;             for (int n = 0; n < 4; ++n) acc[m][n] = (f32x4){0.f, 0.f, 0.f, 0.f};
;         for (int t = 0; t < nt - 2; t += 2) {
;             G_TILE(G_A0, G_B0, true, G_B1, G_A1, t + 1, true, t + 2, (void)0);
;             G_ENDTILE(8);
;             G_TILE(G_A1, G_B1, true, G_B0, G_A0, t + 2, true, t + 3, (void)0);
;             G_ENDTILE(8);
;         }
	v_cvt_pk_bf16_f32 v15, v14, v15
	v_cvt_pk_bf16_f32 v14, v12, v13
	s_waitcnt lgkmcnt(5)
	v_mfma_f32_16x16x32_bf16 v[168:171], v[216:219], v[192:195], v[168:171]
	ds_write_b64 v198, v[14:15] offset:35072
	s_waitcnt lgkmcnt(4)
	v_mfma_f32_16x16x32_bf16 v[164:167], v[248:251], v[192:195], v[164:167]
	s_waitcnt lgkmcnt(2)
	v_mfma_f32_16x16x32_bf16 v[160:163], v[252:255], v[192:195], v[160:163]
	v_mfma_f32_16x16x32_bf16 v[156:159], v[244:247], v[208:211], v[156:159]
	ds_read_b128 v[192:195], v199 offset:7168
	v_mfma_f32_16x16x32_bf16 v[152:155], v[216:219], v[208:211], v[152:155]
	v_mfma_f32_16x16x32_bf16 v[148:151], v[248:251], v[208:211], v[148:151]
	v_mfma_f32_16x16x32_bf16 v[144:147], v[252:255], v[208:211], v[144:147]
	s_waitcnt lgkmcnt(2)
	v_mfma_f32_16x16x32_bf16 v[132:135], v[244:247], v[188:191], v[132:135]
	ds_read_b128 v[208:211], v199 offset:9216
	buffer_load_dwordx4 v[12:15], v197, s[16:19], s38 offen
	s_waitcnt vmcnt(11)
	v_cvt_pk_bf16_f32 v7, v6, v7
	v_cvt_pk_bf16_f32 v6, v4, v5
	v_mfma_f32_16x16x32_bf16 v[124:127], v[216:219], v[188:191], v[124:127]
	ds_write_b64 v198, v[6:7] offset:43776
	v_mfma_f32_16x16x32_bf16 v[120:123], v[248:251], v[188:191], v[120:123]
	v_mfma_f32_16x16x32_bf16 v[140:143], v[252:255], v[188:191], v[140:143]
	s_waitcnt lgkmcnt(2)
	v_mfma_f32_16x16x32_bf16 v[136:139], v[244:247], v[192:195], v[136:139]
	ds_read_b128 v[188:191], v199 offset:11264
	v_mfma_f32_16x16x32_bf16 v[128:131], v[216:219], v[192:195], v[128:131]
	v_mfma_f32_16x16x32_bf16 v[116:119], v[248:251], v[192:195], v[116:119]
	v_mfma_f32_16x16x32_bf16 v[112:115], v[252:255], v[192:195], v[112:115]
	s_waitcnt lgkmcnt(2)
	v_mfma_f32_16x16x32_bf16 v[100:103], v[244:247], v[208:211], v[100:103]
	ds_read_b128 v[192:195], v199 offset:13312
	v_cvt_pk_bf16_f32 v3, v2, v3
	v_cvt_pk_bf16_f32 v2, v0, v1
	v_mfma_f32_16x16x32_bf16 v[92:95], v[216:219], v[208:211], v[92:95]
	ds_write_b64 v198, v[2:3] offset:52480
	v_mfma_f32_16x16x32_bf16 v[88:91], v[248:251], v[208:211], v[88:91]
	v_mfma_f32_16x16x32_bf16 v[108:111], v[252:255], v[208:211], v[108:111]
	buffer_load_dwordx4 v[4:7], v197, s[16:19], s39 offen
	s_waitcnt lgkmcnt(2)
	v_mfma_f32_16x16x32_bf16 v[104:107], v[244:247], v[188:191], v[104:107]
	ds_read_b128 v[208:211], v199 offset:15360
	v_mfma_f32_16x16x32_bf16 v[96:99], v[216:219], v[188:191], v[96:99]
	v_mfma_f32_16x16x32_bf16 v[84:87], v[248:251], v[188:191], v[84:87]
	v_mfma_f32_16x16x32_bf16 v[80:83], v[252:255], v[188:191], v[80:83]
	s_waitcnt lgkmcnt(2)
	v_mfma_f32_16x16x32_bf16 v[72:75], v[244:247], v[192:195], v[72:75]
	ds_read_b128 v[236:239], v199 offset:17408
	buffer_load_dwordx4 v[0:3], v197, s[16:19], s43 offen
	s_waitcnt vmcnt(12)
	v_cvt_pk_bf16_f32 v11, v10, v11
	v_cvt_pk_bf16_f32 v10, v8, v9
	v_mfma_f32_16x16x32_bf16 v[64:67], v[216:219], v[192:195], v[64:67]
	ds_write_b64 v198, v[10:11] offset:61184
	v_mfma_f32_16x16x32_bf16 v[60:63], v[248:251], v[192:195], v[60:63]
	v_mfma_f32_16x16x32_bf16 v[76:79], v[252:255], v[192:195], v[76:79]
	s_waitcnt lgkmcnt(2)
	v_mfma_f32_16x16x32_bf16 v[68:71], v[244:247], v[208:211], v[68:71]
	v_mfma_f32_16x16x32_bf16 v[56:59], v[216:219], v[208:211], v[56:59]
	v_mfma_f32_16x16x32_bf16 v[52:55], v[248:251], v[208:211], v[52:55]
	v_mfma_f32_16x16x32_bf16 v[48:51], v[252:255], v[208:211], v[48:51]
	s_waitcnt lgkmcnt(1)
	buffer_load_dwordx4 v[8:11], v197, s[16:19], s45 offen
	s_waitcnt vmcnt(8)
	s_mov_b32 m0, s49
	s_waitcnt lgkmcnt(0)
	s_barrier
	ds_read_b64_tr_b16 v[178:179], v206 offset:34816
	ds_read_b64_tr_b16 v[176:177], v205 offset:34816
	ds_read_b64_tr_b16 v[180:181], v205 offset:34848
	ds_read_b64_tr_b16 v[184:185], v205 offset:34880
	ds_read_b64_tr_b16 v[188:189], v205 offset:34912
	ds_read_b128 v[192:195], v199 offset:36864
	ds_read_b64_tr_b16 v[182:183], v206 offset:34848
	ds_read_b64_tr_b16 v[186:187], v206 offset:34880
	ds_read_b64_tr_b16 v[190:191], v206 offset:34912
	ds_read_b128 v[208:211], v199 offset:38912
	ds_read_b128 v[212:215], v199 offset:40960
	buffer_load_dwordx4 v200, s[20:23], s36 offen lds
	s_mov_b32 m0, s68
	v_mfma_f32_16x16x32_bf16 v[44:47], v[244:247], v[236:239], v[44:47]
	v_mfma_f32_16x16x32_bf16 v[40:43], v[216:219], v[236:239], v[40:43]
	v_mfma_f32_16x16x32_bf16 v[36:39], v[248:251], v[236:239], v[36:39]
	v_mfma_f32_16x16x32_bf16 v[32:35], v[252:255], v[236:239], v[32:35]
	s_waitcnt lgkmcnt(5)
	v_mfma_f32_16x16x32_bf16 v[172:175], v[176:179], v[192:195], v[172:175]
	buffer_load_dwordx4 v201, s[20:23], s36 offen lds
	s_mov_b32 m0, s77
	s_add_i32 s38, s9, 0xfffa0000
	buffer_load_dwordx4 v202, s[20:23], s36 offen lds
	s_mov_b32 m0, s78
	s_waitcnt lgkmcnt(4)
	v_mfma_f32_16x16x32_bf16 v[168:171], v[180:183], v[192:195], v[168:171]
	buffer_load_dwordx4 v203, s[20:23], s36 offen lds
	s_mov_b32 m0, s79
	s_nop 0
	buffer_load_dwordx4 v204, s[20:23], s36 offen lds
	s_waitcnt lgkmcnt(3)
	v_mfma_f32_16x16x32_bf16 v[164:167], v[184:187], v[192:195], v[164:167]
	s_waitcnt lgkmcnt(2)
	v_mfma_f32_16x16x32_bf16 v[160:163], v[188:191], v[192:195], v[160:163]
	s_waitcnt lgkmcnt(1)
	v_mfma_f32_16x16x32_bf16 v[156:159], v[176:179], v[208:211], v[156:159]
	ds_read_b128 v[192:195], v199 offset:43008
	s_waitcnt vmcnt(12)
	v_cvt_pk_bf16_f32 v23, v22, v23
	v_cvt_pk_bf16_f32 v22, v20, v21
	v_mfma_f32_16x16x32_bf16 v[152:155], v[180:183], v[208:211], v[152:155]
	ds_write_b64 v198, v[22:23]
	v_mfma_f32_16x16x32_bf16 v[148:151], v[184:187], v[208:211], v[148:151]
	v_mfma_f32_16x16x32_bf16 v[144:147], v[188:191], v[208:211], v[144:147]
	s_waitcnt lgkmcnt(2)
; #define G_DMA_A(kt, AO) do { G_DMA1(kt, AO, 0); G_DMA1(kt, AO, 1); G_DMA1(kt, AO, 2); G_DMA1(kt, AO, 3); if (MF == 9) G_DMA5(kt, AO); } while (0)
; #define G_ISSUE_B(kt) do { const unsigned _sb = (unsigned)(kt) * 4u * kstepB; \
;         _Pragma("unroll") for (int _i = 0; _i < 8; ++_i) sb[_i] = bload16(_i < 4 ? rsB0 : rsB1, vob, _sb + (_i & 3) * kstepB); } while (0)
; #define G_WRITE_B(BO) do { \
;         _Pragma("unroll") for (int _i = 0; _i < 8; ++_i) *(LAS u32x2*)(b_wr + (BO) + (_i & 3) * (16 * G_BSTRIDE) + (_i >> 2) * SLAB1) = pack4(__builtin_bit_cast(f32x4, sb[_i])); } while (0)
; #define G_ENDTILE(VM) do { asm volatile("s_waitcnt vmcnt(" #VM ")" ::: "memory"); \
;         asm volatile("s_waitcnt lgkmcnt(0)" ::: "memory"); __builtin_amdgcn_s_barrier(); asm volatile("" ::: "memory"); } while (0)
;     ...
;     __builtin_amdgcn_s_barrier();
;     G_DMA_A(0, G_A0); G_ISSUE_B(0); G_WRITE_B(G_B0);
;     __builtin_amdgcn_sched_barrier(0);
;     G_ISSUE_B(1);
;     __builtin_amdgcn_sched_barrier(0);
;     G_ENDTILE(8);
;     for (int ui = 0;; ++ui) {
; #pragma unroll
;         for (int m = 0; m < MF; ++m)
; #pragma unroll
;             for (int n = 0; n < 4; ++n) acc[m][n] = (f32x4){0.f, 0.f, 0.f, 0.f};
;         for (int t = 0; t < nt - 2; t += 2) {
;             G_TILE(G_A0, G_B0, true, G_B1, G_A1, t + 1, true, t + 2, (void)0);
;             G_ENDTILE(8);
;             G_TILE(G_A1, G_B1, true, G_B0, G_A0, t + 2, true, t + 3, (void)0);
;             G_ENDTILE(8);
;         }
	v_mfma_f32_16x16x32_bf16 v[132:135], v[176:179], v[212:215], v[132:135]
	ds_read_b128 v[208:211], v199 offset:45056
	v_mfma_f32_16x16x32_bf16 v[124:127], v[180:183], v[212:215], v[124:127]
	v_mfma_f32_16x16x32_bf16 v[120:123], v[184:187], v[212:215], v[120:123]
	v_mfma_f32_16x16x32_bf16 v[140:143], v[188:191], v[212:215], v[140:143]
	s_waitcnt lgkmcnt(2)
	v_mfma_f32_16x16x32_bf16 v[136:139], v[176:179], v[192:195], v[136:139]
	ds_read_b128 v[212:215], v199 offset:47104
	buffer_load_dwordx4 v[20:23], v197, s[24:27], s38 offen
	s_waitcnt vmcnt(12)
	v_cvt_pk_bf16_f32 v31, v30, v31
	v_cvt_pk_bf16_f32 v30, v28, v29
	v_mfma_f32_16x16x32_bf16 v[128:131], v[180:183], v[192:195], v[128:131]
	ds_write_b64 v198, v[30:31] offset:8704
	v_mfma_f32_16x16x32_bf16 v[116:119], v[184:187], v[192:195], v[116:119]
	v_mfma_f32_16x16x32_bf16 v[112:115], v[188:191], v[192:195], v[112:115]
	s_add_i32 s39, s9, 0xfffc0000
	s_waitcnt lgkmcnt(2)
	v_mfma_f32_16x16x32_bf16 v[100:103], v[176:179], v[208:211], v[100:103]
	ds_read_b128 v[192:195], v199 offset:49152
	v_mfma_f32_16x16x32_bf16 v[92:95], v[180:183], v[208:211], v[92:95]
	v_mfma_f32_16x16x32_bf16 v[88:91], v[184:187], v[208:211], v[88:91]
	v_mfma_f32_16x16x32_bf16 v[108:111], v[188:191], v[208:211], v[108:111]
	s_waitcnt lgkmcnt(2)
	v_mfma_f32_16x16x32_bf16 v[104:107], v[176:179], v[212:215], v[104:107]
	ds_read_b128 v[208:211], v199 offset:51200
	buffer_load_dwordx4 v[28:31], v197, s[24:27], s39 offen
	s_waitcnt vmcnt(12)
	v_cvt_pk_bf16_f32 v19, v18, v19
	v_cvt_pk_bf16_f32 v18, v16, v17
	v_mfma_f32_16x16x32_bf16 v[96:99], v[180:183], v[212:215], v[96:99]
	ds_write_b64 v198, v[18:19] offset:17408
	v_mfma_f32_16x16x32_bf16 v[84:87], v[184:187], v[212:215], v[84:87]
	v_mfma_f32_16x16x32_bf16 v[80:83], v[188:191], v[212:215], v[80:83]
	s_add_i32 s43, s9, 0xfffe0000
	s_waitcnt lgkmcnt(2)
	v_mfma_f32_16x16x32_bf16 v[72:75], v[176:179], v[192:195], v[72:75]
	ds_read_b128 v[212:215], v199 offset:53248
	v_mfma_f32_16x16x32_bf16 v[64:67], v[180:183], v[192:195], v[64:67]
	v_mfma_f32_16x16x32_bf16 v[60:63], v[184:187], v[192:195], v[60:63]
	v_mfma_f32_16x16x32_bf16 v[76:79], v[188:191], v[192:195], v[76:79]
	s_waitcnt lgkmcnt(2)
	v_mfma_f32_16x16x32_bf16 v[68:71], v[176:179], v[208:211], v[68:71]
	ds_read_b128 v[192:195], v199 offset:37888
	buffer_load_dwordx4 v[16:19], v197, s[24:27], s43 offen
	s_waitcnt vmcnt(12)
	v_cvt_pk_bf16_f32 v27, v26, v27
	v_cvt_pk_bf16_f32 v26, v24, v25
	v_mfma_f32_16x16x32_bf16 v[56:59], v[180:183], v[208:211], v[56:59]
	ds_write_b64 v198, v[26:27] offset:26112
	v_mfma_f32_16x16x32_bf16 v[52:55], v[184:187], v[208:211], v[52:55]
	v_mfma_f32_16x16x32_bf16 v[48:51], v[188:191], v[208:211], v[48:51]
	s_waitcnt lgkmcnt(2)
	v_mfma_f32_16x16x32_bf16 v[44:47], v[176:179], v[212:215], v[44:47]
	ds_read_b128 v[176:179], v199 offset:39936
	v_mfma_f32_16x16x32_bf16 v[40:43], v[180:183], v[212:215], v[40:43]
	ds_read_b64_tr_b16 v[244:245], v205 offset:52224
	ds_read_b64_tr_b16 v[248:249], v205 offset:52256
	ds_read_b64_tr_b16 v[216:217], v205 offset:52288
	ds_read_b64_tr_b16 v[220:221], v205 offset:52320
	ds_read_b64_tr_b16 v[246:247], v206 offset:52224
	ds_read_b64_tr_b16 v[250:251], v206 offset:52256
	ds_read_b64_tr_b16 v[218:219], v206 offset:52288
	ds_read_b64_tr_b16 v[222:223], v206 offset:52320
	v_mfma_f32_16x16x32_bf16 v[36:39], v[184:187], v[212:215], v[36:39]
	v_mfma_f32_16x16x32_bf16 v[32:35], v[188:191], v[212:215], v[32:35]
	s_waitcnt lgkmcnt(3)
	v_mfma_f32_16x16x32_bf16 v[172:175], v[244:247], v[192:195], v[172:175]
	ds_read_b128 v[184:187], v199 offset:41984
	buffer_load_dwordx4 v[24:27], v197, s[24:27], s9 offen
	s_waitcnt vmcnt(12)
	v_cvt_pk_bf16_f32 v15, v14, v15
	v_cvt_pk_bf16_f32 v14, v12, v13
	s_waitcnt lgkmcnt(3)
; #define G_DMA_A(kt, AO) do { G_DMA1(kt, AO, 0); G_DMA1(kt, AO, 1); G_DMA1(kt, AO, 2); G_DMA1(kt, AO, 3); if (MF == 9) G_DMA5(kt, AO); } while (0)
; #define G_ISSUE_B(kt) do { const unsigned _sb = (unsigned)(kt) * 4u * kstepB; \
;         _Pragma("unroll") for (int _i = 0; _i < 8; ++_i) sb[_i] = bload16(_i < 4 ? rsB0 : rsB1, vob, _sb + (_i & 3) * kstepB); } while (0)
; #define G_WRITE_B(BO) do { \
;         _Pragma("unroll") for (int _i = 0; _i < 8; ++_i) *(LAS u32x2*)(b_wr + (BO) + (_i & 3) * (16 * G_BSTRIDE) + (_i >> 2) * SLAB1) = pack4(__builtin_bit_cast(f32x4, sb[_i])); } while (0)
; #define G_ENDTILE(VM) do { asm volatile("s_waitcnt vmcnt(" #VM ")" ::: "memory"); \
;         asm volatile("s_waitcnt lgkmcnt(0)" ::: "memory"); __builtin_amdgcn_s_barrier(); asm volatile("" ::: "memory"); } while (0)
;     ...
;     __builtin_amdgcn_s_barrier();
;     G_DMA_A(0, G_A0); G_ISSUE_B(0); G_WRITE_B(G_B0);
;     __builtin_amdgcn_sched_barrier(0);
;     G_ISSUE_B(1);
;     __builtin_amdgcn_sched_barrier(0);
;     G_ENDTILE(8);
;     for (int ui = 0;; ++ui) {
; #pragma unroll
;         for (int m = 0; m < MF; ++m)
; #pragma unroll
;             for (int n = 0; n < 4; ++n) acc[m][n] = (f32x4){0.f, 0.f, 0.f, 0.f};
;         for (int t = 0; t < nt - 2; t += 2) {
;             G_TILE(G_A0, G_B0, true, G_B1, G_A1, t + 1, true, t + 2, (void)0);
;             G_ENDTILE(8);
;             G_TILE(G_A1, G_B1, true, G_B0, G_A0, t + 2, true, t + 3, (void)0);
;             G_ENDTILE(8);
;         }
	v_mfma_f32_16x16x32_bf16 v[168:171], v[248:251], v[192:195], v[168:171]
	ds_write_b64 v198, v[14:15] offset:256
	s_waitcnt lgkmcnt(3)
	v_mfma_f32_16x16x32_bf16 v[164:167], v[216:219], v[192:195], v[164:167]
	s_waitcnt lgkmcnt(2)
	v_mfma_f32_16x16x32_bf16 v[160:163], v[220:223], v[192:195], v[160:163]
	v_mfma_f32_16x16x32_bf16 v[156:159], v[244:247], v[176:179], v[156:159]
	ds_read_b128 v[188:191], v199 offset:44032
	v_mfma_f32_16x16x32_bf16 v[152:155], v[248:251], v[176:179], v[152:155]
	v_mfma_f32_16x16x32_bf16 v[148:151], v[216:219], v[176:179], v[148:151]
	v_mfma_f32_16x16x32_bf16 v[144:147], v[220:223], v[176:179], v[144:147]
	s_waitcnt lgkmcnt(2)
	v_mfma_f32_16x16x32_bf16 v[132:135], v[244:247], v[184:187], v[132:135]
	ds_read_b128 v[176:179], v199 offset:46080
	buffer_load_dwordx4 v[12:15], v197, s[16:19], s38 offen
	s_waitcnt vmcnt(12)
	v_cvt_pk_bf16_f32 v7, v6, v7
	v_cvt_pk_bf16_f32 v6, v4, v5
	v_mfma_f32_16x16x32_bf16 v[124:127], v[248:251], v[184:187], v[124:127]
	ds_write_b64 v198, v[6:7] offset:8960
	v_mfma_f32_16x16x32_bf16 v[120:123], v[216:219], v[184:187], v[120:123]
	v_mfma_f32_16x16x32_bf16 v[140:143], v[220:223], v[184:187], v[140:143]
	s_waitcnt lgkmcnt(2)
	v_mfma_f32_16x16x32_bf16 v[136:139], v[244:247], v[188:191], v[136:139]
	ds_read_b128 v[184:187], v199 offset:48128
	v_mfma_f32_16x16x32_bf16 v[128:131], v[248:251], v[188:191], v[128:131]
	v_mfma_f32_16x16x32_bf16 v[116:119], v[216:219], v[188:191], v[116:119]
	v_mfma_f32_16x16x32_bf16 v[112:115], v[220:223], v[188:191], v[112:115]
	s_waitcnt lgkmcnt(2)
	v_mfma_f32_16x16x32_bf16 v[100:103], v[244:247], v[176:179], v[100:103]
	ds_read_b128 v[188:191], v199 offset:50176
	buffer_load_dwordx4 v[4:7], v197, s[16:19], s39 offen
	s_waitcnt vmcnt(12)
	v_cvt_pk_bf16_f32 v3, v2, v3
	v_cvt_pk_bf16_f32 v2, v0, v1
	v_mfma_f32_16x16x32_bf16 v[92:95], v[248:251], v[176:179], v[92:95]
	ds_write_b64 v198, v[2:3] offset:17664
	v_mfma_f32_16x16x32_bf16 v[88:91], v[216:219], v[176:179], v[88:91]
	v_mfma_f32_16x16x32_bf16 v[108:111], v[220:223], v[176:179], v[108:111]
	s_waitcnt lgkmcnt(2)
	v_mfma_f32_16x16x32_bf16 v[104:107], v[244:247], v[184:187], v[104:107]
	ds_read_b128 v[176:179], v199 offset:52224
	v_mfma_f32_16x16x32_bf16 v[96:99], v[248:251], v[184:187], v[96:99]
	v_mfma_f32_16x16x32_bf16 v[84:87], v[216:219], v[184:187], v[84:87]
	v_mfma_f32_16x16x32_bf16 v[80:83], v[220:223], v[184:187], v[80:83]
	s_waitcnt lgkmcnt(2)
	v_mfma_f32_16x16x32_bf16 v[72:75], v[244:247], v[188:191], v[72:75]
	ds_read_b128 v[252:255], v199 offset:54272
	buffer_load_dwordx4 v[0:3], v197, s[16:19], s43 offen
	s_waitcnt vmcnt(12)
	v_cvt_pk_bf16_f32 v11, v10, v11
	v_cvt_pk_bf16_f32 v10, v8, v9
	v_mfma_f32_16x16x32_bf16 v[64:67], v[248:251], v[188:191], v[64:67]
	ds_write_b64 v198, v[10:11] offset:26368
	v_mfma_f32_16x16x32_bf16 v[60:63], v[216:219], v[188:191], v[60:63]
	v_mfma_f32_16x16x32_bf16 v[76:79], v[220:223], v[188:191], v[76:79]
	s_waitcnt lgkmcnt(2)
	v_mfma_f32_16x16x32_bf16 v[68:71], v[244:247], v[176:179], v[68:71]
	v_mfma_f32_16x16x32_bf16 v[56:59], v[248:251], v[176:179], v[56:59]
	v_mfma_f32_16x16x32_bf16 v[52:55], v[216:219], v[176:179], v[52:55]
	v_mfma_f32_16x16x32_bf16 v[48:51], v[220:223], v[176:179], v[48:51]
	s_waitcnt lgkmcnt(1)
	buffer_load_dwordx4 v[8:11], v197, s[16:19], s9 offen
	s_waitcnt vmcnt(8)
	s_waitcnt lgkmcnt(0)
	s_barrier
	s_add_i32 s8, s8, 2
	s_add_i32 s9, s9, 0x100000
	s_addk_i32 s36, 0x100
	s_cmp_ge_i32 s8, s84
	s_cbranch_scc0 .LBB0_863
	v_mfma_f32_16x16x32_bf16 v[44:47], v[244:247], v[252:255], v[44:47]
	v_mfma_f32_16x16x32_bf16 v[40:43], v[248:251], v[252:255], v[40:43]
	v_mfma_f32_16x16x32_bf16 v[36:39], v[216:219], v[252:255], v[36:39]
	v_mfma_f32_16x16x32_bf16 v[32:35], v[220:223], v[252:255], v[32:35]
	s_branch .LBB0_865

; #define G_DMA_A(kt, AO) do { G_DMA1(kt, AO, 0); G_DMA1(kt, AO, 1); G_DMA1(kt, AO, 2); G_DMA1(kt, AO, 3); if (MF == 9) G_DMA5(kt, AO); } while (0)
; #define G_ISSUE_B(kt) do { const unsigned _sb = (unsigned)(kt) * 4u * kstepB; \
;         _Pragma("unroll") for (int _i = 0; _i < 8; ++_i) sb[_i] = bload16(_i < 4 ? rsB0 : rsB1, vob, _sb + (_i & 3) * kstepB); } while (0)
; #define G_WRITE_B(BO) do { \
;         _Pragma("unroll") for (int _i = 0; _i < 8; ++_i) *(LAS u32x2*)(b_wr + (BO) + (_i & 3) * (16 * G_BSTRIDE) + (_i >> 2) * SLAB1) = pack4(__builtin_bit_cast(f32x4, sb[_i])); } while (0)
; #define G_ENDTILE(VM) do { asm volatile("s_waitcnt vmcnt(" #VM ")" ::: "memory"); \
;         asm volatile("s_waitcnt lgkmcnt(0)" ::: "memory"); __builtin_amdgcn_s_barrier(); asm volatile("" ::: "memory"); } while (0)
;     ...
;     __builtin_amdgcn_s_barrier();
;     G_DMA_A(0, G_A0); G_ISSUE_B(0); G_WRITE_B(G_B0);
;     __builtin_amdgcn_sched_barrier(0);
;     G_ISSUE_B(1);
;     __builtin_amdgcn_sched_barrier(0);
;     G_ENDTILE(8);
;     for (int ui = 0;; ++ui) {
; #pragma unroll
;         for (int m = 0; m < MF; ++m)
; #pragma unroll
;             for (int n = 0; n < 4; ++n) acc[m][n] = (f32x4){0.f, 0.f, 0.f, 0.f};
;         for (int t = 0; t < nt - 2; t += 2) {
;             G_TILE(G_A0, G_B0, true, G_B1, G_A1, t + 1, true, t + 2, (void)0);
;             G_ENDTILE(8);
;             G_TILE(G_A1, G_B1, true, G_B0, G_A0, t + 2, true, t + 3, (void)0);
;             G_ENDTILE(8);
;         }
.Lchk6_s3:
	ds_read_b128 v[192:195], v199 offset:6144
	v_cvt_pk_bf16_f32 v23, v22, v23
	v_cvt_pk_bf16_f32 v22, v20, v21
	ds_write_b64 v198, v[22:23] offset:34816
	s_cmp_le_u32 s99, 2
	s_cbranch_scc1 .Lchk6_s4
	v_mfma_f32_16x16x32_bf16 v[132:135], v[176:179], v[212:215], v[132:135]
	v_mfma_f32_16x16x32_bf16 v[124:127], v[180:183], v[212:215], v[124:127]
	v_mfma_f32_16x16x32_bf16 v[120:123], v[184:187], v[212:215], v[120:123]
	v_mfma_f32_16x16x32_bf16 v[140:143], v[188:191], v[212:215], v[140:143]
.Lchk6_s4:
	ds_read_b128 v[208:211], v199 offset:8192
	s_waitcnt lgkmcnt(2)
	s_waitcnt vmcnt(10)
	s_cmp_le_u32 s99, 3
	s_cbranch_scc1 .Lchk6_s5
	v_mfma_f32_16x16x32_bf16 v[136:139], v[176:179], v[192:195], v[136:139]
	v_mfma_f32_16x16x32_bf16 v[128:131], v[180:183], v[192:195], v[128:131]
	v_mfma_f32_16x16x32_bf16 v[116:119], v[184:187], v[192:195], v[116:119]
	v_mfma_f32_16x16x32_bf16 v[112:115], v[188:191], v[192:195], v[112:115]
.Lchk6_s5:
	ds_read_b128 v[212:215], v199 offset:10240
	buffer_load_dwordx4 v[20:23], v197, s[24:27], s38 offen
	v_cvt_pk_bf16_f32 v31, v30, v31
	v_cvt_pk_bf16_f32 v30, v28, v29
	ds_write_b64 v198, v[30:31] offset:43520
	s_add_i32 s39, s9, 0xfff40000
	s_waitcnt lgkmcnt(2)
	s_cmp_le_u32 s99, 4
	s_cbranch_scc1 .Lchk6_s6
	v_mfma_f32_16x16x32_bf16 v[100:103], v[176:179], v[208:211], v[100:103]
	v_mfma_f32_16x16x32_bf16 v[92:95], v[180:183], v[208:211], v[92:95]
	v_mfma_f32_16x16x32_bf16 v[88:91], v[184:187], v[208:211], v[88:91]
	v_mfma_f32_16x16x32_bf16 v[108:111], v[188:191], v[208:211], v[108:111]

; #define G_DMA_A(kt, AO) do { G_DMA1(kt, AO, 0); G_DMA1(kt, AO, 1); G_DMA1(kt, AO, 2); G_DMA1(kt, AO, 3); if (MF == 9) G_DMA5(kt, AO); } while (0)
; #define G_ISSUE_B(kt) do { const unsigned _sb = (unsigned)(kt) * 4u * kstepB; \
;         _Pragma("unroll") for (int _i = 0; _i < 8; ++_i) sb[_i] = bload16(_i < 4 ? rsB0 : rsB1, vob, _sb + (_i & 3) * kstepB); } while (0)
; #define G_WRITE_B(BO) do { \
;         _Pragma("unroll") for (int _i = 0; _i < 8; ++_i) *(LAS u32x2*)(b_wr + (BO) + (_i & 3) * (16 * G_BSTRIDE) + (_i >> 2) * SLAB1) = pack4(__builtin_bit_cast(f32x4, sb[_i])); } while (0)
; #define G_ENDTILE(VM) do { asm volatile("s_waitcnt vmcnt(" #VM ")" ::: "memory"); \
;         asm volatile("s_waitcnt lgkmcnt(0)" ::: "memory"); __builtin_amdgcn_s_barrier(); asm volatile("" ::: "memory"); } while (0)
;     ...
;     __builtin_amdgcn_s_barrier();
;     G_DMA_A(0, G_A0); G_ISSUE_B(0); G_WRITE_B(G_B0);
;     __builtin_amdgcn_sched_barrier(0);
;     G_ISSUE_B(1);
;     __builtin_amdgcn_sched_barrier(0);
;     G_ENDTILE(8);
;     for (int ui = 0;; ++ui) {
; #pragma unroll
;         for (int m = 0; m < MF; ++m)
; #pragma unroll
;             for (int n = 0; n < 4; ++n) acc[m][n] = (f32x4){0.f, 0.f, 0.f, 0.f};
;         for (int t = 0; t < nt - 2; t += 2) {
;             G_TILE(G_A0, G_B0, true, G_B1, G_A1, t + 1, true, t + 2, (void)0);
;             G_ENDTILE(8);
;             G_TILE(G_A1, G_B1, true, G_B0, G_A0, t + 2, true, t + 3, (void)0);
;             G_ENDTILE(8);
;         }
.Lchk6_s7:
	ds_read_b128 v[208:211], v199 offset:14336
	v_cvt_pk_bf16_f32 v19, v18, v19
	v_cvt_pk_bf16_f32 v18, v16, v17
	ds_write_b64 v198, v[18:19] offset:52224
	s_add_i32 s43, s9, 0xfff60000
	buffer_load_dwordx4 v[28:31], v197, s[24:27], s39 offen
	s_waitcnt lgkmcnt(2)
	s_cmp_le_u32 s99, 6
	s_cbranch_scc1 .Lchk6_s8
	v_mfma_f32_16x16x32_bf16 v[72:75], v[176:179], v[192:195], v[72:75]
	v_mfma_f32_16x16x32_bf16 v[64:67], v[180:183], v[192:195], v[64:67]
	v_mfma_f32_16x16x32_bf16 v[60:63], v[184:187], v[192:195], v[60:63]
	v_mfma_f32_16x16x32_bf16 v[76:79], v[188:191], v[192:195], v[76:79]
.Lchk6_s8:
	ds_read_b128 v[212:215], v199 offset:16384
	s_waitcnt lgkmcnt(2)
	s_waitcnt vmcnt(11)
	s_cmp_le_u32 s99, 7
	s_cbranch_scc1 .Lchk6_s9
	v_mfma_f32_16x16x32_bf16 v[68:71], v[176:179], v[208:211], v[68:71]
	v_mfma_f32_16x16x32_bf16 v[56:59], v[180:183], v[208:211], v[56:59]
	v_mfma_f32_16x16x32_bf16 v[52:55], v[184:187], v[208:211], v[52:55]
	v_mfma_f32_16x16x32_bf16 v[48:51], v[188:191], v[208:211], v[48:51]
.Lchk6_s9:
	ds_read_b128 v[192:195], v199 offset:1024
	buffer_load_dwordx4 v[16:19], v197, s[24:27], s43 offen
	v_cvt_pk_bf16_f32 v27, v26, v27
	v_cvt_pk_bf16_f32 v26, v24, v25
	ds_write_b64 v198, v[26:27] offset:60928
	s_add_i32 s45, s9, 0xfff80000
	ds_read_b128 v[208:211], v199 offset:3072
	s_waitcnt lgkmcnt(3)
	s_cmp_le_u32 s99, 8
	s_cbranch_scc1 .Lchk6_s10
	v_mfma_f32_16x16x32_bf16 v[44:47], v[176:179], v[212:215], v[44:47]
	v_mfma_f32_16x16x32_bf16 v[40:43], v[180:183], v[212:215], v[40:43]
	v_mfma_f32_16x16x32_bf16 v[36:39], v[184:187], v[212:215], v[36:39]
	v_mfma_f32_16x16x32_bf16 v[32:35], v[188:191], v[212:215], v[32:35]
.Lchk6_s10:
	ds_read_b64_tr_b16 v[246:247], v206 offset:17408
	ds_read_b64_tr_b16 v[218:219], v206 offset:17440
	ds_read_b64_tr_b16 v[244:245], v205 offset:17408
	ds_read_b64_tr_b16 v[216:217], v205 offset:17440
	ds_read_b64_tr_b16 v[248:249], v205 offset:17472
	ds_read_b64_tr_b16 v[250:251], v206 offset:17472
	ds_read_b64_tr_b16 v[252:253], v205 offset:17504
	ds_read_b64_tr_b16 v[254:255], v206 offset:17504
	s_waitcnt lgkmcnt(5)
	s_waitcnt vmcnt(11)
	s_waitcnt lgkmcnt(4)
	s_waitcnt lgkmcnt(2)
	s_waitcnt lgkmcnt(0)
	s_cmp_le_u32 s99, 0
	s_cbranch_scc1 .Lchk6_s11
	v_mfma_f32_16x16x32_bf16 v[172:175], v[244:247], v[192:195], v[172:175]
	v_mfma_f32_16x16x32_bf16 v[168:171], v[216:219], v[192:195], v[168:171]
	v_mfma_f32_16x16x32_bf16 v[164:167], v[248:251], v[192:195], v[164:167]
	v_mfma_f32_16x16x32_bf16 v[160:163], v[252:255], v[192:195], v[160:163]
.Lchk6_s11:
	ds_read_b128 v[188:191], v199 offset:5120
	buffer_load_dwordx4 v[24:27], v197, s[24:27], s45 offen
	v_cvt_pk_bf16_f32 v15, v14, v15
	v_cvt_pk_bf16_f32 v14, v12, v13
	ds_write_b64 v198, v[14:15] offset:35072
	s_cmp_le_u32 s99, 1
	s_cbranch_scc1 .Lchk6_s12
	v_mfma_f32_16x16x32_bf16 v[156:159], v[244:247], v[208:211], v[156:159]
	v_mfma_f32_16x16x32_bf16 v[152:155], v[216:219], v[208:211], v[152:155]
	v_mfma_f32_16x16x32_bf16 v[148:151], v[248:251], v[208:211], v[148:151]
	v_mfma_f32_16x16x32_bf16 v[144:147], v[252:255], v[208:211], v[144:147]
.Lchk6_s12:
	ds_read_b128 v[192:195], v199 offset:7168
	s_waitcnt lgkmcnt(2)
	s_waitcnt vmcnt(10)
	s_cmp_le_u32 s99, 2
	s_cbranch_scc1 .Lchk6_s13
	v_mfma_f32_16x16x32_bf16 v[132:135], v[244:247], v[188:191], v[132:135]
	v_mfma_f32_16x16x32_bf16 v[124:127], v[216:219], v[188:191], v[124:127]
	v_mfma_f32_16x16x32_bf16 v[120:123], v[248:251], v[188:191], v[120:123]
	v_mfma_f32_16x16x32_bf16 v[140:143], v[252:255], v[188:191], v[140:143]
.Lchk6_s13:
	ds_read_b128 v[208:211], v199 offset:9216
	buffer_load_dwordx4 v[12:15], v197, s[16:19], s38 offen
	v_cvt_pk_bf16_f32 v7, v6, v7
	v_cvt_pk_bf16_f32 v6, v4, v5
	ds_write_b64 v198, v[6:7] offset:43776
	s_waitcnt lgkmcnt(2)
	s_cmp_le_u32 s99, 3
	s_cbranch_scc1 .Lchk6_s14
	v_mfma_f32_16x16x32_bf16 v[136:139], v[244:247], v[192:195], v[136:139]
	v_mfma_f32_16x16x32_bf16 v[128:131], v[216:219], v[192:195], v[128:131]
	v_mfma_f32_16x16x32_bf16 v[116:119], v[248:251], v[192:195], v[116:119]
	v_mfma_f32_16x16x32_bf16 v[112:115], v[252:255], v[192:195], v[112:115]

; #define G_DMA_A(kt, AO) do { G_DMA1(kt, AO, 0); G_DMA1(kt, AO, 1); G_DMA1(kt, AO, 2); G_DMA1(kt, AO, 3); if (MF == 9) G_DMA5(kt, AO); } while (0)
; #define G_ISSUE_B(kt) do { const unsigned _sb = (unsigned)(kt) * 4u * kstepB; \
;         _Pragma("unroll") for (int _i = 0; _i < 8; ++_i) sb[_i] = bload16(_i < 4 ? rsB0 : rsB1, vob, _sb + (_i & 3) * kstepB); } while (0)
; #define G_WRITE_B(BO) do { \
;         _Pragma("unroll") for (int _i = 0; _i < 8; ++_i) *(LAS u32x2*)(b_wr + (BO) + (_i & 3) * (16 * G_BSTRIDE) + (_i >> 2) * SLAB1) = pack4(__builtin_bit_cast(f32x4, sb[_i])); } while (0)
; #define G_ENDTILE(VM) do { asm volatile("s_waitcnt vmcnt(" #VM ")" ::: "memory"); \
;         asm volatile("s_waitcnt lgkmcnt(0)" ::: "memory"); __builtin_amdgcn_s_barrier(); asm volatile("" ::: "memory"); } while (0)
;     ...
;     __builtin_amdgcn_s_barrier();
;     G_DMA_A(0, G_A0); G_ISSUE_B(0); G_WRITE_B(G_B0);
;     __builtin_amdgcn_sched_barrier(0);
;     G_ISSUE_B(1);
;     __builtin_amdgcn_sched_barrier(0);
;     G_ENDTILE(8);
;     for (int ui = 0;; ++ui) {
; #pragma unroll
;         for (int m = 0; m < MF; ++m)
; #pragma unroll
;             for (int n = 0; n < 4; ++n) acc[m][n] = (f32x4){0.f, 0.f, 0.f, 0.f};
;         for (int t = 0; t < nt - 2; t += 2) {
;             G_TILE(G_A0, G_B0, true, G_B1, G_A1, t + 1, true, t + 2, (void)0);
;             G_ENDTILE(8);
;             G_TILE(G_A1, G_B1, true, G_B0, G_A0, t + 2, true, t + 3, (void)0);
;             G_ENDTILE(8);
;         }
.Lchk6_s15:
	ds_read_b128 v[192:195], v199 offset:13312
	v_cvt_pk_bf16_f32 v3, v2, v3
	v_cvt_pk_bf16_f32 v2, v0, v1
	ds_write_b64 v198, v[2:3] offset:52480
	buffer_load_dwordx4 v[4:7], v197, s[16:19], s39 offen
	s_waitcnt lgkmcnt(2)
	s_cmp_le_u32 s99, 5
	s_cbranch_scc1 .Lchk6_s16
	v_mfma_f32_16x16x32_bf16 v[104:107], v[244:247], v[188:191], v[104:107]
	v_mfma_f32_16x16x32_bf16 v[96:99], v[216:219], v[188:191], v[96:99]
	v_mfma_f32_16x16x32_bf16 v[84:87], v[248:251], v[188:191], v[84:87]
	v_mfma_f32_16x16x32_bf16 v[80:83], v[252:255], v[188:191], v[80:83]
.Lchk6_s16:
	ds_read_b128 v[208:211], v199 offset:15360
	s_waitcnt lgkmcnt(2)
	s_waitcnt vmcnt(11)
	s_cmp_le_u32 s99, 6
	s_cbranch_scc1 .Lchk6_s17
	v_mfma_f32_16x16x32_bf16 v[72:75], v[244:247], v[192:195], v[72:75]
	v_mfma_f32_16x16x32_bf16 v[64:67], v[216:219], v[192:195], v[64:67]
	v_mfma_f32_16x16x32_bf16 v[60:63], v[248:251], v[192:195], v[60:63]
	v_mfma_f32_16x16x32_bf16 v[76:79], v[252:255], v[192:195], v[76:79]
.Lchk6_s17:
	ds_read_b128 v[236:239], v199 offset:17408
	buffer_load_dwordx4 v[0:3], v197, s[16:19], s43 offen
	v_cvt_pk_bf16_f32 v11, v10, v11
	v_cvt_pk_bf16_f32 v10, v8, v9
	ds_write_b64 v198, v[10:11] offset:61184
	s_waitcnt lgkmcnt(2)
	s_cmp_le_u32 s99, 7
	s_cbranch_scc1 .Lchk6_s18
	v_mfma_f32_16x16x32_bf16 v[68:71], v[244:247], v[208:211], v[68:71]
	v_mfma_f32_16x16x32_bf16 v[56:59], v[216:219], v[208:211], v[56:59]
	v_mfma_f32_16x16x32_bf16 v[52:55], v[248:251], v[208:211], v[52:55]
	v_mfma_f32_16x16x32_bf16 v[48:51], v[252:255], v[208:211], v[48:51]
.Lchk6_s18:
	s_waitcnt lgkmcnt(1)
	buffer_load_dwordx4 v[8:11], v197, s[16:19], s45 offen
	s_waitcnt vmcnt(8)
	s_mov_b32 m0, s49
	s_waitcnt lgkmcnt(0)
	s_barrier
	ds_read_b64_tr_b16 v[178:179], v206 offset:34816
	ds_read_b64_tr_b16 v[176:177], v205 offset:34816
	ds_read_b64_tr_b16 v[180:181], v205 offset:34848
	ds_read_b64_tr_b16 v[184:185], v205 offset:34880
	ds_read_b64_tr_b16 v[188:189], v205 offset:34912
	ds_read_b128 v[192:195], v199 offset:36864
	ds_read_b64_tr_b16 v[182:183], v206 offset:34848
	ds_read_b64_tr_b16 v[186:187], v206 offset:34880
	ds_read_b64_tr_b16 v[190:191], v206 offset:34912
	ds_read_b128 v[208:211], v199 offset:38912
	ds_read_b128 v[212:215], v199 offset:40960
	buffer_load_dwordx4 v200, s[20:23], s36 offen lds
	s_mov_b32 m0, s68
	s_cmp_le_u32 s99, 8
	s_cbranch_scc1 .Lchk6_s19
	v_mfma_f32_16x16x32_bf16 v[44:47], v[244:247], v[236:239], v[44:47]
	v_mfma_f32_16x16x32_bf16 v[40:43], v[216:219], v[236:239], v[40:43]
	v_mfma_f32_16x16x32_bf16 v[36:39], v[248:251], v[236:239], v[36:39]
	v_mfma_f32_16x16x32_bf16 v[32:35], v[252:255], v[236:239], v[32:35]

; #define G_DMA_A(kt, AO) do { G_DMA1(kt, AO, 0); G_DMA1(kt, AO, 1); G_DMA1(kt, AO, 2); G_DMA1(kt, AO, 3); if (MF == 9) G_DMA5(kt, AO); } while (0)
; #define G_ISSUE_B(kt) do { const unsigned _sb = (unsigned)(kt) * 4u * kstepB; \
;         _Pragma("unroll") for (int _i = 0; _i < 8; ++_i) sb[_i] = bload16(_i < 4 ? rsB0 : rsB1, vob, _sb + (_i & 3) * kstepB); } while (0)
; #define G_WRITE_B(BO) do { \
;         _Pragma("unroll") for (int _i = 0; _i < 8; ++_i) *(LAS u32x2*)(b_wr + (BO) + (_i & 3) * (16 * G_BSTRIDE) + (_i >> 2) * SLAB1) = pack4(__builtin_bit_cast(f32x4, sb[_i])); } while (0)
; #define G_ENDTILE(VM) do { asm volatile("s_waitcnt vmcnt(" #VM ")" ::: "memory"); \
;         asm volatile("s_waitcnt lgkmcnt(0)" ::: "memory"); __builtin_amdgcn_s_barrier(); asm volatile("" ::: "memory"); } while (0)
;     ...
;     __builtin_amdgcn_s_barrier();
;     G_DMA_A(0, G_A0); G_ISSUE_B(0); G_WRITE_B(G_B0);
;     __builtin_amdgcn_sched_barrier(0);
;     G_ISSUE_B(1);
;     __builtin_amdgcn_sched_barrier(0);
;     G_ENDTILE(8);
;     for (int ui = 0;; ++ui) {
; #pragma unroll
;         for (int m = 0; m < MF; ++m)
; #pragma unroll
;             for (int n = 0; n < 4; ++n) acc[m][n] = (f32x4){0.f, 0.f, 0.f, 0.f};
;         for (int t = 0; t < nt - 2; t += 2) {
;             G_TILE(G_A0, G_B0, true, G_B1, G_A1, t + 1, true, t + 2, (void)0);
;             G_ENDTILE(8);
;             G_TILE(G_A1, G_B1, true, G_B0, G_A0, t + 2, true, t + 3, (void)0);
;             G_ENDTILE(8);
;         }
.Lchk6_s21:
	ds_read_b128 v[192:195], v199 offset:43008
	v_cvt_pk_bf16_f32 v23, v22, v23
	v_cvt_pk_bf16_f32 v22, v20, v21
	ds_write_b64 v198, v[22:23]
	s_waitcnt lgkmcnt(2)
	s_cmp_le_u32 s99, 2
	s_cbranch_scc1 .Lchk6_s22
	v_mfma_f32_16x16x32_bf16 v[132:135], v[176:179], v[212:215], v[132:135]
	v_mfma_f32_16x16x32_bf16 v[124:127], v[180:183], v[212:215], v[124:127]
	v_mfma_f32_16x16x32_bf16 v[120:123], v[184:187], v[212:215], v[120:123]
	v_mfma_f32_16x16x32_bf16 v[140:143], v[188:191], v[212:215], v[140:143]
.Lchk6_s22:
	ds_read_b128 v[208:211], v199 offset:45056
	s_waitcnt lgkmcnt(2)
	s_waitcnt vmcnt(11)
	s_cmp_le_u32 s99, 3
	s_cbranch_scc1 .Lchk6_s23
	v_mfma_f32_16x16x32_bf16 v[136:139], v[176:179], v[192:195], v[136:139]
	v_mfma_f32_16x16x32_bf16 v[128:131], v[180:183], v[192:195], v[128:131]
	v_mfma_f32_16x16x32_bf16 v[116:119], v[184:187], v[192:195], v[116:119]
	v_mfma_f32_16x16x32_bf16 v[112:115], v[188:191], v[192:195], v[112:115]
.Lchk6_s23:
	ds_read_b128 v[212:215], v199 offset:47104
	buffer_load_dwordx4 v[20:23], v197, s[24:27], s38 offen
	v_cvt_pk_bf16_f32 v31, v30, v31
	v_cvt_pk_bf16_f32 v30, v28, v29
	ds_write_b64 v198, v[30:31] offset:8704
	s_add_i32 s39, s9, 0xfffc0000
	s_waitcnt lgkmcnt(2)
	s_cmp_le_u32 s99, 4
	s_cbranch_scc1 .Lchk6_s24
	v_mfma_f32_16x16x32_bf16 v[100:103], v[176:179], v[208:211], v[100:103]
	v_mfma_f32_16x16x32_bf16 v[92:95], v[180:183], v[208:211], v[92:95]
	v_mfma_f32_16x16x32_bf16 v[88:91], v[184:187], v[208:211], v[88:91]
	v_mfma_f32_16x16x32_bf16 v[108:111], v[188:191], v[208:211], v[108:111]
.Lchk6_s24:
	ds_read_b128 v[192:195], v199 offset:49152
	s_waitcnt lgkmcnt(2)
	s_waitcnt vmcnt(11)
	s_cmp_le_u32 s99, 5
	s_cbranch_scc1 .Lchk6_s25
	v_mfma_f32_16x16x32_bf16 v[104:107], v[176:179], v[212:215], v[104:107]
	v_mfma_f32_16x16x32_bf16 v[96:99], v[180:183], v[212:215], v[96:99]
	v_mfma_f32_16x16x32_bf16 v[84:87], v[184:187], v[212:215], v[84:87]
	v_mfma_f32_16x16x32_bf16 v[80:83], v[188:191], v[212:215], v[80:83]
.Lchk6_s25:
	ds_read_b128 v[208:211], v199 offset:51200
	buffer_load_dwordx4 v[28:31], v197, s[24:27], s39 offen
	v_cvt_pk_bf16_f32 v19, v18, v19
	v_cvt_pk_bf16_f32 v18, v16, v17
	ds_write_b64 v198, v[18:19] offset:17408
	s_add_i32 s43, s9, 0xfffe0000
	s_waitcnt lgkmcnt(2)
	s_cmp_le_u32 s99, 6
	s_cbranch_scc1 .Lchk6_s26
	v_mfma_f32_16x16x32_bf16 v[72:75], v[176:179], v[192:195], v[72:75]
	v_mfma_f32_16x16x32_bf16 v[64:67], v[180:183], v[192:195], v[64:67]
	v_mfma_f32_16x16x32_bf16 v[60:63], v[184:187], v[192:195], v[60:63]
	v_mfma_f32_16x16x32_bf16 v[76:79], v[188:191], v[192:195], v[76:79]
.Lchk6_s26:
	ds_read_b128 v[212:215], v199 offset:53248
	s_waitcnt lgkmcnt(2)
	s_waitcnt vmcnt(11)
	s_cmp_le_u32 s99, 7
	s_cbranch_scc1 .Lchk6_s27
	v_mfma_f32_16x16x32_bf16 v[68:71], v[176:179], v[208:211], v[68:71]
	v_mfma_f32_16x16x32_bf16 v[56:59], v[180:183], v[208:211], v[56:59]
	v_mfma_f32_16x16x32_bf16 v[52:55], v[184:187], v[208:211], v[52:55]
	v_mfma_f32_16x16x32_bf16 v[48:51], v[188:191], v[208:211], v[48:51]
.Lchk6_s27:
	ds_read_b128 v[192:195], v199 offset:37888
	buffer_load_dwordx4 v[16:19], v197, s[24:27], s43 offen
	v_cvt_pk_bf16_f32 v27, v26, v27
	v_cvt_pk_bf16_f32 v26, v24, v25
	ds_write_b64 v198, v[26:27] offset:26112
	s_waitcnt lgkmcnt(2)
	s_cmp_le_u32 s99, 8
	s_cbranch_scc1 .Lchk6_s28
	v_mfma_f32_16x16x32_bf16 v[44:47], v[176:179], v[212:215], v[44:47]
	v_mfma_f32_16x16x32_bf16 v[40:43], v[180:183], v[212:215], v[40:43]
	v_mfma_f32_16x16x32_bf16 v[36:39], v[184:187], v[212:215], v[36:39]
	v_mfma_f32_16x16x32_bf16 v[32:35], v[188:191], v[212:215], v[32:35]
.Lchk6_s28:
	ds_read_b128 v[176:179], v199 offset:39936
	ds_read_b64_tr_b16 v[244:245], v205 offset:52224
	ds_read_b64_tr_b16 v[248:249], v205 offset:52256
	ds_read_b64_tr_b16 v[216:217], v205 offset:52288
	ds_read_b64_tr_b16 v[220:221], v205 offset:52320
	ds_read_b64_tr_b16 v[246:247], v206 offset:52224
	ds_read_b64_tr_b16 v[250:251], v206 offset:52256
	ds_read_b64_tr_b16 v[218:219], v206 offset:52288
	ds_read_b64_tr_b16 v[222:223], v206 offset:52320
	s_waitcnt lgkmcnt(3)
	s_waitcnt vmcnt(11)
	s_waitcnt lgkmcnt(2)
	s_waitcnt lgkmcnt(1)
	s_waitcnt lgkmcnt(0)
	s_cmp_le_u32 s99, 0
	s_cbranch_scc1 .Lchk6_s29
	v_mfma_f32_16x16x32_bf16 v[172:175], v[244:247], v[192:195], v[172:175]
	v_mfma_f32_16x16x32_bf16 v[168:171], v[248:251], v[192:195], v[168:171]
	v_mfma_f32_16x16x32_bf16 v[164:167], v[216:219], v[192:195], v[164:167]
	v_mfma_f32_16x16x32_bf16 v[160:163], v[220:223], v[192:195], v[160:163]
; #define G_DMA_A(kt, AO) do { G_DMA1(kt, AO, 0); G_DMA1(kt, AO, 1); G_DMA1(kt, AO, 2); G_DMA1(kt, AO, 3); if (MF == 9) G_DMA5(kt, AO); } while (0)
; #define G_ISSUE_B(kt) do { const unsigned _sb = (unsigned)(kt) * 4u * kstepB; \
;         _Pragma("unroll") for (int _i = 0; _i < 8; ++_i) sb[_i] = bload16(_i < 4 ? rsB0 : rsB1, vob, _sb + (_i & 3) * kstepB); } while (0)
; #define G_WRITE_B(BO) do { \
;         _Pragma("unroll") for (int _i = 0; _i < 8; ++_i) *(LAS u32x2*)(b_wr + (BO) + (_i & 3) * (16 * G_BSTRIDE) + (_i >> 2) * SLAB1) = pack4(__builtin_bit_cast(f32x4, sb[_i])); } while (0)
; #define G_ENDTILE(VM) do { asm volatile("s_waitcnt vmcnt(" #VM ")" ::: "memory"); \
;         asm volatile("s_waitcnt lgkmcnt(0)" ::: "memory"); __builtin_amdgcn_s_barrier(); asm volatile("" ::: "memory"); } while (0)
;     ...
;     __builtin_amdgcn_s_barrier();
;     G_DMA_A(0, G_A0); G_ISSUE_B(0); G_WRITE_B(G_B0);
;     __builtin_amdgcn_sched_barrier(0);
;     G_ISSUE_B(1);
;     __builtin_amdgcn_sched_barrier(0);
;     G_ENDTILE(8);
;     for (int ui = 0;; ++ui) {
; #pragma unroll
;         for (int m = 0; m < MF; ++m)
; #pragma unroll
;             for (int n = 0; n < 4; ++n) acc[m][n] = (f32x4){0.f, 0.f, 0.f, 0.f};
;         for (int t = 0; t < nt - 2; t += 2) {
;             G_TILE(G_A0, G_B0, true, G_B1, G_A1, t + 1, true, t + 2, (void)0);
;             G_ENDTILE(8);
;             G_TILE(G_A1, G_B1, true, G_B0, G_A0, t + 2, true, t + 3, (void)0);
;             G_ENDTILE(8);
;         }
.Lchk6_s29:
	ds_read_b128 v[184:187], v199 offset:41984
	buffer_load_dwordx4 v[24:27], v197, s[24:27], s9 offen
	v_cvt_pk_bf16_f32 v15, v14, v15
	v_cvt_pk_bf16_f32 v14, v12, v13
	ds_write_b64 v198, v[14:15] offset:256
	s_cmp_le_u32 s99, 1
	s_cbranch_scc1 .Lchk6_s30
	v_mfma_f32_16x16x32_bf16 v[156:159], v[244:247], v[176:179], v[156:159]
	v_mfma_f32_16x16x32_bf16 v[152:155], v[248:251], v[176:179], v[152:155]
	v_mfma_f32_16x16x32_bf16 v[148:151], v[216:219], v[176:179], v[148:151]
	v_mfma_f32_16x16x32_bf16 v[144:147], v[220:223], v[176:179], v[144:147]
.Lchk6_s30:
	ds_read_b128 v[188:191], v199 offset:44032
	s_waitcnt lgkmcnt(2)
	s_waitcnt vmcnt(11)
	s_cmp_le_u32 s99, 2
	s_cbranch_scc1 .Lchk6_s31
	v_mfma_f32_16x16x32_bf16 v[132:135], v[244:247], v[184:187], v[132:135]
	v_mfma_f32_16x16x32_bf16 v[124:127], v[248:251], v[184:187], v[124:127]
	v_mfma_f32_16x16x32_bf16 v[120:123], v[216:219], v[184:187], v[120:123]
	v_mfma_f32_16x16x32_bf16 v[140:143], v[220:223], v[184:187], v[140:143]
.Lchk6_s31:
	ds_read_b128 v[176:179], v199 offset:46080
	buffer_load_dwordx4 v[12:15], v197, s[16:19], s38 offen
	v_cvt_pk_bf16_f32 v7, v6, v7
	v_cvt_pk_bf16_f32 v6, v4, v5
	ds_write_b64 v198, v[6:7] offset:8960
	s_waitcnt lgkmcnt(2)
	s_cmp_le_u32 s99, 3
	s_cbranch_scc1 .Lchk6_s32
	v_mfma_f32_16x16x32_bf16 v[136:139], v[244:247], v[188:191], v[136:139]
	v_mfma_f32_16x16x32_bf16 v[128:131], v[248:251], v[188:191], v[128:131]
	v_mfma_f32_16x16x32_bf16 v[116:119], v[216:219], v[188:191], v[116:119]
	v_mfma_f32_16x16x32_bf16 v[112:115], v[220:223], v[188:191], v[112:115]
.Lchk6_s32:
	ds_read_b128 v[184:187], v199 offset:48128
	s_waitcnt lgkmcnt(2)
	s_waitcnt vmcnt(11)
	s_cmp_le_u32 s99, 4
	s_cbranch_scc1 .Lchk6_s33
	v_mfma_f32_16x16x32_bf16 v[100:103], v[244:247], v[176:179], v[100:103]
	v_mfma_f32_16x16x32_bf16 v[92:95], v[248:251], v[176:179], v[92:95]
	v_mfma_f32_16x16x32_bf16 v[88:91], v[216:219], v[176:179], v[88:91]
	v_mfma_f32_16x16x32_bf16 v[108:111], v[220:223], v[176:179], v[108:111]
.Lchk6_s33:
	ds_read_b128 v[188:191], v199 offset:50176
	buffer_load_dwordx4 v[4:7], v197, s[16:19], s39 offen
	v_cvt_pk_bf16_f32 v3, v2, v3
	v_cvt_pk_bf16_f32 v2, v0, v1
	ds_write_b64 v198, v[2:3] offset:17664
	s_waitcnt lgkmcnt(2)
	s_cmp_le_u32 s99, 5
	s_cbranch_scc1 .Lchk6_s34
	v_mfma_f32_16x16x32_bf16 v[104:107], v[244:247], v[184:187], v[104:107]
	v_mfma_f32_16x16x32_bf16 v[96:99], v[248:251], v[184:187], v[96:99]
	v_mfma_f32_16x16x32_bf16 v[84:87], v[216:219], v[184:187], v[84:87]
	v_mfma_f32_16x16x32_bf16 v[80:83], v[220:223], v[184:187], v[80:83]
.Lchk6_s34:
	ds_read_b128 v[176:179], v199 offset:52224
	s_waitcnt lgkmcnt(2)
	s_waitcnt vmcnt(11)
	s_cmp_le_u32 s99, 6
	s_cbranch_scc1 .Lchk6_s35
	v_mfma_f32_16x16x32_bf16 v[72:75], v[244:247], v[188:191], v[72:75]
	v_mfma_f32_16x16x32_bf16 v[64:67], v[248:251], v[188:191], v[64:67]
	v_mfma_f32_16x16x32_bf16 v[60:63], v[216:219], v[188:191], v[60:63]
	v_mfma_f32_16x16x32_bf16 v[76:79], v[220:223], v[188:191], v[76:79]
.Lchk6_s35:
	ds_read_b128 v[252:255], v199 offset:54272
	buffer_load_dwordx4 v[0:3], v197, s[16:19], s43 offen
	v_cvt_pk_bf16_f32 v11, v10, v11
	v_cvt_pk_bf16_f32 v10, v8, v9
	ds_write_b64 v198, v[10:11] offset:26368
	s_waitcnt lgkmcnt(2)
	s_cmp_le_u32 s99, 7
	s_cbranch_scc1 .Lchk6_s36
	v_mfma_f32_16x16x32_bf16 v[68:71], v[244:247], v[176:179], v[68:71]
	v_mfma_f32_16x16x32_bf16 v[56:59], v[248:251], v[176:179], v[56:59]
	v_mfma_f32_16x16x32_bf16 v[52:55], v[216:219], v[176:179], v[52:55]
	v_mfma_f32_16x16x32_bf16 v[48:51], v[220:223], v[176:179], v[48:51]
.Lchk6_s36:
	s_waitcnt lgkmcnt(1)
	buffer_load_dwordx4 v[8:11], v197, s[16:19], s9 offen
	s_waitcnt vmcnt(8)
	s_waitcnt lgkmcnt(0)
	s_barrier
	s_add_i32 s8, s8, 2
	s_add_i32 s9, s9, 0x100000
	s_addk_i32 s36, 0x100
	s_cmp_ge_i32 s8, s84
	s_cbranch_scc0 .Lchk6_loop
	s_cmp_le_u32 s99, 8
	s_cbranch_scc1 .Lchk6_s37
	v_mfma_f32_16x16x32_bf16 v[44:47], v[244:247], v[252:255], v[44:47]
	v_mfma_f32_16x16x32_bf16 v[40:43], v[248:251], v[252:255], v[40:43]
	v_mfma_f32_16x16x32_bf16 v[36:39], v[216:219], v[252:255], v[36:39]
	v_mfma_f32_16x16x32_bf16 v[32:35], v[220:223], v[252:255], v[32:35]

; #define G_DMA_A(kt, AO) do { G_DMA1(kt, AO, 0); G_DMA1(kt, AO, 1); G_DMA1(kt, AO, 2); G_DMA1(kt, AO, 3); if (MF == 9) G_DMA5(kt, AO); } while (0)
; #define G_ISSUE_B(kt) do { const unsigned _sb = (unsigned)(kt) * 4u * kstepB; \
;         _Pragma("unroll") for (int _i = 0; _i < 8; ++_i) sb[_i] = bload16(_i < 4 ? rsB0 : rsB1, vob, _sb + (_i & 3) * kstepB); } while (0)
; #define G_WRITE_B(BO) do { \
;         _Pragma("unroll") for (int _i = 0; _i < 8; ++_i) *(LAS u32x2*)(b_wr + (BO) + (_i & 3) * (16 * G_BSTRIDE) + (_i >> 2) * SLAB1) = pack4(__builtin_bit_cast(f32x4, sb[_i])); } while (0)
; #define G_ENDTILE(VM) do { asm volatile("s_waitcnt vmcnt(" #VM ")" ::: "memory"); \
;         asm volatile("s_waitcnt lgkmcnt(0)" ::: "memory"); __builtin_amdgcn_s_barrier(); asm volatile("" ::: "memory"); } while (0)
;     ...
;     __builtin_amdgcn_s_barrier();
;     G_DMA_A(0, G_A0); G_ISSUE_B(0); G_WRITE_B(G_B0);
;     __builtin_amdgcn_sched_barrier(0);
;     G_ISSUE_B(1);
;     __builtin_amdgcn_sched_barrier(0);
;     G_ENDTILE(8);
;     for (int ui = 0;; ++ui) {
; #pragma unroll
;         for (int m = 0; m < MF; ++m)
; #pragma unroll
;             for (int n = 0; n < 4; ++n) acc[m][n] = (f32x4){0.f, 0.f, 0.f, 0.f};
;         for (int t = 0; t < nt - 2; t += 2) {
;             G_TILE(G_A0, G_B0, true, G_B1, G_A1, t + 1, true, t + 2, (void)0);
;             G_ENDTILE(8);
;             G_TILE(G_A1, G_B1, true, G_B0, G_A0, t + 2, true, t + 3, (void)0);
;             G_ENDTILE(8);
;         }
.LBB0_899:
	s_mov_b32 m0, s64
	s_add_i32 s69, s45, 0xffffff80
	ds_read_b64_tr_b16 v[170:171], v166
	ds_read_b64_tr_b16 v[172:173], v167
	ds_read_b64_tr_b16 v[176:177], v167 offset:32
	ds_read_b128 v[178:181], v162
	ds_read_b64_tr_b16 v[174:175], v166 offset:32
	ds_read_b64_tr_b16 v[182:183], v166 offset:64
	ds_read_b64_tr_b16 v[186:187], v166 offset:96
	ds_read_b64_tr_b16 v[184:185], v167 offset:64
	ds_read_b64_tr_b16 v[188:189], v167 offset:96
	ds_read_b128 v[190:193], v162 offset:2048
	ds_read_b128 v[198:201], v162 offset:4096
	buffer_load_dwordx4 v163, s[20:23], s69 offen lds
	s_mov_b32 m0, s63
	v_mfma_f32_16x16x32_bf16 v[44:47], v[244:247], v[252:255], v[44:47]
	v_mfma_f32_16x16x32_bf16 v[40:43], v[248:251], v[252:255], v[40:43]
	v_mfma_f32_16x16x32_bf16 v[36:39], v[202:205], v[252:255], v[36:39]
	v_mfma_f32_16x16x32_bf16 v[32:35], v[206:209], v[252:255], v[32:35]
	s_waitcnt lgkmcnt(7)
	v_mfma_f32_16x16x32_bf16 v[156:159], v[170:173], v[178:181], v[156:159]
	buffer_load_dwordx4 v165, s[20:23], s69 offen lds
	s_mov_b32 m0, s62
	s_nop 0
	buffer_load_dwordx4 v164, s[20:23], s69 offen lds
	s_mov_b32 m0, s31
	s_waitcnt lgkmcnt(6)
	v_mfma_f32_16x16x32_bf16 v[152:155], v[174:177], v[178:181], v[152:155]
	buffer_load_dwordx4 v168, s[20:23], s69 offen lds
	s_add_i32 s69, s13, 0xfff20000
	s_waitcnt lgkmcnt(3)
	v_mfma_f32_16x16x32_bf16 v[148:151], v[182:185], v[178:181], v[148:151]
	s_waitcnt lgkmcnt(2)
	v_mfma_f32_16x16x32_bf16 v[144:147], v[186:189], v[178:181], v[144:147]
	s_waitcnt lgkmcnt(1)
	v_mfma_f32_16x16x32_bf16 v[140:143], v[170:173], v[190:193], v[140:143]
	ds_read_b128 v[178:181], v162 offset:6144
	s_waitcnt vmcnt(11)
	v_cvt_pk_bf16_f32 v15, v14, v15
	v_cvt_pk_bf16_f32 v14, v12, v13
	v_mfma_f32_16x16x32_bf16 v[136:139], v[174:177], v[190:193], v[136:139]
	ds_write_b64 v161, v[14:15] offset:34816
	v_mfma_f32_16x16x32_bf16 v[132:135], v[182:185], v[190:193], v[132:135]
	v_mfma_f32_16x16x32_bf16 v[128:131], v[186:189], v[190:193], v[128:131]
	s_waitcnt lgkmcnt(2)
	v_mfma_f32_16x16x32_bf16 v[124:127], v[170:173], v[198:201], v[124:127]
	ds_read_b128 v[190:193], v162 offset:8192
	v_mfma_f32_16x16x32_bf16 v[120:123], v[174:177], v[198:201], v[120:123]
	v_mfma_f32_16x16x32_bf16 v[116:119], v[182:185], v[198:201], v[116:119]
	v_mfma_f32_16x16x32_bf16 v[112:115], v[186:189], v[198:201], v[112:115]
	s_waitcnt lgkmcnt(2)
	v_mfma_f32_16x16x32_bf16 v[108:111], v[170:173], v[178:181], v[108:111]
	ds_read_b128 v[198:201], v162 offset:10240
	buffer_load_dwordx4 v[12:15], v160, s[24:27], s69 offen
	s_waitcnt vmcnt(11)
	v_cvt_pk_bf16_f32 v3, v2, v3
	v_cvt_pk_bf16_f32 v2, v0, v1
	v_mfma_f32_16x16x32_bf16 v[104:107], v[174:177], v[178:181], v[104:107]
	ds_write_b64 v161, v[2:3] offset:43520
	v_mfma_f32_16x16x32_bf16 v[100:103], v[182:185], v[178:181], v[100:103]
	v_mfma_f32_16x16x32_bf16 v[96:99], v[186:189], v[178:181], v[96:99]
	s_add_i32 s74, s13, 0xfff40000
	s_waitcnt lgkmcnt(2)
	v_mfma_f32_16x16x32_bf16 v[92:95], v[170:173], v[190:193], v[92:95]
	ds_read_b128 v[178:181], v162 offset:12288
	v_mfma_f32_16x16x32_bf16 v[88:91], v[174:177], v[190:193], v[88:91]
	v_mfma_f32_16x16x32_bf16 v[84:87], v[182:185], v[190:193], v[84:87]
	v_mfma_f32_16x16x32_bf16 v[80:83], v[186:189], v[190:193], v[80:83]
	s_waitcnt lgkmcnt(2)
	v_mfma_f32_16x16x32_bf16 v[76:79], v[170:173], v[198:201], v[76:79]
	ds_read_b128 v[190:193], v162 offset:14336
	buffer_load_dwordx4 v[0:3], v160, s[24:27], s74 offen
	s_waitcnt vmcnt(11)
	v_cvt_pk_bf16_f32 v31, v30, v31
	v_cvt_pk_bf16_f32 v30, v28, v29
	v_mfma_f32_16x16x32_bf16 v[72:75], v[174:177], v[198:201], v[72:75]
	ds_write_b64 v161, v[30:31] offset:52224
	v_mfma_f32_16x16x32_bf16 v[68:71], v[182:185], v[198:201], v[68:71]
	v_mfma_f32_16x16x32_bf16 v[64:67], v[186:189], v[198:201], v[64:67]
	s_add_i32 s75, s13, 0xfff60000
	s_waitcnt lgkmcnt(2)
	v_mfma_f32_16x16x32_bf16 v[60:63], v[170:173], v[178:181], v[60:63]
	ds_read_b128 v[198:201], v162 offset:1024
	v_mfma_f32_16x16x32_bf16 v[56:59], v[174:177], v[178:181], v[56:59]
	v_mfma_f32_16x16x32_bf16 v[52:55], v[182:185], v[178:181], v[52:55]
	v_mfma_f32_16x16x32_bf16 v[48:51], v[186:189], v[178:181], v[48:51]
	s_waitcnt lgkmcnt(2)
	v_mfma_f32_16x16x32_bf16 v[44:47], v[170:173], v[190:193], v[44:47]
	ds_read_b128 v[170:173], v162 offset:3072
	buffer_load_dwordx4 v[28:31], v160, s[24:27], s75 offen
	s_waitcnt vmcnt(11)
	v_cvt_pk_bf16_f32 v27, v26, v27
	v_cvt_pk_bf16_f32 v26, v24, v25
	v_mfma_f32_16x16x32_bf16 v[40:43], v[174:177], v[190:193], v[40:43]
	ds_read_b64_tr_b16 v[244:245], v166 offset:17408
	ds_read_b64_tr_b16 v[248:249], v166 offset:17440
	ds_read_b64_tr_b16 v[202:203], v166 offset:17472
	ds_read_b64_tr_b16 v[206:207], v166 offset:17504
	ds_read_b64_tr_b16 v[246:247], v167 offset:17408
	ds_read_b64_tr_b16 v[250:251], v167 offset:17440
	ds_read_b64_tr_b16 v[204:205], v167 offset:17472
	ds_read_b64_tr_b16 v[208:209], v167 offset:17504
	ds_write_b64 v161, v[26:27] offset:60928
	v_mfma_f32_16x16x32_bf16 v[36:39], v[182:185], v[190:193], v[36:39]
	v_mfma_f32_16x16x32_bf16 v[32:35], v[186:189], v[190:193], v[32:35]
	s_add_i32 s76, s13, 0xfff80000
	s_waitcnt lgkmcnt(4)
	v_mfma_f32_16x16x32_bf16 v[156:159], v[244:247], v[198:201], v[156:159]
	ds_read_b128 v[182:185], v162 offset:5120
	s_waitcnt lgkmcnt(4)
	v_mfma_f32_16x16x32_bf16 v[152:155], v[248:251], v[198:201], v[152:155]
	s_waitcnt lgkmcnt(3)
	v_mfma_f32_16x16x32_bf16 v[148:151], v[202:205], v[198:201], v[148:151]
	s_waitcnt lgkmcnt(2)
	v_mfma_f32_16x16x32_bf16 v[144:147], v[206:209], v[198:201], v[144:147]
	v_mfma_f32_16x16x32_bf16 v[140:143], v[244:247], v[170:173], v[140:143]
	ds_read_b128 v[186:189], v162 offset:7168
	buffer_load_dwordx4 v[24:27], v160, s[24:27], s76 offen
	s_waitcnt vmcnt(11)
; #define G_DMA_A(kt, AO) do { G_DMA1(kt, AO, 0); G_DMA1(kt, AO, 1); G_DMA1(kt, AO, 2); G_DMA1(kt, AO, 3); if (MF == 9) G_DMA5(kt, AO); } while (0)
; #define G_ISSUE_B(kt) do { const unsigned _sb = (unsigned)(kt) * 4u * kstepB; \
;         _Pragma("unroll") for (int _i = 0; _i < 8; ++_i) sb[_i] = bload16(_i < 4 ? rsB0 : rsB1, vob, _sb + (_i & 3) * kstepB); } while (0)
; #define G_WRITE_B(BO) do { \
;         _Pragma("unroll") for (int _i = 0; _i < 8; ++_i) *(LAS u32x2*)(b_wr + (BO) + (_i & 3) * (16 * G_BSTRIDE) + (_i >> 2) * SLAB1) = pack4(__builtin_bit_cast(f32x4, sb[_i])); } while (0)
; #define G_ENDTILE(VM) do { asm volatile("s_waitcnt vmcnt(" #VM ")" ::: "memory"); \
;         asm volatile("s_waitcnt lgkmcnt(0)" ::: "memory"); __builtin_amdgcn_s_barrier(); asm volatile("" ::: "memory"); } while (0)
;     ...
;     __builtin_amdgcn_s_barrier();
;     G_DMA_A(0, G_A0); G_ISSUE_B(0); G_WRITE_B(G_B0);
;     __builtin_amdgcn_sched_barrier(0);
;     G_ISSUE_B(1);
;     __builtin_amdgcn_sched_barrier(0);
;     G_ENDTILE(8);
;     for (int ui = 0;; ++ui) {
; #pragma unroll
;         for (int m = 0; m < MF; ++m)
; #pragma unroll
;             for (int n = 0; n < 4; ++n) acc[m][n] = (f32x4){0.f, 0.f, 0.f, 0.f};
;         for (int t = 0; t < nt - 2; t += 2) {
;             G_TILE(G_A0, G_B0, true, G_B1, G_A1, t + 1, true, t + 2, (void)0);
;             G_ENDTILE(8);
;             G_TILE(G_A1, G_B1, true, G_B0, G_A0, t + 2, true, t + 3, (void)0);
;             G_ENDTILE(8);
;         }
	v_cvt_pk_bf16_f32 v23, v22, v23
	v_cvt_pk_bf16_f32 v22, v20, v21
	v_mfma_f32_16x16x32_bf16 v[136:139], v[248:251], v[170:173], v[136:139]
	ds_write_b64 v161, v[22:23] offset:35072
	v_mfma_f32_16x16x32_bf16 v[132:135], v[202:205], v[170:173], v[132:135]
	v_mfma_f32_16x16x32_bf16 v[128:131], v[206:209], v[170:173], v[128:131]
	s_waitcnt lgkmcnt(2)
	v_mfma_f32_16x16x32_bf16 v[124:127], v[244:247], v[182:185], v[124:127]
	ds_read_b128 v[170:173], v162 offset:9216
	v_mfma_f32_16x16x32_bf16 v[120:123], v[248:251], v[182:185], v[120:123]
	v_mfma_f32_16x16x32_bf16 v[116:119], v[202:205], v[182:185], v[116:119]
	v_mfma_f32_16x16x32_bf16 v[112:115], v[206:209], v[182:185], v[112:115]
	s_waitcnt lgkmcnt(2)
	v_mfma_f32_16x16x32_bf16 v[108:111], v[244:247], v[186:189], v[108:111]
	ds_read_b128 v[182:185], v162 offset:11264
	buffer_load_dwordx4 v[20:23], v160, s[16:19], s69 offen
	s_waitcnt vmcnt(11)
	v_cvt_pk_bf16_f32 v7, v6, v7
	v_cvt_pk_bf16_f32 v6, v4, v5
	v_mfma_f32_16x16x32_bf16 v[104:107], v[248:251], v[186:189], v[104:107]
	ds_write_b64 v161, v[6:7] offset:43776
	v_mfma_f32_16x16x32_bf16 v[100:103], v[202:205], v[186:189], v[100:103]
	v_mfma_f32_16x16x32_bf16 v[96:99], v[206:209], v[186:189], v[96:99]
	s_waitcnt lgkmcnt(2)
	v_mfma_f32_16x16x32_bf16 v[92:95], v[244:247], v[170:173], v[92:95]
	ds_read_b128 v[186:189], v162 offset:13312
	v_mfma_f32_16x16x32_bf16 v[88:91], v[248:251], v[170:173], v[88:91]
	v_mfma_f32_16x16x32_bf16 v[84:87], v[202:205], v[170:173], v[84:87]
	v_mfma_f32_16x16x32_bf16 v[80:83], v[206:209], v[170:173], v[80:83]
	s_waitcnt lgkmcnt(2)
	v_mfma_f32_16x16x32_bf16 v[76:79], v[244:247], v[182:185], v[76:79]
	ds_read_b128 v[252:255], v162 offset:15360
	buffer_load_dwordx4 v[4:7], v160, s[16:19], s74 offen
	s_waitcnt vmcnt(11)
	v_cvt_pk_bf16_f32 v11, v10, v11
	v_cvt_pk_bf16_f32 v10, v8, v9
	v_mfma_f32_16x16x32_bf16 v[72:75], v[248:251], v[182:185], v[72:75]
	ds_write_b64 v161, v[10:11] offset:52480
	v_mfma_f32_16x16x32_bf16 v[68:71], v[202:205], v[182:185], v[68:71]
	v_mfma_f32_16x16x32_bf16 v[64:67], v[206:209], v[182:185], v[64:67]
	s_waitcnt lgkmcnt(2)
	v_mfma_f32_16x16x32_bf16 v[60:63], v[244:247], v[186:189], v[60:63]
	v_mfma_f32_16x16x32_bf16 v[56:59], v[248:251], v[186:189], v[56:59]
	v_mfma_f32_16x16x32_bf16 v[52:55], v[202:205], v[186:189], v[52:55]
	v_mfma_f32_16x16x32_bf16 v[48:51], v[206:209], v[186:189], v[48:51]
	s_waitcnt lgkmcnt(1)
	buffer_load_dwordx4 v[8:11], v160, s[16:19], s75 offen
	s_waitcnt vmcnt(11)
	v_cvt_pk_bf16_f32 v19, v18, v19
	v_cvt_pk_bf16_f32 v18, v16, v17
	ds_write_b64 v161, v[18:19] offset:61184
	buffer_load_dwordx4 v[16:19], v160, s[16:19], s76 offen
	s_waitcnt vmcnt(8)
	s_mov_b32 m0, s56
	s_waitcnt lgkmcnt(0)
	s_barrier
	ds_read_b64_tr_b16 v[170:171], v166 offset:34816
	ds_read_b64_tr_b16 v[172:173], v167 offset:34816
	ds_read_b64_tr_b16 v[176:177], v167 offset:34848
	ds_read_b128 v[178:181], v162 offset:32768
	ds_read_b64_tr_b16 v[174:175], v166 offset:34848
	ds_read_b64_tr_b16 v[182:183], v166 offset:34880
	ds_read_b64_tr_b16 v[186:187], v166 offset:34912
	ds_read_b64_tr_b16 v[184:185], v167 offset:34880
	ds_read_b64_tr_b16 v[188:189], v167 offset:34912
	ds_read_b128 v[190:193], v162 offset:34816
	ds_read_b128 v[198:201], v162 offset:36864
	buffer_load_dwordx4 v163, s[20:23], s45 offen lds
	s_mov_b32 m0, s57
	v_mfma_f32_16x16x32_bf16 v[44:47], v[244:247], v[252:255], v[44:47]
	v_mfma_f32_16x16x32_bf16 v[40:43], v[248:251], v[252:255], v[40:43]
	v_mfma_f32_16x16x32_bf16 v[36:39], v[202:205], v[252:255], v[36:39]
	v_mfma_f32_16x16x32_bf16 v[32:35], v[206:209], v[252:255], v[32:35]
	s_waitcnt lgkmcnt(7)
	v_mfma_f32_16x16x32_bf16 v[156:159], v[170:173], v[178:181], v[156:159]
	buffer_load_dwordx4 v165, s[20:23], s45 offen lds
	s_mov_b32 m0, s58
	s_add_i32 s69, s13, 0xfffa0000
	buffer_load_dwordx4 v164, s[20:23], s45 offen lds
	s_mov_b32 m0, s59
	s_waitcnt lgkmcnt(6)
	v_mfma_f32_16x16x32_bf16 v[152:155], v[174:177], v[178:181], v[152:155]
	buffer_load_dwordx4 v168, s[20:23], s45 offen lds
	s_waitcnt lgkmcnt(3)
	v_mfma_f32_16x16x32_bf16 v[148:151], v[182:185], v[178:181], v[148:151]
	s_waitcnt lgkmcnt(2)
	v_mfma_f32_16x16x32_bf16 v[144:147], v[186:189], v[178:181], v[144:147]
	s_waitcnt lgkmcnt(1)
	v_mfma_f32_16x16x32_bf16 v[140:143], v[170:173], v[190:193], v[140:143]
	ds_read_b128 v[178:181], v162 offset:38912
	s_waitcnt vmcnt(11)
	v_cvt_pk_bf16_f32 v15, v14, v15
	v_cvt_pk_bf16_f32 v14, v12, v13
	v_mfma_f32_16x16x32_bf16 v[136:139], v[174:177], v[190:193], v[136:139]
	ds_write_b64 v161, v[14:15]
	v_mfma_f32_16x16x32_bf16 v[132:135], v[182:185], v[190:193], v[132:135]
	v_mfma_f32_16x16x32_bf16 v[128:131], v[186:189], v[190:193], v[128:131]
	s_waitcnt lgkmcnt(2)
	v_mfma_f32_16x16x32_bf16 v[124:127], v[170:173], v[198:201], v[124:127]
	ds_read_b128 v[190:193], v162 offset:40960
	v_mfma_f32_16x16x32_bf16 v[120:123], v[174:177], v[198:201], v[120:123]
	v_mfma_f32_16x16x32_bf16 v[116:119], v[182:185], v[198:201], v[116:119]
	v_mfma_f32_16x16x32_bf16 v[112:115], v[186:189], v[198:201], v[112:115]
	s_waitcnt lgkmcnt(2)
	v_mfma_f32_16x16x32_bf16 v[108:111], v[170:173], v[178:181], v[108:111]
	ds_read_b128 v[198:201], v162 offset:43008
	buffer_load_dwordx4 v[12:15], v160, s[24:27], s69 offen
	s_waitcnt vmcnt(11)
	v_cvt_pk_bf16_f32 v3, v2, v3
	v_cvt_pk_bf16_f32 v2, v0, v1
	v_mfma_f32_16x16x32_bf16 v[104:107], v[174:177], v[178:181], v[104:107]
	ds_write_b64 v161, v[2:3] offset:8704
	v_mfma_f32_16x16x32_bf16 v[100:103], v[182:185], v[178:181], v[100:103]
	v_mfma_f32_16x16x32_bf16 v[96:99], v[186:189], v[178:181], v[96:99]
	s_add_i32 s74, s13, 0xfffc0000
	s_waitcnt lgkmcnt(2)
; #define G_DMA_A(kt, AO) do { G_DMA1(kt, AO, 0); G_DMA1(kt, AO, 1); G_DMA1(kt, AO, 2); G_DMA1(kt, AO, 3); if (MF == 9) G_DMA5(kt, AO); } while (0)
; #define G_ISSUE_B(kt) do { const unsigned _sb = (unsigned)(kt) * 4u * kstepB; \
;         _Pragma("unroll") for (int _i = 0; _i < 8; ++_i) sb[_i] = bload16(_i < 4 ? rsB0 : rsB1, vob, _sb + (_i & 3) * kstepB); } while (0)
; #define G_WRITE_B(BO) do { \
;         _Pragma("unroll") for (int _i = 0; _i < 8; ++_i) *(LAS u32x2*)(b_wr + (BO) + (_i & 3) * (16 * G_BSTRIDE) + (_i >> 2) * SLAB1) = pack4(__builtin_bit_cast(f32x4, sb[_i])); } while (0)
; #define G_ENDTILE(VM) do { asm volatile("s_waitcnt vmcnt(" #VM ")" ::: "memory"); \
;         asm volatile("s_waitcnt lgkmcnt(0)" ::: "memory"); __builtin_amdgcn_s_barrier(); asm volatile("" ::: "memory"); } while (0)
;     ...
;     __builtin_amdgcn_s_barrier();
;     G_DMA_A(0, G_A0); G_ISSUE_B(0); G_WRITE_B(G_B0);
;     __builtin_amdgcn_sched_barrier(0);
;     G_ISSUE_B(1);
;     __builtin_amdgcn_sched_barrier(0);
;     G_ENDTILE(8);
;     for (int ui = 0;; ++ui) {
; #pragma unroll
;         for (int m = 0; m < MF; ++m)
; #pragma unroll
;             for (int n = 0; n < 4; ++n) acc[m][n] = (f32x4){0.f, 0.f, 0.f, 0.f};
;         for (int t = 0; t < nt - 2; t += 2) {
;             G_TILE(G_A0, G_B0, true, G_B1, G_A1, t + 1, true, t + 2, (void)0);
;             G_ENDTILE(8);
;             G_TILE(G_A1, G_B1, true, G_B0, G_A0, t + 2, true, t + 3, (void)0);
;             G_ENDTILE(8);
;         }
	v_mfma_f32_16x16x32_bf16 v[92:95], v[170:173], v[190:193], v[92:95]
	ds_read_b128 v[178:181], v162 offset:45056
	v_mfma_f32_16x16x32_bf16 v[88:91], v[174:177], v[190:193], v[88:91]
	v_mfma_f32_16x16x32_bf16 v[84:87], v[182:185], v[190:193], v[84:87]
	v_mfma_f32_16x16x32_bf16 v[80:83], v[186:189], v[190:193], v[80:83]
	s_waitcnt lgkmcnt(2)
	v_mfma_f32_16x16x32_bf16 v[76:79], v[170:173], v[198:201], v[76:79]
	ds_read_b128 v[190:193], v162 offset:47104
	buffer_load_dwordx4 v[0:3], v160, s[24:27], s74 offen
	s_waitcnt vmcnt(11)
	v_cvt_pk_bf16_f32 v31, v30, v31
	v_cvt_pk_bf16_f32 v30, v28, v29
	v_mfma_f32_16x16x32_bf16 v[72:75], v[174:177], v[198:201], v[72:75]
	ds_write_b64 v161, v[30:31] offset:17408
	v_mfma_f32_16x16x32_bf16 v[68:71], v[182:185], v[198:201], v[68:71]
	v_mfma_f32_16x16x32_bf16 v[64:67], v[186:189], v[198:201], v[64:67]
	s_add_i32 s75, s13, 0xfffe0000
	s_waitcnt lgkmcnt(2)
	v_mfma_f32_16x16x32_bf16 v[60:63], v[170:173], v[178:181], v[60:63]
	ds_read_b128 v[198:201], v162 offset:33792
	v_mfma_f32_16x16x32_bf16 v[56:59], v[174:177], v[178:181], v[56:59]
	v_mfma_f32_16x16x32_bf16 v[52:55], v[182:185], v[178:181], v[52:55]
	v_mfma_f32_16x16x32_bf16 v[48:51], v[186:189], v[178:181], v[48:51]
	s_waitcnt lgkmcnt(2)
	v_mfma_f32_16x16x32_bf16 v[44:47], v[170:173], v[190:193], v[44:47]
	ds_read_b128 v[170:173], v162 offset:35840
	buffer_load_dwordx4 v[28:31], v160, s[24:27], s75 offen
	s_waitcnt vmcnt(11)
	v_cvt_pk_bf16_f32 v27, v26, v27
	v_cvt_pk_bf16_f32 v26, v24, v25
	v_mfma_f32_16x16x32_bf16 v[40:43], v[174:177], v[190:193], v[40:43]
	ds_read_b64_tr_b16 v[244:245], v166 offset:52224
	ds_read_b64_tr_b16 v[248:249], v166 offset:52256
	ds_read_b64_tr_b16 v[202:203], v166 offset:52288
	ds_read_b64_tr_b16 v[206:207], v166 offset:52320
	ds_read_b64_tr_b16 v[246:247], v167 offset:52224
	ds_read_b64_tr_b16 v[250:251], v167 offset:52256
	ds_read_b64_tr_b16 v[204:205], v167 offset:52288
	ds_read_b64_tr_b16 v[208:209], v167 offset:52320
	ds_write_b64 v161, v[26:27] offset:26112
	v_mfma_f32_16x16x32_bf16 v[36:39], v[182:185], v[190:193], v[36:39]
	v_mfma_f32_16x16x32_bf16 v[32:35], v[186:189], v[190:193], v[32:35]
	s_waitcnt lgkmcnt(4)
	v_mfma_f32_16x16x32_bf16 v[156:159], v[244:247], v[198:201], v[156:159]
	ds_read_b128 v[182:185], v162 offset:37888
	s_waitcnt lgkmcnt(4)
	v_mfma_f32_16x16x32_bf16 v[152:155], v[248:251], v[198:201], v[152:155]
	s_waitcnt lgkmcnt(3)
	v_mfma_f32_16x16x32_bf16 v[148:151], v[202:205], v[198:201], v[148:151]
	s_waitcnt lgkmcnt(2)
	v_mfma_f32_16x16x32_bf16 v[144:147], v[206:209], v[198:201], v[144:147]
	v_mfma_f32_16x16x32_bf16 v[140:143], v[244:247], v[170:173], v[140:143]
	ds_read_b128 v[186:189], v162 offset:39936
	buffer_load_dwordx4 v[24:27], v160, s[24:27], s13 offen
	s_waitcnt vmcnt(11)
	v_cvt_pk_bf16_f32 v23, v22, v23
	v_cvt_pk_bf16_f32 v22, v20, v21
	v_mfma_f32_16x16x32_bf16 v[136:139], v[248:251], v[170:173], v[136:139]
	ds_write_b64 v161, v[22:23] offset:256
	v_mfma_f32_16x16x32_bf16 v[132:135], v[202:205], v[170:173], v[132:135]
	v_mfma_f32_16x16x32_bf16 v[128:131], v[206:209], v[170:173], v[128:131]
	s_waitcnt lgkmcnt(2)
	v_mfma_f32_16x16x32_bf16 v[124:127], v[244:247], v[182:185], v[124:127]
	ds_read_b128 v[170:173], v162 offset:41984
	v_mfma_f32_16x16x32_bf16 v[120:123], v[248:251], v[182:185], v[120:123]
	v_mfma_f32_16x16x32_bf16 v[116:119], v[202:205], v[182:185], v[116:119]
	v_mfma_f32_16x16x32_bf16 v[112:115], v[206:209], v[182:185], v[112:115]
	s_waitcnt lgkmcnt(2)
	v_mfma_f32_16x16x32_bf16 v[108:111], v[244:247], v[186:189], v[108:111]
	ds_read_b128 v[182:185], v162 offset:44032
	buffer_load_dwordx4 v[20:23], v160, s[16:19], s69 offen
	s_waitcnt vmcnt(11)
	v_cvt_pk_bf16_f32 v7, v6, v7
	v_cvt_pk_bf16_f32 v6, v4, v5
	v_mfma_f32_16x16x32_bf16 v[104:107], v[248:251], v[186:189], v[104:107]
	ds_write_b64 v161, v[6:7] offset:8960
	v_mfma_f32_16x16x32_bf16 v[100:103], v[202:205], v[186:189], v[100:103]
	v_mfma_f32_16x16x32_bf16 v[96:99], v[206:209], v[186:189], v[96:99]
	s_waitcnt lgkmcnt(2)
	v_mfma_f32_16x16x32_bf16 v[92:95], v[244:247], v[170:173], v[92:95]
	ds_read_b128 v[186:189], v162 offset:46080
	v_mfma_f32_16x16x32_bf16 v[88:91], v[248:251], v[170:173], v[88:91]
	v_mfma_f32_16x16x32_bf16 v[84:87], v[202:205], v[170:173], v[84:87]
	v_mfma_f32_16x16x32_bf16 v[80:83], v[206:209], v[170:173], v[80:83]
	s_waitcnt lgkmcnt(2)
	v_mfma_f32_16x16x32_bf16 v[76:79], v[244:247], v[182:185], v[76:79]
	ds_read_b128 v[252:255], v162 offset:48128
	buffer_load_dwordx4 v[4:7], v160, s[16:19], s74 offen
	s_waitcnt vmcnt(11)
	v_cvt_pk_bf16_f32 v11, v10, v11
	v_cvt_pk_bf16_f32 v10, v8, v9
	v_mfma_f32_16x16x32_bf16 v[72:75], v[248:251], v[182:185], v[72:75]
	ds_write_b64 v161, v[10:11] offset:17664
	v_mfma_f32_16x16x32_bf16 v[68:71], v[202:205], v[182:185], v[68:71]
	v_mfma_f32_16x16x32_bf16 v[64:67], v[206:209], v[182:185], v[64:67]
	s_waitcnt lgkmcnt(2)
	v_mfma_f32_16x16x32_bf16 v[60:63], v[244:247], v[186:189], v[60:63]
	v_mfma_f32_16x16x32_bf16 v[56:59], v[248:251], v[186:189], v[56:59]
	v_mfma_f32_16x16x32_bf16 v[52:55], v[202:205], v[186:189], v[52:55]
	v_mfma_f32_16x16x32_bf16 v[48:51], v[206:209], v[186:189], v[48:51]
	s_waitcnt lgkmcnt(1)
	buffer_load_dwordx4 v[8:11], v160, s[16:19], s75 offen
	s_waitcnt vmcnt(11)
	v_cvt_pk_bf16_f32 v19, v18, v19
	v_cvt_pk_bf16_f32 v18, v16, v17
	ds_write_b64 v161, v[18:19] offset:26368
	buffer_load_dwordx4 v[16:19], v160, s[16:19], s13 offen
	s_waitcnt vmcnt(8)
	s_waitcnt lgkmcnt(0)
	s_barrier
	s_add_i32 s12, s12, 2
	s_add_i32 s13, s13, 0x100000
	s_addk_i32 s45, 0x100
	s_cmp_ge_i32 s12, s30
	s_cbranch_scc0 .LBB0_899
	v_mfma_f32_16x16x32_bf16 v[44:47], v[244:247], v[252:255], v[44:47]
	v_mfma_f32_16x16x32_bf16 v[40:43], v[248:251], v[252:255], v[40:43]
	v_mfma_f32_16x16x32_bf16 v[36:39], v[202:205], v[252:255], v[36:39]
	v_mfma_f32_16x16x32_bf16 v[32:35], v[206:209], v[252:255], v[32:35]
	s_branch .LBB0_901

; #define G_DMA_A(kt, AO) do { G_DMA1(kt, AO, 0); G_DMA1(kt, AO, 1); G_DMA1(kt, AO, 2); G_DMA1(kt, AO, 3); if (MF == 9) G_DMA5(kt, AO); } while (0)
; #define G_ISSUE_B(kt) do { const unsigned _sb = (unsigned)(kt) * 4u * kstepB; \
;         _Pragma("unroll") for (int _i = 0; _i < 8; ++_i) sb[_i] = bload16(_i < 4 ? rsB0 : rsB1, vob, _sb + (_i & 3) * kstepB); } while (0)
; #define G_WRITE_B(BO) do { \
;         _Pragma("unroll") for (int _i = 0; _i < 8; ++_i) *(LAS u32x2*)(b_wr + (BO) + (_i & 3) * (16 * G_BSTRIDE) + (_i >> 2) * SLAB1) = pack4(__builtin_bit_cast(f32x4, sb[_i])); } while (0)
; #define G_ENDTILE(VM) do { asm volatile("s_waitcnt vmcnt(" #VM ")" ::: "memory"); \
;         asm volatile("s_waitcnt lgkmcnt(0)" ::: "memory"); __builtin_amdgcn_s_barrier(); asm volatile("" ::: "memory"); } while (0)
;     ...
;     __builtin_amdgcn_s_barrier();
;     G_DMA_A(0, G_A0); G_ISSUE_B(0); G_WRITE_B(G_B0);
;     __builtin_amdgcn_sched_barrier(0);
;     G_ISSUE_B(1);
;     __builtin_amdgcn_sched_barrier(0);
;     G_ENDTILE(8);
;     for (int ui = 0;; ++ui) {
; #pragma unroll
;         for (int m = 0; m < MF; ++m)
; #pragma unroll
;             for (int n = 0; n < 4; ++n) acc[m][n] = (f32x4){0.f, 0.f, 0.f, 0.f};
;         for (int t = 0; t < nt - 2; t += 2) {
;             G_TILE(G_A0, G_B0, true, G_B1, G_A1, t + 1, true, t + 2, (void)0);
;             G_ENDTILE(8);
;             G_TILE(G_A1, G_B1, true, G_B0, G_A0, t + 2, true, t + 3, (void)0);
;             G_ENDTILE(8);
;         }
.LBB0_1038:
	s_mov_b32 m0, s64
	s_add_i32 s5, s4, 0xffffff80
	ds_read_b64_tr_b16 v[160:161], v178
	ds_read_b64_tr_b16 v[162:163], v179
	ds_read_b64_tr_b16 v[166:167], v179 offset:32
	ds_read_b128 v[168:171], v175
	ds_read_b64_tr_b16 v[164:165], v178 offset:32
	ds_read_b64_tr_b16 v[182:183], v178 offset:64
	ds_read_b64_tr_b16 v[186:187], v178 offset:96
	ds_read_b64_tr_b16 v[184:185], v179 offset:64
	ds_read_b64_tr_b16 v[188:189], v179 offset:96
	ds_read_b128 v[190:193], v175 offset:2048
	ds_read_b128 v[194:197], v175 offset:4096
	buffer_load_dwordx4 v176, s[16:19], s5 offen lds
	s_mov_b32 m0, s63
	v_mfma_f32_16x16x32_bf16 v[44:47], v[244:247], v[252:255], v[44:47]
	v_mfma_f32_16x16x32_bf16 v[40:43], v[248:251], v[252:255], v[40:43]
	v_mfma_f32_16x16x32_bf16 v[36:39], v[198:201], v[252:255], v[36:39]
	v_mfma_f32_16x16x32_bf16 v[32:35], v[202:205], v[252:255], v[32:35]
	s_waitcnt lgkmcnt(7)
	v_mfma_f32_16x16x32_bf16 v[156:159], v[160:163], v[168:171], v[156:159]
	buffer_load_dwordx4 v177, s[16:19], s5 offen lds
	s_mov_b32 m0, s62
	s_nop 0
	buffer_load_dwordx4 v180, s[16:19], s5 offen lds
	s_mov_b32 m0, s61
	s_waitcnt lgkmcnt(6)
	v_mfma_f32_16x16x32_bf16 v[152:155], v[164:167], v[168:171], v[152:155]
	buffer_load_dwordx4 v181, s[16:19], s5 offen lds
	s_add_i32 s5, s1, 0xfff20000
	s_waitcnt lgkmcnt(3)
	v_mfma_f32_16x16x32_bf16 v[148:151], v[182:185], v[168:171], v[148:151]
	s_waitcnt lgkmcnt(2)
	v_mfma_f32_16x16x32_bf16 v[144:147], v[186:189], v[168:171], v[144:147]
	s_waitcnt lgkmcnt(1)
	v_mfma_f32_16x16x32_bf16 v[140:143], v[160:163], v[190:193], v[140:143]
	ds_read_b128 v[168:171], v175 offset:6144
	s_waitcnt vmcnt(11)
	v_cvt_pk_bf16_f32 v15, v14, v15
	v_cvt_pk_bf16_f32 v14, v12, v13
	v_mfma_f32_16x16x32_bf16 v[136:139], v[164:167], v[190:193], v[136:139]
	ds_write_b64 v174, v[14:15] offset:34816
	v_mfma_f32_16x16x32_bf16 v[132:135], v[182:185], v[190:193], v[132:135]
	v_mfma_f32_16x16x32_bf16 v[128:131], v[186:189], v[190:193], v[128:131]
	s_waitcnt lgkmcnt(2)
	v_mfma_f32_16x16x32_bf16 v[124:127], v[160:163], v[194:197], v[124:127]
	ds_read_b128 v[190:193], v175 offset:8192
	v_mfma_f32_16x16x32_bf16 v[120:123], v[164:167], v[194:197], v[120:123]
	v_mfma_f32_16x16x32_bf16 v[116:119], v[182:185], v[194:197], v[116:119]
	v_mfma_f32_16x16x32_bf16 v[112:115], v[186:189], v[194:197], v[112:115]
	s_waitcnt lgkmcnt(2)
	v_mfma_f32_16x16x32_bf16 v[108:111], v[160:163], v[168:171], v[108:111]
	ds_read_b128 v[194:197], v175 offset:10240
	buffer_load_dwordx4 v[12:15], v173, s[8:11], s5 offen
	s_waitcnt vmcnt(10)
	v_cvt_pk_bf16_f32 v31, v30, v31
	v_cvt_pk_bf16_f32 v30, v28, v29
	v_mfma_f32_16x16x32_bf16 v[104:107], v[164:167], v[168:171], v[104:107]
	ds_write_b64 v174, v[30:31] offset:43520
	v_mfma_f32_16x16x32_bf16 v[100:103], v[182:185], v[168:171], v[100:103]
	v_mfma_f32_16x16x32_bf16 v[96:99], v[186:189], v[168:171], v[96:99]
	s_add_i32 s20, s1, 0xfff40000
	s_waitcnt lgkmcnt(2)
	v_mfma_f32_16x16x32_bf16 v[92:95], v[160:163], v[190:193], v[92:95]
	ds_read_b128 v[168:171], v175 offset:12288
	v_mfma_f32_16x16x32_bf16 v[88:91], v[164:167], v[190:193], v[88:91]
	v_mfma_f32_16x16x32_bf16 v[84:87], v[182:185], v[190:193], v[84:87]
	v_mfma_f32_16x16x32_bf16 v[80:83], v[186:189], v[190:193], v[80:83]
	s_waitcnt lgkmcnt(2)
	v_mfma_f32_16x16x32_bf16 v[76:79], v[160:163], v[194:197], v[76:79]
	ds_read_b128 v[190:193], v175 offset:14336
	v_cvt_pk_bf16_f32 v7, v6, v7
	v_cvt_pk_bf16_f32 v6, v4, v5
	v_mfma_f32_16x16x32_bf16 v[72:75], v[164:167], v[194:197], v[72:75]
	ds_write_b64 v174, v[6:7] offset:52224
	v_mfma_f32_16x16x32_bf16 v[68:71], v[182:185], v[194:197], v[68:71]
	v_mfma_f32_16x16x32_bf16 v[64:67], v[186:189], v[194:197], v[64:67]
	s_add_i32 s21, s1, 0xfff60000
	buffer_load_dwordx4 v[28:31], v173, s[8:11], s20 offen
	s_waitcnt lgkmcnt(2)
	v_mfma_f32_16x16x32_bf16 v[60:63], v[160:163], v[168:171], v[60:63]
	ds_read_b128 v[194:197], v175 offset:1024
	v_mfma_f32_16x16x32_bf16 v[56:59], v[164:167], v[168:171], v[56:59]
	v_mfma_f32_16x16x32_bf16 v[52:55], v[182:185], v[168:171], v[52:55]
	v_mfma_f32_16x16x32_bf16 v[48:51], v[186:189], v[168:171], v[48:51]
	s_waitcnt lgkmcnt(2)
	v_mfma_f32_16x16x32_bf16 v[44:47], v[160:163], v[190:193], v[44:47]
	ds_read_b128 v[160:163], v175 offset:3072
	buffer_load_dwordx4 v[4:7], v173, s[8:11], s21 offen
	s_waitcnt vmcnt(11)
	v_cvt_pk_bf16_f32 v27, v26, v27
	v_cvt_pk_bf16_f32 v26, v24, v25
	v_mfma_f32_16x16x32_bf16 v[40:43], v[164:167], v[190:193], v[40:43]
	ds_read_b64_tr_b16 v[244:245], v178 offset:17408
	ds_read_b64_tr_b16 v[248:249], v178 offset:17440
	ds_read_b64_tr_b16 v[198:199], v178 offset:17472
	ds_read_b64_tr_b16 v[202:203], v178 offset:17504
	ds_read_b64_tr_b16 v[246:247], v179 offset:17408
	ds_read_b64_tr_b16 v[250:251], v179 offset:17440
	ds_read_b64_tr_b16 v[200:201], v179 offset:17472
	ds_read_b64_tr_b16 v[204:205], v179 offset:17504
	ds_write_b64 v174, v[26:27] offset:60928
	v_mfma_f32_16x16x32_bf16 v[36:39], v[182:185], v[190:193], v[36:39]
	v_mfma_f32_16x16x32_bf16 v[32:35], v[186:189], v[190:193], v[32:35]
	s_add_i32 s22, s1, 0xfff80000
	s_waitcnt lgkmcnt(4)
	v_mfma_f32_16x16x32_bf16 v[156:159], v[244:247], v[194:197], v[156:159]
	ds_read_b128 v[182:185], v175 offset:5120
	s_waitcnt lgkmcnt(4)
	v_mfma_f32_16x16x32_bf16 v[152:155], v[248:251], v[194:197], v[152:155]
	s_waitcnt lgkmcnt(3)
	v_mfma_f32_16x16x32_bf16 v[148:151], v[198:201], v[194:197], v[148:151]
	s_waitcnt lgkmcnt(2)
	v_mfma_f32_16x16x32_bf16 v[144:147], v[202:205], v[194:197], v[144:147]
	v_mfma_f32_16x16x32_bf16 v[140:143], v[244:247], v[160:163], v[140:143]
	ds_read_b128 v[186:189], v175 offset:7168
	buffer_load_dwordx4 v[24:27], v173, s[8:11], s22 offen
	s_waitcnt vmcnt(11)
; #define G_DMA_A(kt, AO) do { G_DMA1(kt, AO, 0); G_DMA1(kt, AO, 1); G_DMA1(kt, AO, 2); G_DMA1(kt, AO, 3); if (MF == 9) G_DMA5(kt, AO); } while (0)
; #define G_ISSUE_B(kt) do { const unsigned _sb = (unsigned)(kt) * 4u * kstepB; \
;         _Pragma("unroll") for (int _i = 0; _i < 8; ++_i) sb[_i] = bload16(_i < 4 ? rsB0 : rsB1, vob, _sb + (_i & 3) * kstepB); } while (0)
; #define G_WRITE_B(BO) do { \
;         _Pragma("unroll") for (int _i = 0; _i < 8; ++_i) *(LAS u32x2*)(b_wr + (BO) + (_i & 3) * (16 * G_BSTRIDE) + (_i >> 2) * SLAB1) = pack4(__builtin_bit_cast(f32x4, sb[_i])); } while (0)
; #define G_ENDTILE(VM) do { asm volatile("s_waitcnt vmcnt(" #VM ")" ::: "memory"); \
;         asm volatile("s_waitcnt lgkmcnt(0)" ::: "memory"); __builtin_amdgcn_s_barrier(); asm volatile("" ::: "memory"); } while (0)
;     ...
;     __builtin_amdgcn_s_barrier();
;     G_DMA_A(0, G_A0); G_ISSUE_B(0); G_WRITE_B(G_B0);
;     __builtin_amdgcn_sched_barrier(0);
;     G_ISSUE_B(1);
;     __builtin_amdgcn_sched_barrier(0);
;     G_ENDTILE(8);
;     for (int ui = 0;; ++ui) {
; #pragma unroll
;         for (int m = 0; m < MF; ++m)
; #pragma unroll
;             for (int n = 0; n < 4; ++n) acc[m][n] = (f32x4){0.f, 0.f, 0.f, 0.f};
;         for (int t = 0; t < nt - 2; t += 2) {
;             G_TILE(G_A0, G_B0, true, G_B1, G_A1, t + 1, true, t + 2, (void)0);
;             G_ENDTILE(8);
;             G_TILE(G_A1, G_B1, true, G_B0, G_A0, t + 2, true, t + 3, (void)0);
;             G_ENDTILE(8);
;         }
	v_cvt_pk_bf16_f32 v23, v22, v23
	v_cvt_pk_bf16_f32 v22, v20, v21
	v_mfma_f32_16x16x32_bf16 v[136:139], v[248:251], v[160:163], v[136:139]
	ds_write_b64 v174, v[22:23] offset:35072
	v_mfma_f32_16x16x32_bf16 v[132:135], v[198:201], v[160:163], v[132:135]
	v_mfma_f32_16x16x32_bf16 v[128:131], v[202:205], v[160:163], v[128:131]
	s_waitcnt lgkmcnt(2)
	v_mfma_f32_16x16x32_bf16 v[124:127], v[244:247], v[182:185], v[124:127]
	ds_read_b128 v[160:163], v175 offset:9216
	v_mfma_f32_16x16x32_bf16 v[120:123], v[248:251], v[182:185], v[120:123]
	v_mfma_f32_16x16x32_bf16 v[116:119], v[198:201], v[182:185], v[116:119]
	v_mfma_f32_16x16x32_bf16 v[112:115], v[202:205], v[182:185], v[112:115]
	s_waitcnt lgkmcnt(2)
	v_mfma_f32_16x16x32_bf16 v[108:111], v[244:247], v[186:189], v[108:111]
	ds_read_b128 v[182:185], v175 offset:11264
	buffer_load_dwordx4 v[20:23], v173, s[12:15], s5 offen
	s_waitcnt vmcnt(10)
	v_cvt_pk_bf16_f32 v11, v10, v11
	v_cvt_pk_bf16_f32 v10, v8, v9
	v_mfma_f32_16x16x32_bf16 v[104:107], v[248:251], v[186:189], v[104:107]
	ds_write_b64 v174, v[10:11] offset:43776
	v_mfma_f32_16x16x32_bf16 v[100:103], v[198:201], v[186:189], v[100:103]
	v_mfma_f32_16x16x32_bf16 v[96:99], v[202:205], v[186:189], v[96:99]
	s_waitcnt lgkmcnt(2)
	v_mfma_f32_16x16x32_bf16 v[92:95], v[244:247], v[160:163], v[92:95]
	ds_read_b128 v[186:189], v175 offset:13312
	v_mfma_f32_16x16x32_bf16 v[88:91], v[248:251], v[160:163], v[88:91]
	v_mfma_f32_16x16x32_bf16 v[84:87], v[198:201], v[160:163], v[84:87]
	v_mfma_f32_16x16x32_bf16 v[80:83], v[202:205], v[160:163], v[80:83]
	s_waitcnt lgkmcnt(2)
	v_mfma_f32_16x16x32_bf16 v[76:79], v[244:247], v[182:185], v[76:79]
	ds_read_b128 v[252:255], v175 offset:15360
	v_cvt_pk_bf16_f32 v3, v2, v3
	v_cvt_pk_bf16_f32 v2, v0, v1
	v_mfma_f32_16x16x32_bf16 v[72:75], v[248:251], v[182:185], v[72:75]
	ds_write_b64 v174, v[2:3] offset:52480
	v_mfma_f32_16x16x32_bf16 v[68:71], v[198:201], v[182:185], v[68:71]
	v_mfma_f32_16x16x32_bf16 v[64:67], v[202:205], v[182:185], v[64:67]
	buffer_load_dwordx4 v[8:11], v173, s[12:15], s20 offen
	s_waitcnt lgkmcnt(2)
	v_mfma_f32_16x16x32_bf16 v[60:63], v[244:247], v[186:189], v[60:63]
	v_mfma_f32_16x16x32_bf16 v[56:59], v[248:251], v[186:189], v[56:59]
	v_mfma_f32_16x16x32_bf16 v[52:55], v[198:201], v[186:189], v[52:55]
	v_mfma_f32_16x16x32_bf16 v[48:51], v[202:205], v[186:189], v[48:51]
	s_waitcnt lgkmcnt(1)
	buffer_load_dwordx4 v[0:3], v173, s[12:15], s21 offen
	s_waitcnt vmcnt(11)
	v_cvt_pk_bf16_f32 v19, v18, v19
	v_cvt_pk_bf16_f32 v18, v16, v17
	ds_write_b64 v174, v[18:19] offset:61184
	buffer_load_dwordx4 v[16:19], v173, s[12:15], s22 offen
	s_waitcnt vmcnt(8)
	s_mov_b32 m0, s45
	s_waitcnt lgkmcnt(0)
	s_barrier
	ds_read_b64_tr_b16 v[160:161], v178 offset:34816
	ds_read_b64_tr_b16 v[162:163], v179 offset:34816
	ds_read_b64_tr_b16 v[166:167], v179 offset:34848
	ds_read_b128 v[168:171], v175 offset:32768
	ds_read_b64_tr_b16 v[164:165], v178 offset:34848
	ds_read_b64_tr_b16 v[182:183], v178 offset:34880
	ds_read_b64_tr_b16 v[186:187], v178 offset:34912
	ds_read_b64_tr_b16 v[184:185], v179 offset:34880
	ds_read_b64_tr_b16 v[188:189], v179 offset:34912
	ds_read_b128 v[190:193], v175 offset:34816
	ds_read_b128 v[194:197], v175 offset:36864
	buffer_load_dwordx4 v176, s[16:19], s4 offen lds
	s_mov_b32 m0, s53
	v_mfma_f32_16x16x32_bf16 v[44:47], v[244:247], v[252:255], v[44:47]
	v_mfma_f32_16x16x32_bf16 v[40:43], v[248:251], v[252:255], v[40:43]
	v_mfma_f32_16x16x32_bf16 v[36:39], v[198:201], v[252:255], v[36:39]
	v_mfma_f32_16x16x32_bf16 v[32:35], v[202:205], v[252:255], v[32:35]
	s_waitcnt lgkmcnt(7)
	v_mfma_f32_16x16x32_bf16 v[156:159], v[160:163], v[168:171], v[156:159]
	buffer_load_dwordx4 v177, s[16:19], s4 offen lds
	s_mov_b32 m0, s54
	s_add_i32 s5, s1, 0xfffa0000
	buffer_load_dwordx4 v180, s[16:19], s4 offen lds
	s_mov_b32 m0, s55
	s_waitcnt lgkmcnt(6)
	v_mfma_f32_16x16x32_bf16 v[152:155], v[164:167], v[168:171], v[152:155]
	buffer_load_dwordx4 v181, s[16:19], s4 offen lds
	s_waitcnt lgkmcnt(3)
	v_mfma_f32_16x16x32_bf16 v[148:151], v[182:185], v[168:171], v[148:151]
	s_waitcnt lgkmcnt(2)
	v_mfma_f32_16x16x32_bf16 v[144:147], v[186:189], v[168:171], v[144:147]
	s_waitcnt lgkmcnt(1)
	v_mfma_f32_16x16x32_bf16 v[140:143], v[160:163], v[190:193], v[140:143]
	ds_read_b128 v[168:171], v175 offset:38912
	s_waitcnt vmcnt(11)
	v_cvt_pk_bf16_f32 v15, v14, v15
	v_cvt_pk_bf16_f32 v14, v12, v13
	v_mfma_f32_16x16x32_bf16 v[136:139], v[164:167], v[190:193], v[136:139]
	ds_write_b64 v174, v[14:15]
	v_mfma_f32_16x16x32_bf16 v[132:135], v[182:185], v[190:193], v[132:135]
	v_mfma_f32_16x16x32_bf16 v[128:131], v[186:189], v[190:193], v[128:131]
	s_waitcnt lgkmcnt(2)
	v_mfma_f32_16x16x32_bf16 v[124:127], v[160:163], v[194:197], v[124:127]
	ds_read_b128 v[190:193], v175 offset:40960
	v_mfma_f32_16x16x32_bf16 v[120:123], v[164:167], v[194:197], v[120:123]
	v_mfma_f32_16x16x32_bf16 v[116:119], v[182:185], v[194:197], v[116:119]
	v_mfma_f32_16x16x32_bf16 v[112:115], v[186:189], v[194:197], v[112:115]
	s_waitcnt lgkmcnt(2)
	v_mfma_f32_16x16x32_bf16 v[108:111], v[160:163], v[168:171], v[108:111]
	ds_read_b128 v[194:197], v175 offset:43008
	buffer_load_dwordx4 v[12:15], v173, s[8:11], s5 offen
	s_waitcnt vmcnt(11)
	v_cvt_pk_bf16_f32 v31, v30, v31
	v_cvt_pk_bf16_f32 v30, v28, v29
	v_mfma_f32_16x16x32_bf16 v[104:107], v[164:167], v[168:171], v[104:107]
	ds_write_b64 v174, v[30:31] offset:8704
	v_mfma_f32_16x16x32_bf16 v[100:103], v[182:185], v[168:171], v[100:103]
	v_mfma_f32_16x16x32_bf16 v[96:99], v[186:189], v[168:171], v[96:99]
	s_add_i32 s20, s1, 0xfffc0000
	s_waitcnt lgkmcnt(2)
; #define G_DMA_A(kt, AO) do { G_DMA1(kt, AO, 0); G_DMA1(kt, AO, 1); G_DMA1(kt, AO, 2); G_DMA1(kt, AO, 3); if (MF == 9) G_DMA5(kt, AO); } while (0)
; #define G_ISSUE_B(kt) do { const unsigned _sb = (unsigned)(kt) * 4u * kstepB; \
;         _Pragma("unroll") for (int _i = 0; _i < 8; ++_i) sb[_i] = bload16(_i < 4 ? rsB0 : rsB1, vob, _sb + (_i & 3) * kstepB); } while (0)
; #define G_WRITE_B(BO) do { \
;         _Pragma("unroll") for (int _i = 0; _i < 8; ++_i) *(LAS u32x2*)(b_wr + (BO) + (_i & 3) * (16 * G_BSTRIDE) + (_i >> 2) * SLAB1) = pack4(__builtin_bit_cast(f32x4, sb[_i])); } while (0)
; #define G_ENDTILE(VM) do { asm volatile("s_waitcnt vmcnt(" #VM ")" ::: "memory"); \
;         asm volatile("s_waitcnt lgkmcnt(0)" ::: "memory"); __builtin_amdgcn_s_barrier(); asm volatile("" ::: "memory"); } while (0)
;     ...
;     __builtin_amdgcn_s_barrier();
;     G_DMA_A(0, G_A0); G_ISSUE_B(0); G_WRITE_B(G_B0);
;     __builtin_amdgcn_sched_barrier(0);
;     G_ISSUE_B(1);
;     __builtin_amdgcn_sched_barrier(0);
;     G_ENDTILE(8);
;     for (int ui = 0;; ++ui) {
; #pragma unroll
;         for (int m = 0; m < MF; ++m)
; #pragma unroll
;             for (int n = 0; n < 4; ++n) acc[m][n] = (f32x4){0.f, 0.f, 0.f, 0.f};
;         for (int t = 0; t < nt - 2; t += 2) {
;             G_TILE(G_A0, G_B0, true, G_B1, G_A1, t + 1, true, t + 2, (void)0);
;             G_ENDTILE(8);
;             G_TILE(G_A1, G_B1, true, G_B0, G_A0, t + 2, true, t + 3, (void)0);
;             G_ENDTILE(8);
;         }
	v_mfma_f32_16x16x32_bf16 v[92:95], v[160:163], v[190:193], v[92:95]
	ds_read_b128 v[168:171], v175 offset:45056
	v_mfma_f32_16x16x32_bf16 v[88:91], v[164:167], v[190:193], v[88:91]
	v_mfma_f32_16x16x32_bf16 v[84:87], v[182:185], v[190:193], v[84:87]
	v_mfma_f32_16x16x32_bf16 v[80:83], v[186:189], v[190:193], v[80:83]
	s_waitcnt lgkmcnt(2)
	v_mfma_f32_16x16x32_bf16 v[76:79], v[160:163], v[194:197], v[76:79]
	ds_read_b128 v[190:193], v175 offset:47104
	buffer_load_dwordx4 v[28:31], v173, s[8:11], s20 offen
	s_waitcnt vmcnt(11)
	v_cvt_pk_bf16_f32 v7, v6, v7
	v_cvt_pk_bf16_f32 v6, v4, v5
	v_mfma_f32_16x16x32_bf16 v[72:75], v[164:167], v[194:197], v[72:75]
	ds_write_b64 v174, v[6:7] offset:17408
	v_mfma_f32_16x16x32_bf16 v[68:71], v[182:185], v[194:197], v[68:71]
	v_mfma_f32_16x16x32_bf16 v[64:67], v[186:189], v[194:197], v[64:67]
	s_add_i32 s21, s1, 0xfffe0000
	s_waitcnt lgkmcnt(2)
	v_mfma_f32_16x16x32_bf16 v[60:63], v[160:163], v[168:171], v[60:63]
	ds_read_b128 v[194:197], v175 offset:33792
	v_mfma_f32_16x16x32_bf16 v[56:59], v[164:167], v[168:171], v[56:59]
	v_mfma_f32_16x16x32_bf16 v[52:55], v[182:185], v[168:171], v[52:55]
	v_mfma_f32_16x16x32_bf16 v[48:51], v[186:189], v[168:171], v[48:51]
	s_waitcnt lgkmcnt(2)
	v_mfma_f32_16x16x32_bf16 v[44:47], v[160:163], v[190:193], v[44:47]
	ds_read_b128 v[160:163], v175 offset:35840
	buffer_load_dwordx4 v[4:7], v173, s[8:11], s21 offen
	s_waitcnt vmcnt(11)
	v_cvt_pk_bf16_f32 v27, v26, v27
	v_cvt_pk_bf16_f32 v26, v24, v25
	v_mfma_f32_16x16x32_bf16 v[40:43], v[164:167], v[190:193], v[40:43]
	ds_read_b64_tr_b16 v[244:245], v178 offset:52224
	ds_read_b64_tr_b16 v[248:249], v178 offset:52256
	ds_read_b64_tr_b16 v[198:199], v178 offset:52288
	ds_read_b64_tr_b16 v[202:203], v178 offset:52320
	ds_read_b64_tr_b16 v[246:247], v179 offset:52224
	ds_read_b64_tr_b16 v[250:251], v179 offset:52256
	ds_read_b64_tr_b16 v[200:201], v179 offset:52288
	ds_read_b64_tr_b16 v[204:205], v179 offset:52320
	ds_write_b64 v174, v[26:27] offset:26112
	v_mfma_f32_16x16x32_bf16 v[36:39], v[182:185], v[190:193], v[36:39]
	v_mfma_f32_16x16x32_bf16 v[32:35], v[186:189], v[190:193], v[32:35]
	s_waitcnt lgkmcnt(4)
	v_mfma_f32_16x16x32_bf16 v[156:159], v[244:247], v[194:197], v[156:159]
	ds_read_b128 v[182:185], v175 offset:37888
	s_waitcnt lgkmcnt(4)
	v_mfma_f32_16x16x32_bf16 v[152:155], v[248:251], v[194:197], v[152:155]
	s_waitcnt lgkmcnt(3)
	v_mfma_f32_16x16x32_bf16 v[148:151], v[198:201], v[194:197], v[148:151]
	s_waitcnt lgkmcnt(2)
	v_mfma_f32_16x16x32_bf16 v[144:147], v[202:205], v[194:197], v[144:147]
	v_mfma_f32_16x16x32_bf16 v[140:143], v[244:247], v[160:163], v[140:143]
	ds_read_b128 v[186:189], v175 offset:39936
	buffer_load_dwordx4 v[24:27], v173, s[8:11], s1 offen
	s_waitcnt vmcnt(11)
	v_cvt_pk_bf16_f32 v23, v22, v23
	v_cvt_pk_bf16_f32 v22, v20, v21
	v_mfma_f32_16x16x32_bf16 v[136:139], v[248:251], v[160:163], v[136:139]
	ds_write_b64 v174, v[22:23] offset:256
	v_mfma_f32_16x16x32_bf16 v[132:135], v[198:201], v[160:163], v[132:135]
	v_mfma_f32_16x16x32_bf16 v[128:131], v[202:205], v[160:163], v[128:131]
	s_waitcnt lgkmcnt(2)
	v_mfma_f32_16x16x32_bf16 v[124:127], v[244:247], v[182:185], v[124:127]
	ds_read_b128 v[160:163], v175 offset:41984
	v_mfma_f32_16x16x32_bf16 v[120:123], v[248:251], v[182:185], v[120:123]
	v_mfma_f32_16x16x32_bf16 v[116:119], v[198:201], v[182:185], v[116:119]
	v_mfma_f32_16x16x32_bf16 v[112:115], v[202:205], v[182:185], v[112:115]
	s_waitcnt lgkmcnt(2)
	v_mfma_f32_16x16x32_bf16 v[108:111], v[244:247], v[186:189], v[108:111]
	ds_read_b128 v[182:185], v175 offset:44032
	buffer_load_dwordx4 v[20:23], v173, s[12:15], s5 offen
	s_waitcnt vmcnt(11)
	v_cvt_pk_bf16_f32 v11, v10, v11
	v_cvt_pk_bf16_f32 v10, v8, v9
	v_mfma_f32_16x16x32_bf16 v[104:107], v[248:251], v[186:189], v[104:107]
	ds_write_b64 v174, v[10:11] offset:8960
	v_mfma_f32_16x16x32_bf16 v[100:103], v[198:201], v[186:189], v[100:103]
	v_mfma_f32_16x16x32_bf16 v[96:99], v[202:205], v[186:189], v[96:99]
	s_waitcnt lgkmcnt(2)
	v_mfma_f32_16x16x32_bf16 v[92:95], v[244:247], v[160:163], v[92:95]
	ds_read_b128 v[186:189], v175 offset:46080
	v_mfma_f32_16x16x32_bf16 v[88:91], v[248:251], v[160:163], v[88:91]
	v_mfma_f32_16x16x32_bf16 v[84:87], v[198:201], v[160:163], v[84:87]
	v_mfma_f32_16x16x32_bf16 v[80:83], v[202:205], v[160:163], v[80:83]
	s_waitcnt lgkmcnt(2)
	v_mfma_f32_16x16x32_bf16 v[76:79], v[244:247], v[182:185], v[76:79]
	ds_read_b128 v[252:255], v175 offset:48128
	buffer_load_dwordx4 v[8:11], v173, s[12:15], s20 offen
	s_waitcnt vmcnt(11)
	v_cvt_pk_bf16_f32 v3, v2, v3
	v_cvt_pk_bf16_f32 v2, v0, v1
	v_mfma_f32_16x16x32_bf16 v[72:75], v[248:251], v[182:185], v[72:75]
	ds_write_b64 v174, v[2:3] offset:17664
	v_mfma_f32_16x16x32_bf16 v[68:71], v[198:201], v[182:185], v[68:71]
	v_mfma_f32_16x16x32_bf16 v[64:67], v[202:205], v[182:185], v[64:67]
	s_waitcnt lgkmcnt(2)
	v_mfma_f32_16x16x32_bf16 v[60:63], v[244:247], v[186:189], v[60:63]
	v_mfma_f32_16x16x32_bf16 v[56:59], v[248:251], v[186:189], v[56:59]
	v_mfma_f32_16x16x32_bf16 v[52:55], v[198:201], v[186:189], v[52:55]
	v_mfma_f32_16x16x32_bf16 v[48:51], v[202:205], v[186:189], v[48:51]
	s_waitcnt lgkmcnt(1)
	buffer_load_dwordx4 v[0:3], v173, s[12:15], s21 offen
	s_waitcnt vmcnt(11)
	v_cvt_pk_bf16_f32 v19, v18, v19
	v_cvt_pk_bf16_f32 v18, v16, v17
	ds_write_b64 v174, v[18:19] offset:26368
	buffer_load_dwordx4 v[16:19], v173, s[12:15], s1 offen
	s_waitcnt vmcnt(8)
	s_waitcnt lgkmcnt(0)
	s_barrier
	s_add_i32 s0, s0, 2
	s_add_i32 s1, s1, 0x100000
	s_addk_i32 s4, 0x100
	s_cmp_ge_i32 s0, s60
	s_cbranch_scc0 .LBB0_1038
	v_mfma_f32_16x16x32_bf16 v[44:47], v[244:247], v[252:255], v[44:47]
	v_mfma_f32_16x16x32_bf16 v[40:43], v[248:251], v[252:255], v[40:43]
	v_mfma_f32_16x16x32_bf16 v[36:39], v[198:201], v[252:255], v[36:39]
	v_mfma_f32_16x16x32_bf16 v[32:35], v[202:205], v[252:255], v[32:35]
	s_branch .LBB0_1040
